# router K-loop: software-pipelined (fragments/conversion of chunk c+1 under the MFMAs of chunk c), 4-buffer ring, per-workgroup rotated K order
# speedup vs baseline: 1.0767x; 1.0012x over previous
; __device__ __forceinline__ void p5_router(Frame& F) {
;     ...
;     for (int tile = F.bid; tile < M / 64; tile += F.G) {
;         const int m0 = tile * 64;
;         { const int tg = wave & 1, kq = wave >> 1, fr = lane & 15, fq = lane >> 4;
;           f32x4 acc[2][5];
; #pragma unroll
;           for (int a = 0; a < 2; ++a)
; #pragma unroll
;               for (int n = 0; n < 5; ++n) acc[a][n] = (f32x4){0.f, 0.f, 0.f, 0.f};
;           float ss[2] = {0.f, 0.f};
;           const size_t roff = (size_t)(m0 + 32 * tg + fr) * D + kq * 1024 + 8 * fq;
;           const bf16_t* h0 = H + roff; const bf16_t* h1 = h0 + (size_t)16 * D;
;           const float* gp = F.g_ffn + kq * 1024 + 8 * fq;
;           const bf16_t* bh = RBH + (size_t)fr * D + kq * 1024 + 8 * fq; const bf16_t* bl = RBL + (size_t)fr * D + kq * 1024 + 8 * fq;
;           RtLoad La, Lb; rt_load(La, h0, h1, gp, 0);
.LBB0_606:
	s_lshl_b32 s10, s64, 6
	v_readlane_b32 s84, v254, 23
	v_readlane_b32 s86, v254, 31
	v_readlane_b32 s87, v254, 32
	v_readlane_b32 s66, v254, 9
	v_readlane_b32 s67, v254, 10
	s_and_b32 s88, s84, 3
	s_lshr_b32 s89, s84, 2
	s_mov_b32 s94, 0xe00000
	s_mov_b32 s95, 0xea0000
	s_lshl_b32 s91, s64, 19
	s_add_i32 s91, s91, 0x29e00000
	v_and_b32_e32 v217, 7, v131
	v_lshrrev_b32_e32 v218, 1, v130
	v_lshlrev_b32_e32 v219, 13, v130
	s_add_i32 s24, s84, 0
	s_lshl_b32 s98, s24, 10
	s_sub_i32 s85, s24, 10
	s_sub_i32 s33, s24, 20
	s_cmp_lt_u32 s24, 20
	s_cselect_b32 s33, s85, s33
	s_cselect_b32 s85, s95, s91
	s_cmp_lt_u32 s24, 10
	s_cselect_b32 s33, s24, s33
	s_cselect_b32 s85, s94, s85
	s_and_b32 s24, s33, 1
	s_lshl_b32 s24, s24, 2
	s_lshl_b32 s33, s33, 16
	s_add_i32 s85, s85, s33
	v_add_u32_e32 v220, s24, v218
	v_xor_b32_e32 v220, v220, v217
	v_lshl_add_u32 v220, v220, 4, v219
	v_add_u32_e32 v208, s85, v220
	s_add_i32 s24, s84, 8
	s_lshl_b32 s99, s24, 10
	s_sub_i32 s85, s24, 10
	s_sub_i32 s33, s24, 20
	s_cmp_lt_u32 s24, 20
	s_cselect_b32 s33, s85, s33
	s_cselect_b32 s85, s95, s91
	s_cmp_lt_u32 s24, 10
	s_cselect_b32 s33, s24, s33
	s_cselect_b32 s85, s94, s85
	s_and_b32 s24, s33, 1
	s_lshl_b32 s24, s24, 2
	s_lshl_b32 s33, s33, 16
	s_add_i32 s85, s85, s33
	v_add_u32_e32 v220, s24, v218
	v_xor_b32_e32 v220, v220, v217
	v_lshl_add_u32 v220, v220, 4, v219
	v_add_u32_e32 v209, s85, v220
	s_add_i32 s24, s84, 16
	s_lshl_b32 s100, s24, 10
	s_sub_i32 s85, s24, 10
	s_sub_i32 s33, s24, 20
	s_cmp_lt_u32 s24, 20
	s_cselect_b32 s33, s85, s33
	s_cselect_b32 s85, s95, s91
	s_cmp_lt_u32 s24, 10
	s_cselect_b32 s33, s24, s33
	s_cselect_b32 s85, s94, s85
	s_and_b32 s24, s33, 1
	s_lshl_b32 s24, s24, 2
	s_lshl_b32 s33, s33, 16
	s_add_i32 s85, s85, s33
	v_add_u32_e32 v220, s24, v218
	v_xor_b32_e32 v220, v220, v217
	v_lshl_add_u32 v220, v220, 4, v219
	v_add_u32_e32 v210, s85, v220
	s_add_i32 s24, s84, 24
	s_lshl_b32 s101, s24, 10
	s_sub_i32 s85, s24, 10
	s_sub_i32 s33, s24, 20
	s_cmp_lt_u32 s24, 20
	s_cselect_b32 s33, s85, s33
	s_cselect_b32 s85, s95, s91
	s_cmp_lt_u32 s24, 10
	s_cselect_b32 s33, s24, s33
	s_cselect_b32 s85, s94, s85
	s_and_b32 s24, s33, 1
	s_lshl_b32 s24, s24, 2
	s_lshl_b32 s33, s33, 16
	s_add_i32 s85, s85, s33
	v_add_u32_e32 v220, s24, v218
	v_xor_b32_e32 v220, v220, v217
	v_lshl_add_u32 v220, v220, 4, v219
	v_add_u32_e32 v211, s85, v220
	s_lshl_b32 s24, s89, 2
	v_add_u32_e32 v217, s24, v171
	v_bfe_u32 v218, v131, 1, 3
	v_xor_b32_e32 v217, v217, v218
	v_lshlrev_b32_e32 v217, 4, v217
	v_lshl_add_u32 v212, v170, 7, v217
	s_lshl_b32 s24, s88, 11
	s_add_i32 s24, s24, 20480
	v_add_u32_e32 v213, s24, v212
	s_lshr_b32 s39, s64, 2
	s_and_b32 s39, s39, 62
	s_lshl_b32 s39, s39, 7
	s_sub_u32 s39, s39, 0x80
	s_lshl_b32 s24, s89, 7
	v_lshl_add_u32 v216, v171, 5, s24
	s_cmp_gt_u32 s84, 3
	s_cbranch_scc1 .Lrt_pro3
	s_add_i32 s39, s39, 0x80
	s_and_b32 s39, s39, 0x1fff
	s_add_u32 s40, s86, s39
	s_addc_u32 s41, s87, 0
	s_lshl_b32 s33, s39, 1
	s_add_u32 s44, s66, s33
	s_addc_u32 s45, s67, 0
	global_load_dwordx4 v[42:45], v216, s[44:45]
	global_load_dwordx4 v[46:49], v216, s[44:45] offset:16
	s_mov_b32 m0, s98
	s_nop 0
	global_load_lds_dwordx4 v208, s[40:41]
	s_mov_b32 m0, s99
	s_nop 0
	global_load_lds_dwordx4 v209, s[40:41]
	s_mov_b32 m0, s100
	s_nop 0
	global_load_lds_dwordx4 v210, s[40:41]
	s_mov_b32 m0, s101
	s_nop 0
	global_load_lds_dwordx4 v211, s[40:41]
	s_add_i32 s39, s39, 0x80
	s_and_b32 s39, s39, 0x1fff
	s_add_u32 s40, s86, s39
	s_addc_u32 s41, s87, 0
	s_lshl_b32 s33, s39, 1
	s_add_u32 s44, s66, s33
	s_addc_u32 s45, s67, 0
	global_load_dwordx4 v[50:53], v216, s[44:45]
	global_load_dwordx4 v[54:57], v216, s[44:45] offset:16
	s_add_i32 m0, s98, 28672
	s_nop 0
	global_load_lds_dwordx4 v208, s[40:41]
	s_add_i32 m0, s99, 28672
	s_nop 0
	global_load_lds_dwordx4 v209, s[40:41]
	s_add_i32 m0, s100, 28672
	s_nop 0
	global_load_lds_dwordx4 v210, s[40:41]
	s_add_i32 m0, s101, 28672
	s_nop 0
	global_load_lds_dwordx4 v211, s[40:41]
	s_add_i32 s39, s39, 0x80
	s_and_b32 s39, s39, 0x1fff
	s_add_u32 s40, s86, s39
	s_addc_u32 s41, s87, 0
	s_lshl_b32 s33, s39, 1
	s_add_u32 s44, s66, s33
	s_addc_u32 s45, s67, 0
	global_load_dwordx4 v[2:5], v216, s[44:45]
	global_load_dwordx4 v[6:9], v216, s[44:45] offset:16
	s_add_i32 m0, s98, 57344
	s_nop 0
	global_load_lds_dwordx4 v208, s[40:41]
	s_add_i32 m0, s99, 57344
	s_nop 0
	global_load_lds_dwordx4 v209, s[40:41]
	s_add_i32 m0, s100, 57344
	s_nop 0
	global_load_lds_dwordx4 v210, s[40:41]
	s_add_i32 m0, s101, 57344
	s_nop 0
	global_load_lds_dwordx4 v211, s[40:41]
	s_waitcnt vmcnt(12)
	s_branch .Lrt_prodone
.Lrt_pro3:
	s_add_i32 s39, s39, 0x80
	s_and_b32 s39, s39, 0x1fff
	s_add_u32 s40, s86, s39
	s_addc_u32 s41, s87, 0
	s_lshl_b32 s33, s39, 1
	s_add_u32 s44, s66, s33
	s_addc_u32 s45, s67, 0
	global_load_dwordx4 v[42:45], v216, s[44:45]
	global_load_dwordx4 v[46:49], v216, s[44:45] offset:16
	s_mov_b32 m0, s98
	s_nop 0
	global_load_lds_dwordx4 v208, s[40:41]
	s_mov_b32 m0, s99
	s_nop 0
	global_load_lds_dwordx4 v209, s[40:41]
	s_mov_b32 m0, s100
	s_nop 0
	global_load_lds_dwordx4 v210, s[40:41]
	s_add_i32 s39, s39, 0x80
	s_and_b32 s39, s39, 0x1fff
	s_add_u32 s40, s86, s39
	s_addc_u32 s41, s87, 0
	s_lshl_b32 s33, s39, 1
	s_add_u32 s44, s66, s33
	s_addc_u32 s45, s67, 0
	global_load_dwordx4 v[50:53], v216, s[44:45]
	global_load_dwordx4 v[54:57], v216, s[44:45] offset:16
	s_add_i32 m0, s98, 28672
	s_nop 0
	global_load_lds_dwordx4 v208, s[40:41]
	s_add_i32 m0, s99, 28672
	s_nop 0
	global_load_lds_dwordx4 v209, s[40:41]
	s_add_i32 m0, s100, 28672
	s_nop 0
	global_load_lds_dwordx4 v210, s[40:41]
	s_add_i32 s39, s39, 0x80
	s_and_b32 s39, s39, 0x1fff
	s_add_u32 s40, s86, s39
	s_addc_u32 s41, s87, 0
	s_lshl_b32 s33, s39, 1
	s_add_u32 s44, s66, s33
	s_addc_u32 s45, s67, 0
	global_load_dwordx4 v[2:5], v216, s[44:45]
	global_load_dwordx4 v[6:9], v216, s[44:45] offset:16
	s_add_i32 m0, s98, 57344
	s_nop 0
	global_load_lds_dwordx4 v208, s[40:41]
	s_add_i32 m0, s99, 57344
	s_nop 0
	global_load_lds_dwordx4 v209, s[40:41]
	s_add_i32 m0, s100, 57344
	s_nop 0
	global_load_lds_dwordx4 v210, s[40:41]
	s_waitcnt vmcnt(10)
; __device__ __forceinline__ unsigned f2bf(float f) { unsigned u = __builtin_bit_cast(unsigned, f); return (u + 0x7fffu + ((u >> 16) & 1u)) >> 16; }
; __device__ __forceinline__ void rt_step(const RtLoad& L, const bf16_t* bh, const bf16_t* bl, f32x4 (&acc)[2][5], float (&ss)[2], int ko) {
;     RtW W;
; #pragma unroll
;     for (int n = 0; n < 5; ++n) { W.wh[n] = *(const bf16x8*)(bh + (size_t)n * 16 * D + ko); W.wl[n] = *(const bf16x8*)(bl + (size_t)n * 16 * D + ko); }
;     bf16x8 ahi[2], alo[2];
; #pragma unroll
;     for (int mi = 0; mi < 2; ++mi) { const u32x4 xw = L.x[mi]; const f32x4 xa = (f32x4){bflo(xw.x), bfhi(xw.x), bflo(xw.y), bfhi(xw.y)}, xb = (f32x4){bflo(xw.z), bfhi(xw.z), bflo(xw.w), bfhi(xw.w)};
;         ss[mi] += (xa.x * xa.x + xa.y * xa.y) + (xa.z * xa.z + xa.w * xa.w) + (xb.x * xb.x + xb.y * xb.y) + (xb.z * xb.z + xb.w * xb.w);
;         const float u[8] = {xa.x * L.g[0].x, xa.y * L.g[0].y, xa.z * L.g[0].z, xa.w * L.g[0].w, xb.x * L.g[1].x, xb.y * L.g[1].y, xb.z * L.g[1].z, xb.w * L.g[1].w};
;         unsigned hb[8]; float lo[8];
; #pragma unroll
;         for (int j = 0; j < 8; ++j) { hb[j] = f2bf(u[j]); lo[j] = u[j] - __builtin_bit_cast(float, hb[j] << 16); }
;         const u32x4 hw = (u32x4){hb[0] | (hb[1] << 16), hb[2] | (hb[3] << 16), hb[4] | (hb[5] << 16), hb[6] | (hb[7] << 16)};
;         const u32x4 lw = (u32x4){pk2(lo[0], lo[1]), pk2(lo[2], lo[3]), pk2(lo[4], lo[5]), pk2(lo[6], lo[7])};
;         ahi[mi] = __builtin_bit_cast(bf16x8, hw); alo[mi] = __builtin_bit_cast(bf16x8, lw); }
; #pragma unroll
;     for (int n = 0; n < 5; ++n)
; #pragma unroll
;         for (int mi = 0; mi < 2; ++mi) { acc[mi][n] = __builtin_amdgcn_mfma_f32_16x16x32_bf16(ahi[mi], W.wh[n], acc[mi][n], 0, 0, 0);
;             acc[mi][n] = __builtin_amdgcn_mfma_f32_16x16x32_bf16(alo[mi], W.wh[n], acc[mi][n], 0, 0, 0);
;             acc[mi][n] = __builtin_amdgcn_mfma_f32_16x16x32_bf16(ahi[mi], W.wl[n], acc[mi][n], 0, 0, 0); }
; }
; __device__ __forceinline__ void p5_router(Frame& F) {
;     ...
; #pragma unroll 1
;           for (int ks = 0; ks < 32; ks += 2) {
;               rt_load(Lb, h0, h1, gp, (ks + 1) * 32); rt_step(La, bh, bl, acc, ss, ks * 32);
;               if (ks + 2 < 32) rt_load(La, h0, h1, gp, (ks + 2) * 32);
;               rt_step(Lb, bh, bl, acc, ss, (ks + 1) * 32); }
.Lrt_prodone:
	v_mov_b32_e32 v18, 0
	v_mov_b32_e32 v19, 0
	v_mov_b32_e32 v20, 0
	v_mov_b32_e32 v21, 0
	v_mov_b32_e32 v22, 0
	v_mov_b32_e32 v23, 0
	v_mov_b32_e32 v24, 0
	v_mov_b32_e32 v25, 0
	v_mov_b32_e32 v26, 0
	v_mov_b32_e32 v27, 0
	v_mov_b32_e32 v28, 0
	v_mov_b32_e32 v29, 0
	v_mov_b32_e32 v30, 0
	v_mov_b32_e32 v31, 0
	v_mov_b32_e32 v32, 0
	v_mov_b32_e32 v33, 0
	v_mov_b32_e32 v34, 0
	v_mov_b32_e32 v35, 0
	v_mov_b32_e32 v36, 0
	v_mov_b32_e32 v37, 0
	v_mov_b32_e32 v224, 0
	s_mov_b32 s94, 86016
	s_mov_b32 s95, 0
	s_mov_b32 s91, 28672
	s_mov_b32 s25, 57344
	s_barrier
	s_cmp_gt_u32 s84, 3
	s_cbranch_scc1 .Lrt_path3
	s_add_i32 s39, s39, 0x80
	s_and_b32 s39, s39, 0x1fff
	s_add_u32 s40, s86, s39
	s_addc_u32 s41, s87, 0
	s_lshl_b32 s33, s39, 1
	s_add_u32 s44, s66, s33
	s_addc_u32 s45, s67, 0
	global_load_dwordx4 v[10:13], v216, s[44:45]
	global_load_dwordx4 v[14:17], v216, s[44:45] offset:16
	s_add_i32 m0, s94, s98
	s_nop 0
	global_load_lds_dwordx4 v208, s[40:41]
	s_add_i32 m0, s94, s99
	s_nop 0
	global_load_lds_dwordx4 v209, s[40:41]
	s_add_i32 m0, s94, s100
	s_nop 0
	global_load_lds_dwordx4 v210, s[40:41]
	s_add_i32 m0, s94, s101
	s_nop 0
	global_load_lds_dwordx4 v211, s[40:41]
	v_add_u32_e32 v214, s95, v212
	v_add_u32_e32 v215, s95, v213
	ds_read_b128 v[38:41], v215
	ds_read_b128 v[58:61], v214 offset:0
	ds_read_b128 v[62:65], v214 offset:2048
	ds_read_b128 v[66:69], v214 offset:4096
	ds_read_b128 v[70:73], v214 offset:6144
	ds_read_b128 v[74:77], v214 offset:8192
	ds_read_b128 v[100:103], v214 offset:10240
	ds_read_b128 v[104:107], v214 offset:12288
	ds_read_b128 v[108:111], v214 offset:14336
	ds_read_b128 v[112:115], v214 offset:16384
	ds_read_b128 v[116:119], v214 offset:18432
	s_waitcnt lgkmcnt(10)
	v_lshlrev_b32_e32 v172, 16, v38
	v_and_b32_e32 v173, 0xffff0000, v38
	v_lshlrev_b32_e32 v174, 16, v39
	v_and_b32_e32 v175, 0xffff0000, v39
	v_lshlrev_b32_e32 v176, 16, v40
	v_and_b32_e32 v177, 0xffff0000, v40
	v_lshlrev_b32_e32 v178, 16, v41
	v_and_b32_e32 v179, 0xffff0000, v41
	v_mul_f32_e32 v180, v42, v172
	v_mul_f32_e32 v181, v43, v173
	v_mul_f32_e32 v182, v44, v174
	v_mul_f32_e32 v183, v45, v175
	v_mul_f32_e32 v184, v46, v176
	v_mul_f32_e32 v185, v47, v177
	v_mul_f32_e32 v186, v48, v178
	v_mul_f32_e32 v187, v49, v179
	v_cvt_pk_bf16_f32 v200, v180, v181
	v_cvt_pk_bf16_f32 v201, v182, v183
	v_cvt_pk_bf16_f32 v202, v184, v185
	v_cvt_pk_bf16_f32 v203, v186, v187
	v_mul_f32_e32 v196, v172, v172
	v_mul_f32_e32 v197, v174, v174
	v_mul_f32_e32 v198, v176, v176
	v_mul_f32_e32 v199, v178, v178
	v_fma_f32 v196, v173, v173, v196
	v_fma_f32 v197, v175, v175, v197
	v_fma_f32 v198, v177, v177, v198
	v_fma_f32 v199, v179, v179, v199
	v_lshlrev_b32_e32 v188, 16, v200
	v_and_b32_e32 v189, 0xffff0000, v200
	v_lshlrev_b32_e32 v190, 16, v201
	v_and_b32_e32 v191, 0xffff0000, v201
	v_lshlrev_b32_e32 v192, 16, v202
	v_and_b32_e32 v193, 0xffff0000, v202
	v_lshlrev_b32_e32 v194, 16, v203
	v_and_b32_e32 v195, 0xffff0000, v203
	v_fma_f32 v180, v42, v172, -v188
	v_fma_f32 v181, v43, v173, -v189
	v_fma_f32 v182, v44, v174, -v190
	v_fma_f32 v183, v45, v175, -v191
	v_fma_f32 v184, v46, v176, -v192
	v_fma_f32 v185, v47, v177, -v193
	v_fma_f32 v186, v48, v178, -v194
	v_fma_f32 v187, v49, v179, -v195
	v_add_f32_e32 v196, v196, v197
	v_add_f32_e32 v196, v196, v198
	v_add_f32_e32 v196, v196, v199
	v_add_f32_e32 v224, v224, v196
	v_cvt_pk_bf16_f32 v204, v180, v181
	v_cvt_pk_bf16_f32 v205, v182, v183
	v_cvt_pk_bf16_f32 v206, v184, v185
	v_cvt_pk_bf16_f32 v207, v186, v187
	s_waitcnt vmcnt(12)
	s_waitcnt lgkmcnt(0)
	s_barrier
	s_mov_b32 s33, s94
	s_mov_b32 s94, s95
	s_mov_b32 s95, s91
	s_mov_b32 s91, s25
	s_mov_b32 s25, s33
	s_add_i32 s39, s39, 0x80
	s_and_b32 s39, s39, 0x1fff
	s_add_u32 s40, s86, s39
	s_addc_u32 s41, s87, 0
	s_lshl_b32 s33, s39, 1
	s_add_u32 s44, s66, s33
	s_addc_u32 s45, s67, 0
	global_load_dwordx4 v[42:45], v216, s[44:45]
	global_load_dwordx4 v[46:49], v216, s[44:45] offset:16
	s_add_i32 m0, s94, s98
	s_nop 0
	global_load_lds_dwordx4 v208, s[40:41]
	s_add_i32 m0, s94, s99
	s_nop 0
	global_load_lds_dwordx4 v209, s[40:41]
	s_add_i32 m0, s94, s100
	s_nop 0
	global_load_lds_dwordx4 v210, s[40:41]
	s_add_i32 m0, s94, s101
	s_nop 0
	global_load_lds_dwordx4 v211, s[40:41]
	v_add_u32_e32 v214, s95, v212
	v_add_u32_e32 v215, s95, v213
	ds_read_b128 v[226:229], v215
	ds_read_b128 v[230:233], v214 offset:0
	ds_read_b128 v[234:237], v214 offset:2048
	ds_read_b128 v[238:241], v214 offset:4096
	ds_read_b128 v[242:245], v214 offset:6144
	ds_read_b128 v[246:249], v214 offset:8192
	ds_read_b128 v[120:123], v214 offset:10240
	ds_read_b128 v[124:127], v214 offset:12288
	ds_read_b128 v[132:135], v214 offset:14336
	ds_read_b128 v[136:139], v214 offset:16384
	ds_read_b128 v[140:143], v214 offset:18432
	v_mfma_f32_16x16x32_bf16 v[18:21], v[200:203], v[58:61], v[18:21]
	v_mfma_f32_16x16x32_bf16 v[22:25], v[200:203], v[62:65], v[22:25]
	s_waitcnt lgkmcnt(10)
; __device__ __forceinline__ unsigned f2bf(float f) { unsigned u = __builtin_bit_cast(unsigned, f); return (u + 0x7fffu + ((u >> 16) & 1u)) >> 16; }
; __device__ __forceinline__ void rt_step(const RtLoad& L, const bf16_t* bh, const bf16_t* bl, f32x4 (&acc)[2][5], float (&ss)[2], int ko) {
;     RtW W;
; #pragma unroll
;     for (int n = 0; n < 5; ++n) { W.wh[n] = *(const bf16x8*)(bh + (size_t)n * 16 * D + ko); W.wl[n] = *(const bf16x8*)(bl + (size_t)n * 16 * D + ko); }
;     bf16x8 ahi[2], alo[2];
; #pragma unroll
;     for (int mi = 0; mi < 2; ++mi) { const u32x4 xw = L.x[mi]; const f32x4 xa = (f32x4){bflo(xw.x), bfhi(xw.x), bflo(xw.y), bfhi(xw.y)}, xb = (f32x4){bflo(xw.z), bfhi(xw.z), bflo(xw.w), bfhi(xw.w)};
;         ss[mi] += (xa.x * xa.x + xa.y * xa.y) + (xa.z * xa.z + xa.w * xa.w) + (xb.x * xb.x + xb.y * xb.y) + (xb.z * xb.z + xb.w * xb.w);
;         const float u[8] = {xa.x * L.g[0].x, xa.y * L.g[0].y, xa.z * L.g[0].z, xa.w * L.g[0].w, xb.x * L.g[1].x, xb.y * L.g[1].y, xb.z * L.g[1].z, xb.w * L.g[1].w};
;         unsigned hb[8]; float lo[8];
; #pragma unroll
;         for (int j = 0; j < 8; ++j) { hb[j] = f2bf(u[j]); lo[j] = u[j] - __builtin_bit_cast(float, hb[j] << 16); }
;         const u32x4 hw = (u32x4){hb[0] | (hb[1] << 16), hb[2] | (hb[3] << 16), hb[4] | (hb[5] << 16), hb[6] | (hb[7] << 16)};
;         const u32x4 lw = (u32x4){pk2(lo[0], lo[1]), pk2(lo[2], lo[3]), pk2(lo[4], lo[5]), pk2(lo[6], lo[7])};
;         ahi[mi] = __builtin_bit_cast(bf16x8, hw); alo[mi] = __builtin_bit_cast(bf16x8, lw); }
; #pragma unroll
;     for (int n = 0; n < 5; ++n)
; #pragma unroll
;         for (int mi = 0; mi < 2; ++mi) { acc[mi][n] = __builtin_amdgcn_mfma_f32_16x16x32_bf16(ahi[mi], W.wh[n], acc[mi][n], 0, 0, 0);
;             acc[mi][n] = __builtin_amdgcn_mfma_f32_16x16x32_bf16(alo[mi], W.wh[n], acc[mi][n], 0, 0, 0);
;             acc[mi][n] = __builtin_amdgcn_mfma_f32_16x16x32_bf16(ahi[mi], W.wl[n], acc[mi][n], 0, 0, 0); }
; }
; __device__ __forceinline__ void p5_router(Frame& F) {
;     ...
; #pragma unroll 1
;           for (int ks = 0; ks < 32; ks += 2) {
;               rt_load(Lb, h0, h1, gp, (ks + 1) * 32); rt_step(La, bh, bl, acc, ss, ks * 32);
;               if (ks + 2 < 32) rt_load(La, h0, h1, gp, (ks + 2) * 32);
;               rt_step(Lb, bh, bl, acc, ss, (ks + 1) * 32); }
	v_lshlrev_b32_e32 v172, 16, v226
	v_and_b32_e32 v173, 0xffff0000, v226
	v_lshlrev_b32_e32 v174, 16, v227
	v_and_b32_e32 v175, 0xffff0000, v227
	v_mfma_f32_16x16x32_bf16 v[26:29], v[200:203], v[66:69], v[26:29]
	v_lshlrev_b32_e32 v176, 16, v228
	v_and_b32_e32 v177, 0xffff0000, v228
	v_lshlrev_b32_e32 v178, 16, v229
	v_and_b32_e32 v179, 0xffff0000, v229
	v_mfma_f32_16x16x32_bf16 v[30:33], v[200:203], v[70:73], v[30:33]
	v_mul_f32_e32 v180, v50, v172
	v_mul_f32_e32 v181, v51, v173
	v_mul_f32_e32 v182, v52, v174
	v_mul_f32_e32 v183, v53, v175
	v_mfma_f32_16x16x32_bf16 v[34:37], v[200:203], v[74:77], v[34:37]
	v_mul_f32_e32 v184, v54, v176
	v_mul_f32_e32 v185, v55, v177
	v_mul_f32_e32 v186, v56, v178
	v_mul_f32_e32 v187, v57, v179
	v_mfma_f32_16x16x32_bf16 v[18:21], v[204:207], v[58:61], v[18:21]
	v_cvt_pk_bf16_f32 v158, v180, v181
	v_cvt_pk_bf16_f32 v159, v182, v183
	v_cvt_pk_bf16_f32 v160, v184, v185
	v_cvt_pk_bf16_f32 v161, v186, v187
	v_mfma_f32_16x16x32_bf16 v[22:25], v[204:207], v[62:65], v[22:25]
	v_mul_f32_e32 v196, v172, v172
	v_mul_f32_e32 v197, v174, v174
	v_mul_f32_e32 v198, v176, v176
	v_mul_f32_e32 v199, v178, v178
	v_mfma_f32_16x16x32_bf16 v[26:29], v[204:207], v[66:69], v[26:29]
	v_fma_f32 v196, v173, v173, v196
	v_fma_f32 v197, v175, v175, v197
	v_fma_f32 v198, v177, v177, v198
	v_fma_f32 v199, v179, v179, v199
	v_mfma_f32_16x16x32_bf16 v[30:33], v[204:207], v[70:73], v[30:33]
	v_lshlrev_b32_e32 v188, 16, v158
	v_and_b32_e32 v189, 0xffff0000, v158
	v_lshlrev_b32_e32 v190, 16, v159
	v_and_b32_e32 v191, 0xffff0000, v159
	v_mfma_f32_16x16x32_bf16 v[34:37], v[204:207], v[74:77], v[34:37]
	v_lshlrev_b32_e32 v192, 16, v160
	v_and_b32_e32 v193, 0xffff0000, v160
	v_lshlrev_b32_e32 v194, 16, v161
	v_and_b32_e32 v195, 0xffff0000, v161
	v_mfma_f32_16x16x32_bf16 v[18:21], v[200:203], v[100:103], v[18:21]
	v_fma_f32 v180, v50, v172, -v188
	v_fma_f32 v181, v51, v173, -v189
	v_fma_f32 v182, v52, v174, -v190
	v_fma_f32 v183, v53, v175, -v191
	v_mfma_f32_16x16x32_bf16 v[22:25], v[200:203], v[104:107], v[22:25]
	v_fma_f32 v184, v54, v176, -v192
	v_fma_f32 v185, v55, v177, -v193
	v_fma_f32 v186, v56, v178, -v194
	v_fma_f32 v187, v57, v179, -v195
	v_mfma_f32_16x16x32_bf16 v[26:29], v[200:203], v[108:111], v[26:29]
	v_add_f32_e32 v196, v196, v197
	v_add_f32_e32 v196, v196, v198
	v_add_f32_e32 v196, v196, v199
	v_add_f32_e32 v224, v224, v196
	v_mfma_f32_16x16x32_bf16 v[30:33], v[200:203], v[112:115], v[30:33]
	v_cvt_pk_bf16_f32 v162, v180, v181
	v_cvt_pk_bf16_f32 v163, v182, v183
	v_cvt_pk_bf16_f32 v164, v184, v185
	v_cvt_pk_bf16_f32 v165, v186, v187
	v_mfma_f32_16x16x32_bf16 v[34:37], v[200:203], v[116:119], v[34:37]
	s_waitcnt vmcnt(12)
	s_waitcnt lgkmcnt(0)
	s_barrier
	s_mov_b32 s33, s94
	s_mov_b32 s94, s95
	s_mov_b32 s95, s91
	s_mov_b32 s91, s25
	s_mov_b32 s25, s33
	s_add_i32 s39, s39, 0x80
	s_and_b32 s39, s39, 0x1fff
	s_add_u32 s40, s86, s39
	s_addc_u32 s41, s87, 0
	s_lshl_b32 s33, s39, 1
	s_add_u32 s44, s66, s33
	s_addc_u32 s45, s67, 0
	global_load_dwordx4 v[50:53], v216, s[44:45]
	global_load_dwordx4 v[54:57], v216, s[44:45] offset:16
	s_add_i32 m0, s94, s98
	s_nop 0
	global_load_lds_dwordx4 v208, s[40:41]
	s_add_i32 m0, s94, s99
	s_nop 0
	global_load_lds_dwordx4 v209, s[40:41]
	s_add_i32 m0, s94, s100
	s_nop 0
	global_load_lds_dwordx4 v210, s[40:41]
	s_add_i32 m0, s94, s101
	s_nop 0
	global_load_lds_dwordx4 v211, s[40:41]
	v_add_u32_e32 v214, s95, v212
	v_add_u32_e32 v215, s95, v213
	ds_read_b128 v[38:41], v215
	ds_read_b128 v[58:61], v214 offset:0
	ds_read_b128 v[62:65], v214 offset:2048
	ds_read_b128 v[66:69], v214 offset:4096
	ds_read_b128 v[70:73], v214 offset:6144
	ds_read_b128 v[74:77], v214 offset:8192
	ds_read_b128 v[100:103], v214 offset:10240
	ds_read_b128 v[104:107], v214 offset:12288
	ds_read_b128 v[108:111], v214 offset:14336
	ds_read_b128 v[112:115], v214 offset:16384
	ds_read_b128 v[116:119], v214 offset:18432
	v_mfma_f32_16x16x32_bf16 v[18:21], v[158:161], v[230:233], v[18:21]
	v_mfma_f32_16x16x32_bf16 v[22:25], v[158:161], v[234:237], v[22:25]
	s_waitcnt lgkmcnt(10)
	v_lshlrev_b32_e32 v172, 16, v38
	v_and_b32_e32 v173, 0xffff0000, v38
	v_lshlrev_b32_e32 v174, 16, v39
	v_and_b32_e32 v175, 0xffff0000, v39
	v_mfma_f32_16x16x32_bf16 v[26:29], v[158:161], v[238:241], v[26:29]
	v_lshlrev_b32_e32 v176, 16, v40
	v_and_b32_e32 v177, 0xffff0000, v40
	v_lshlrev_b32_e32 v178, 16, v41
	v_and_b32_e32 v179, 0xffff0000, v41
	v_mfma_f32_16x16x32_bf16 v[30:33], v[158:161], v[242:245], v[30:33]
	v_mul_f32_e32 v180, v2, v172
	v_mul_f32_e32 v181, v3, v173
	v_mul_f32_e32 v182, v4, v174
	v_mul_f32_e32 v183, v5, v175
	v_mfma_f32_16x16x32_bf16 v[34:37], v[158:161], v[246:249], v[34:37]
	v_mul_f32_e32 v184, v6, v176
	v_mul_f32_e32 v185, v7, v177
	v_mul_f32_e32 v186, v8, v178
	v_mul_f32_e32 v187, v9, v179
	v_mfma_f32_16x16x32_bf16 v[18:21], v[162:165], v[230:233], v[18:21]
	v_cvt_pk_bf16_f32 v200, v180, v181
	v_cvt_pk_bf16_f32 v201, v182, v183
	v_cvt_pk_bf16_f32 v202, v184, v185
	v_cvt_pk_bf16_f32 v203, v186, v187
	v_mfma_f32_16x16x32_bf16 v[22:25], v[162:165], v[234:237], v[22:25]
	v_mul_f32_e32 v196, v172, v172
	v_mul_f32_e32 v197, v174, v174
	v_mul_f32_e32 v198, v176, v176
	v_mul_f32_e32 v199, v178, v178
	v_mfma_f32_16x16x32_bf16 v[26:29], v[162:165], v[238:241], v[26:29]
	v_fma_f32 v196, v173, v173, v196
	v_fma_f32 v197, v175, v175, v197
	v_fma_f32 v198, v177, v177, v198
	v_fma_f32 v199, v179, v179, v199
	v_mfma_f32_16x16x32_bf16 v[30:33], v[162:165], v[242:245], v[30:33]
	v_lshlrev_b32_e32 v188, 16, v200
	v_and_b32_e32 v189, 0xffff0000, v200
	v_lshlrev_b32_e32 v190, 16, v201
	v_and_b32_e32 v191, 0xffff0000, v201
	v_mfma_f32_16x16x32_bf16 v[34:37], v[162:165], v[246:249], v[34:37]
	v_lshlrev_b32_e32 v192, 16, v202
	v_and_b32_e32 v193, 0xffff0000, v202
	v_lshlrev_b32_e32 v194, 16, v203
	v_and_b32_e32 v195, 0xffff0000, v203
	v_mfma_f32_16x16x32_bf16 v[18:21], v[158:161], v[120:123], v[18:21]
	v_fma_f32 v180, v2, v172, -v188
	v_fma_f32 v181, v3, v173, -v189
	v_fma_f32 v182, v4, v174, -v190
	v_fma_f32 v183, v5, v175, -v191
	v_mfma_f32_16x16x32_bf16 v[22:25], v[158:161], v[124:127], v[22:25]
	v_fma_f32 v184, v6, v176, -v192
	v_fma_f32 v185, v7, v177, -v193
	v_fma_f32 v186, v8, v178, -v194
	v_fma_f32 v187, v9, v179, -v195
	v_mfma_f32_16x16x32_bf16 v[26:29], v[158:161], v[132:135], v[26:29]
	v_add_f32_e32 v196, v196, v197
	v_add_f32_e32 v196, v196, v198
	v_add_f32_e32 v196, v196, v199
	v_add_f32_e32 v224, v224, v196
	v_mfma_f32_16x16x32_bf16 v[30:33], v[158:161], v[136:139], v[30:33]
	v_cvt_pk_bf16_f32 v204, v180, v181
	v_cvt_pk_bf16_f32 v205, v182, v183
	v_cvt_pk_bf16_f32 v206, v184, v185
	v_cvt_pk_bf16_f32 v207, v186, v187
	v_mfma_f32_16x16x32_bf16 v[34:37], v[158:161], v[140:143], v[34:37]
	s_waitcnt vmcnt(12)
	s_waitcnt lgkmcnt(0)
	s_barrier
; __device__ __forceinline__ unsigned f2bf(float f) { unsigned u = __builtin_bit_cast(unsigned, f); return (u + 0x7fffu + ((u >> 16) & 1u)) >> 16; }
; __device__ __forceinline__ void rt_step(const RtLoad& L, const bf16_t* bh, const bf16_t* bl, f32x4 (&acc)[2][5], float (&ss)[2], int ko) {
;     RtW W;
; #pragma unroll
;     for (int n = 0; n < 5; ++n) { W.wh[n] = *(const bf16x8*)(bh + (size_t)n * 16 * D + ko); W.wl[n] = *(const bf16x8*)(bl + (size_t)n * 16 * D + ko); }
;     bf16x8 ahi[2], alo[2];
; #pragma unroll
;     for (int mi = 0; mi < 2; ++mi) { const u32x4 xw = L.x[mi]; const f32x4 xa = (f32x4){bflo(xw.x), bfhi(xw.x), bflo(xw.y), bfhi(xw.y)}, xb = (f32x4){bflo(xw.z), bfhi(xw.z), bflo(xw.w), bfhi(xw.w)};
;         ss[mi] += (xa.x * xa.x + xa.y * xa.y) + (xa.z * xa.z + xa.w * xa.w) + (xb.x * xb.x + xb.y * xb.y) + (xb.z * xb.z + xb.w * xb.w);
;         const float u[8] = {xa.x * L.g[0].x, xa.y * L.g[0].y, xa.z * L.g[0].z, xa.w * L.g[0].w, xb.x * L.g[1].x, xb.y * L.g[1].y, xb.z * L.g[1].z, xb.w * L.g[1].w};
;         unsigned hb[8]; float lo[8];
; #pragma unroll
;         for (int j = 0; j < 8; ++j) { hb[j] = f2bf(u[j]); lo[j] = u[j] - __builtin_bit_cast(float, hb[j] << 16); }
;         const u32x4 hw = (u32x4){hb[0] | (hb[1] << 16), hb[2] | (hb[3] << 16), hb[4] | (hb[5] << 16), hb[6] | (hb[7] << 16)};
;         const u32x4 lw = (u32x4){pk2(lo[0], lo[1]), pk2(lo[2], lo[3]), pk2(lo[4], lo[5]), pk2(lo[6], lo[7])};
;         ahi[mi] = __builtin_bit_cast(bf16x8, hw); alo[mi] = __builtin_bit_cast(bf16x8, lw); }
; #pragma unroll
;     for (int n = 0; n < 5; ++n)
; #pragma unroll
;         for (int mi = 0; mi < 2; ++mi) { acc[mi][n] = __builtin_amdgcn_mfma_f32_16x16x32_bf16(ahi[mi], W.wh[n], acc[mi][n], 0, 0, 0);
;             acc[mi][n] = __builtin_amdgcn_mfma_f32_16x16x32_bf16(alo[mi], W.wh[n], acc[mi][n], 0, 0, 0);
;             acc[mi][n] = __builtin_amdgcn_mfma_f32_16x16x32_bf16(ahi[mi], W.wl[n], acc[mi][n], 0, 0, 0); }
; }
; __device__ __forceinline__ void p5_router(Frame& F) {
;     ...
; #pragma unroll 1
;           for (int ks = 0; ks < 32; ks += 2) {
;               rt_load(Lb, h0, h1, gp, (ks + 1) * 32); rt_step(La, bh, bl, acc, ss, ks * 32);
;               if (ks + 2 < 32) rt_load(La, h0, h1, gp, (ks + 2) * 32);
;               rt_step(Lb, bh, bl, acc, ss, (ks + 1) * 32); }
	s_mov_b32 s33, s94
	s_mov_b32 s94, s95
	s_mov_b32 s95, s91
	s_mov_b32 s91, s25
	s_mov_b32 s25, s33
	s_add_i32 s39, s39, 0x80
	s_and_b32 s39, s39, 0x1fff
	s_add_u32 s40, s86, s39
	s_addc_u32 s41, s87, 0
	s_lshl_b32 s33, s39, 1
	s_add_u32 s44, s66, s33
	s_addc_u32 s45, s67, 0
	global_load_dwordx4 v[2:5], v216, s[44:45]
	global_load_dwordx4 v[6:9], v216, s[44:45] offset:16
	s_add_i32 m0, s94, s98
	s_nop 0
	global_load_lds_dwordx4 v208, s[40:41]
	s_add_i32 m0, s94, s99
	s_nop 0
	global_load_lds_dwordx4 v209, s[40:41]
	s_add_i32 m0, s94, s100
	s_nop 0
	global_load_lds_dwordx4 v210, s[40:41]
	s_add_i32 m0, s94, s101
	s_nop 0
	global_load_lds_dwordx4 v211, s[40:41]
	v_add_u32_e32 v214, s95, v212
	v_add_u32_e32 v215, s95, v213
	ds_read_b128 v[226:229], v215
	ds_read_b128 v[230:233], v214 offset:0
	ds_read_b128 v[234:237], v214 offset:2048
	ds_read_b128 v[238:241], v214 offset:4096
	ds_read_b128 v[242:245], v214 offset:6144
	ds_read_b128 v[246:249], v214 offset:8192
	ds_read_b128 v[120:123], v214 offset:10240
	ds_read_b128 v[124:127], v214 offset:12288
	ds_read_b128 v[132:135], v214 offset:14336
	ds_read_b128 v[136:139], v214 offset:16384
	ds_read_b128 v[140:143], v214 offset:18432
	v_mfma_f32_16x16x32_bf16 v[18:21], v[200:203], v[58:61], v[18:21]
	v_mfma_f32_16x16x32_bf16 v[22:25], v[200:203], v[62:65], v[22:25]
	s_waitcnt lgkmcnt(10)
	v_lshlrev_b32_e32 v172, 16, v226
	v_and_b32_e32 v173, 0xffff0000, v226
	v_lshlrev_b32_e32 v174, 16, v227
	v_and_b32_e32 v175, 0xffff0000, v227
	v_mfma_f32_16x16x32_bf16 v[26:29], v[200:203], v[66:69], v[26:29]
	v_lshlrev_b32_e32 v176, 16, v228
	v_and_b32_e32 v177, 0xffff0000, v228
	v_lshlrev_b32_e32 v178, 16, v229
	v_and_b32_e32 v179, 0xffff0000, v229
	v_mfma_f32_16x16x32_bf16 v[30:33], v[200:203], v[70:73], v[30:33]
	v_mul_f32_e32 v180, v10, v172
	v_mul_f32_e32 v181, v11, v173
	v_mul_f32_e32 v182, v12, v174
	v_mul_f32_e32 v183, v13, v175
	v_mfma_f32_16x16x32_bf16 v[34:37], v[200:203], v[74:77], v[34:37]
	v_mul_f32_e32 v184, v14, v176
	v_mul_f32_e32 v185, v15, v177
	v_mul_f32_e32 v186, v16, v178
	v_mul_f32_e32 v187, v17, v179
	v_mfma_f32_16x16x32_bf16 v[18:21], v[204:207], v[58:61], v[18:21]
	v_cvt_pk_bf16_f32 v158, v180, v181
	v_cvt_pk_bf16_f32 v159, v182, v183
	v_cvt_pk_bf16_f32 v160, v184, v185
	v_cvt_pk_bf16_f32 v161, v186, v187
	v_mfma_f32_16x16x32_bf16 v[22:25], v[204:207], v[62:65], v[22:25]
	v_mul_f32_e32 v196, v172, v172
	v_mul_f32_e32 v197, v174, v174
	v_mul_f32_e32 v198, v176, v176
	v_mul_f32_e32 v199, v178, v178
	v_mfma_f32_16x16x32_bf16 v[26:29], v[204:207], v[66:69], v[26:29]
	v_fma_f32 v196, v173, v173, v196
	v_fma_f32 v197, v175, v175, v197
	v_fma_f32 v198, v177, v177, v198
	v_fma_f32 v199, v179, v179, v199
	v_mfma_f32_16x16x32_bf16 v[30:33], v[204:207], v[70:73], v[30:33]
	v_lshlrev_b32_e32 v188, 16, v158
	v_and_b32_e32 v189, 0xffff0000, v158
	v_lshlrev_b32_e32 v190, 16, v159
	v_and_b32_e32 v191, 0xffff0000, v159
	v_mfma_f32_16x16x32_bf16 v[34:37], v[204:207], v[74:77], v[34:37]
	v_lshlrev_b32_e32 v192, 16, v160
	v_and_b32_e32 v193, 0xffff0000, v160
	v_lshlrev_b32_e32 v194, 16, v161
	v_and_b32_e32 v195, 0xffff0000, v161
	v_mfma_f32_16x16x32_bf16 v[18:21], v[200:203], v[100:103], v[18:21]
	v_fma_f32 v180, v10, v172, -v188
	v_fma_f32 v181, v11, v173, -v189
	v_fma_f32 v182, v12, v174, -v190
	v_fma_f32 v183, v13, v175, -v191
	v_mfma_f32_16x16x32_bf16 v[22:25], v[200:203], v[104:107], v[22:25]
	v_fma_f32 v184, v14, v176, -v192
	v_fma_f32 v185, v15, v177, -v193
	v_fma_f32 v186, v16, v178, -v194
	v_fma_f32 v187, v17, v179, -v195
	v_mfma_f32_16x16x32_bf16 v[26:29], v[200:203], v[108:111], v[26:29]
	v_add_f32_e32 v196, v196, v197
	v_add_f32_e32 v196, v196, v198
	v_add_f32_e32 v196, v196, v199
	v_add_f32_e32 v224, v224, v196
	v_mfma_f32_16x16x32_bf16 v[30:33], v[200:203], v[112:115], v[30:33]
	v_cvt_pk_bf16_f32 v162, v180, v181
	v_cvt_pk_bf16_f32 v163, v182, v183
	v_cvt_pk_bf16_f32 v164, v184, v185
	v_cvt_pk_bf16_f32 v165, v186, v187
	v_mfma_f32_16x16x32_bf16 v[34:37], v[200:203], v[116:119], v[34:37]
	s_waitcnt vmcnt(12)
	s_waitcnt lgkmcnt(0)
	s_barrier
	s_mov_b32 s33, s94
	s_mov_b32 s94, s95
	s_mov_b32 s95, s91
	s_mov_b32 s91, s25
	s_mov_b32 s25, s33
	s_add_i32 s39, s39, 0x80
	s_and_b32 s39, s39, 0x1fff
	s_add_u32 s40, s86, s39
	s_addc_u32 s41, s87, 0
	s_lshl_b32 s33, s39, 1
	s_add_u32 s44, s66, s33
	s_addc_u32 s45, s67, 0
	global_load_dwordx4 v[10:13], v216, s[44:45]
	global_load_dwordx4 v[14:17], v216, s[44:45] offset:16
	s_add_i32 m0, s94, s98
	s_nop 0
	global_load_lds_dwordx4 v208, s[40:41]
	s_add_i32 m0, s94, s99
	s_nop 0
	global_load_lds_dwordx4 v209, s[40:41]
	s_add_i32 m0, s94, s100
	s_nop 0
	global_load_lds_dwordx4 v210, s[40:41]
	s_add_i32 m0, s94, s101
	s_nop 0
	global_load_lds_dwordx4 v211, s[40:41]
	v_add_u32_e32 v214, s95, v212
	v_add_u32_e32 v215, s95, v213
	ds_read_b128 v[38:41], v215
	ds_read_b128 v[58:61], v214 offset:0
	ds_read_b128 v[62:65], v214 offset:2048
	ds_read_b128 v[66:69], v214 offset:4096
	ds_read_b128 v[70:73], v214 offset:6144
	ds_read_b128 v[74:77], v214 offset:8192
	ds_read_b128 v[100:103], v214 offset:10240
	ds_read_b128 v[104:107], v214 offset:12288
	ds_read_b128 v[108:111], v214 offset:14336
	ds_read_b128 v[112:115], v214 offset:16384
	ds_read_b128 v[116:119], v214 offset:18432
	v_mfma_f32_16x16x32_bf16 v[18:21], v[158:161], v[230:233], v[18:21]
	v_mfma_f32_16x16x32_bf16 v[22:25], v[158:161], v[234:237], v[22:25]
	s_waitcnt lgkmcnt(10)
; __device__ __forceinline__ unsigned f2bf(float f) { unsigned u = __builtin_bit_cast(unsigned, f); return (u + 0x7fffu + ((u >> 16) & 1u)) >> 16; }
; __device__ __forceinline__ void rt_step(const RtLoad& L, const bf16_t* bh, const bf16_t* bl, f32x4 (&acc)[2][5], float (&ss)[2], int ko) {
;     RtW W;
; #pragma unroll
;     for (int n = 0; n < 5; ++n) { W.wh[n] = *(const bf16x8*)(bh + (size_t)n * 16 * D + ko); W.wl[n] = *(const bf16x8*)(bl + (size_t)n * 16 * D + ko); }
;     bf16x8 ahi[2], alo[2];
; #pragma unroll
;     for (int mi = 0; mi < 2; ++mi) { const u32x4 xw = L.x[mi]; const f32x4 xa = (f32x4){bflo(xw.x), bfhi(xw.x), bflo(xw.y), bfhi(xw.y)}, xb = (f32x4){bflo(xw.z), bfhi(xw.z), bflo(xw.w), bfhi(xw.w)};
;         ss[mi] += (xa.x * xa.x + xa.y * xa.y) + (xa.z * xa.z + xa.w * xa.w) + (xb.x * xb.x + xb.y * xb.y) + (xb.z * xb.z + xb.w * xb.w);
;         const float u[8] = {xa.x * L.g[0].x, xa.y * L.g[0].y, xa.z * L.g[0].z, xa.w * L.g[0].w, xb.x * L.g[1].x, xb.y * L.g[1].y, xb.z * L.g[1].z, xb.w * L.g[1].w};
;         unsigned hb[8]; float lo[8];
; #pragma unroll
;         for (int j = 0; j < 8; ++j) { hb[j] = f2bf(u[j]); lo[j] = u[j] - __builtin_bit_cast(float, hb[j] << 16); }
;         const u32x4 hw = (u32x4){hb[0] | (hb[1] << 16), hb[2] | (hb[3] << 16), hb[4] | (hb[5] << 16), hb[6] | (hb[7] << 16)};
;         const u32x4 lw = (u32x4){pk2(lo[0], lo[1]), pk2(lo[2], lo[3]), pk2(lo[4], lo[5]), pk2(lo[6], lo[7])};
;         ahi[mi] = __builtin_bit_cast(bf16x8, hw); alo[mi] = __builtin_bit_cast(bf16x8, lw); }
; #pragma unroll
;     for (int n = 0; n < 5; ++n)
; #pragma unroll
;         for (int mi = 0; mi < 2; ++mi) { acc[mi][n] = __builtin_amdgcn_mfma_f32_16x16x32_bf16(ahi[mi], W.wh[n], acc[mi][n], 0, 0, 0);
;             acc[mi][n] = __builtin_amdgcn_mfma_f32_16x16x32_bf16(alo[mi], W.wh[n], acc[mi][n], 0, 0, 0);
;             acc[mi][n] = __builtin_amdgcn_mfma_f32_16x16x32_bf16(ahi[mi], W.wl[n], acc[mi][n], 0, 0, 0); }
; }
; __device__ __forceinline__ void p5_router(Frame& F) {
;     ...
; #pragma unroll 1
;           for (int ks = 0; ks < 32; ks += 2) {
;               rt_load(Lb, h0, h1, gp, (ks + 1) * 32); rt_step(La, bh, bl, acc, ss, ks * 32);
;               if (ks + 2 < 32) rt_load(La, h0, h1, gp, (ks + 2) * 32);
;               rt_step(Lb, bh, bl, acc, ss, (ks + 1) * 32); }
	v_lshlrev_b32_e32 v172, 16, v38
	v_and_b32_e32 v173, 0xffff0000, v38
	v_lshlrev_b32_e32 v174, 16, v39
	v_and_b32_e32 v175, 0xffff0000, v39
	v_mfma_f32_16x16x32_bf16 v[26:29], v[158:161], v[238:241], v[26:29]
	v_lshlrev_b32_e32 v176, 16, v40
	v_and_b32_e32 v177, 0xffff0000, v40
	v_lshlrev_b32_e32 v178, 16, v41
	v_and_b32_e32 v179, 0xffff0000, v41
	v_mfma_f32_16x16x32_bf16 v[30:33], v[158:161], v[242:245], v[30:33]
	v_mul_f32_e32 v180, v42, v172
	v_mul_f32_e32 v181, v43, v173
	v_mul_f32_e32 v182, v44, v174
	v_mul_f32_e32 v183, v45, v175
	v_mfma_f32_16x16x32_bf16 v[34:37], v[158:161], v[246:249], v[34:37]
	v_mul_f32_e32 v184, v46, v176
	v_mul_f32_e32 v185, v47, v177
	v_mul_f32_e32 v186, v48, v178
	v_mul_f32_e32 v187, v49, v179
	v_mfma_f32_16x16x32_bf16 v[18:21], v[162:165], v[230:233], v[18:21]
	v_cvt_pk_bf16_f32 v200, v180, v181
	v_cvt_pk_bf16_f32 v201, v182, v183
	v_cvt_pk_bf16_f32 v202, v184, v185
	v_cvt_pk_bf16_f32 v203, v186, v187
	v_mfma_f32_16x16x32_bf16 v[22:25], v[162:165], v[234:237], v[22:25]
	v_mul_f32_e32 v196, v172, v172
	v_mul_f32_e32 v197, v174, v174
	v_mul_f32_e32 v198, v176, v176
	v_mul_f32_e32 v199, v178, v178
	v_mfma_f32_16x16x32_bf16 v[26:29], v[162:165], v[238:241], v[26:29]
	v_fma_f32 v196, v173, v173, v196
	v_fma_f32 v197, v175, v175, v197
	v_fma_f32 v198, v177, v177, v198
	v_fma_f32 v199, v179, v179, v199
	v_mfma_f32_16x16x32_bf16 v[30:33], v[162:165], v[242:245], v[30:33]
	v_lshlrev_b32_e32 v188, 16, v200
	v_and_b32_e32 v189, 0xffff0000, v200
	v_lshlrev_b32_e32 v190, 16, v201
	v_and_b32_e32 v191, 0xffff0000, v201
	v_mfma_f32_16x16x32_bf16 v[34:37], v[162:165], v[246:249], v[34:37]
	v_lshlrev_b32_e32 v192, 16, v202
	v_and_b32_e32 v193, 0xffff0000, v202
	v_lshlrev_b32_e32 v194, 16, v203
	v_and_b32_e32 v195, 0xffff0000, v203
	v_mfma_f32_16x16x32_bf16 v[18:21], v[158:161], v[120:123], v[18:21]
	v_fma_f32 v180, v42, v172, -v188
	v_fma_f32 v181, v43, v173, -v189
	v_fma_f32 v182, v44, v174, -v190
	v_fma_f32 v183, v45, v175, -v191
	v_mfma_f32_16x16x32_bf16 v[22:25], v[158:161], v[124:127], v[22:25]
	v_fma_f32 v184, v46, v176, -v192
	v_fma_f32 v185, v47, v177, -v193
	v_fma_f32 v186, v48, v178, -v194
	v_fma_f32 v187, v49, v179, -v195
	v_mfma_f32_16x16x32_bf16 v[26:29], v[158:161], v[132:135], v[26:29]
	v_add_f32_e32 v196, v196, v197
	v_add_f32_e32 v196, v196, v198
	v_add_f32_e32 v196, v196, v199
	v_add_f32_e32 v224, v224, v196
	v_mfma_f32_16x16x32_bf16 v[30:33], v[158:161], v[136:139], v[30:33]
	v_cvt_pk_bf16_f32 v204, v180, v181
	v_cvt_pk_bf16_f32 v205, v182, v183
	v_cvt_pk_bf16_f32 v206, v184, v185
	v_cvt_pk_bf16_f32 v207, v186, v187
	v_mfma_f32_16x16x32_bf16 v[34:37], v[158:161], v[140:143], v[34:37]
	s_waitcnt vmcnt(12)
	s_waitcnt lgkmcnt(0)
	s_barrier
	s_mov_b32 s33, s94
	s_mov_b32 s94, s95
	s_mov_b32 s95, s91
	s_mov_b32 s91, s25
	s_mov_b32 s25, s33
	s_mov_b32 s85, 13
.Lrt_loop_p4:
	s_add_i32 s39, s39, 0x80
	s_and_b32 s39, s39, 0x1fff
	s_add_u32 s40, s86, s39
	s_addc_u32 s41, s87, 0
	s_lshl_b32 s33, s39, 1
	s_add_u32 s44, s66, s33
	s_addc_u32 s45, s67, 0
	global_load_dwordx4 v[42:45], v216, s[44:45]
	global_load_dwordx4 v[46:49], v216, s[44:45] offset:16
	s_add_i32 m0, s94, s98
	s_nop 0
	global_load_lds_dwordx4 v208, s[40:41]
	s_add_i32 m0, s94, s99
	s_nop 0
	global_load_lds_dwordx4 v209, s[40:41]
	s_add_i32 m0, s94, s100
	s_nop 0
	global_load_lds_dwordx4 v210, s[40:41]
	s_add_i32 m0, s94, s101
	s_nop 0
	global_load_lds_dwordx4 v211, s[40:41]
	v_add_u32_e32 v214, s95, v212
	v_add_u32_e32 v215, s95, v213
	ds_read_b128 v[226:229], v215
	ds_read_b128 v[230:233], v214 offset:0
	ds_read_b128 v[234:237], v214 offset:2048
	ds_read_b128 v[238:241], v214 offset:4096
	ds_read_b128 v[242:245], v214 offset:6144
	ds_read_b128 v[246:249], v214 offset:8192
	ds_read_b128 v[120:123], v214 offset:10240
	ds_read_b128 v[124:127], v214 offset:12288
	ds_read_b128 v[132:135], v214 offset:14336
	ds_read_b128 v[136:139], v214 offset:16384
	ds_read_b128 v[140:143], v214 offset:18432
	v_mfma_f32_16x16x32_bf16 v[18:21], v[200:203], v[58:61], v[18:21]
	v_mfma_f32_16x16x32_bf16 v[22:25], v[200:203], v[62:65], v[22:25]
	s_waitcnt lgkmcnt(10)
	v_lshlrev_b32_e32 v172, 16, v226
	v_and_b32_e32 v173, 0xffff0000, v226
	v_lshlrev_b32_e32 v174, 16, v227
	v_and_b32_e32 v175, 0xffff0000, v227
	v_mfma_f32_16x16x32_bf16 v[26:29], v[200:203], v[66:69], v[26:29]
	v_lshlrev_b32_e32 v176, 16, v228
	v_and_b32_e32 v177, 0xffff0000, v228
	v_lshlrev_b32_e32 v178, 16, v229
	v_and_b32_e32 v179, 0xffff0000, v229
	v_mfma_f32_16x16x32_bf16 v[30:33], v[200:203], v[70:73], v[30:33]
	v_mul_f32_e32 v180, v50, v172
	v_mul_f32_e32 v181, v51, v173
	v_mul_f32_e32 v182, v52, v174
	v_mul_f32_e32 v183, v53, v175
	v_mfma_f32_16x16x32_bf16 v[34:37], v[200:203], v[74:77], v[34:37]
	v_mul_f32_e32 v184, v54, v176
	v_mul_f32_e32 v185, v55, v177
	v_mul_f32_e32 v186, v56, v178
	v_mul_f32_e32 v187, v57, v179
	v_mfma_f32_16x16x32_bf16 v[18:21], v[204:207], v[58:61], v[18:21]
	v_cvt_pk_bf16_f32 v158, v180, v181
	v_cvt_pk_bf16_f32 v159, v182, v183
	v_cvt_pk_bf16_f32 v160, v184, v185
	v_cvt_pk_bf16_f32 v161, v186, v187
	v_mfma_f32_16x16x32_bf16 v[22:25], v[204:207], v[62:65], v[22:25]
	v_mul_f32_e32 v196, v172, v172
	v_mul_f32_e32 v197, v174, v174
	v_mul_f32_e32 v198, v176, v176
	v_mul_f32_e32 v199, v178, v178
	v_mfma_f32_16x16x32_bf16 v[26:29], v[204:207], v[66:69], v[26:29]
	v_fma_f32 v196, v173, v173, v196
	v_fma_f32 v197, v175, v175, v197
	v_fma_f32 v198, v177, v177, v198
	v_fma_f32 v199, v179, v179, v199
	v_mfma_f32_16x16x32_bf16 v[30:33], v[204:207], v[70:73], v[30:33]
	v_lshlrev_b32_e32 v188, 16, v158
	v_and_b32_e32 v189, 0xffff0000, v158
	v_lshlrev_b32_e32 v190, 16, v159
	v_and_b32_e32 v191, 0xffff0000, v159
	v_mfma_f32_16x16x32_bf16 v[34:37], v[204:207], v[74:77], v[34:37]
	v_lshlrev_b32_e32 v192, 16, v160
	v_and_b32_e32 v193, 0xffff0000, v160
	v_lshlrev_b32_e32 v194, 16, v161
	v_and_b32_e32 v195, 0xffff0000, v161
	v_mfma_f32_16x16x32_bf16 v[18:21], v[200:203], v[100:103], v[18:21]
	v_fma_f32 v180, v50, v172, -v188
	v_fma_f32 v181, v51, v173, -v189
	v_fma_f32 v182, v52, v174, -v190
	v_fma_f32 v183, v53, v175, -v191
	v_mfma_f32_16x16x32_bf16 v[22:25], v[200:203], v[104:107], v[22:25]
	v_fma_f32 v184, v54, v176, -v192
	v_fma_f32 v185, v55, v177, -v193
	v_fma_f32 v186, v56, v178, -v194
	v_fma_f32 v187, v57, v179, -v195
	v_mfma_f32_16x16x32_bf16 v[26:29], v[200:203], v[108:111], v[26:29]
	v_add_f32_e32 v196, v196, v197
	v_add_f32_e32 v196, v196, v198
	v_add_f32_e32 v196, v196, v199
	v_add_f32_e32 v224, v224, v196
	v_mfma_f32_16x16x32_bf16 v[30:33], v[200:203], v[112:115], v[30:33]
	v_cvt_pk_bf16_f32 v162, v180, v181
	v_cvt_pk_bf16_f32 v163, v182, v183
	v_cvt_pk_bf16_f32 v164, v184, v185
	v_cvt_pk_bf16_f32 v165, v186, v187
	v_mfma_f32_16x16x32_bf16 v[34:37], v[200:203], v[116:119], v[34:37]
	s_waitcnt vmcnt(12)
	s_waitcnt lgkmcnt(0)
	s_barrier
; __device__ __forceinline__ unsigned f2bf(float f) { unsigned u = __builtin_bit_cast(unsigned, f); return (u + 0x7fffu + ((u >> 16) & 1u)) >> 16; }
; __device__ __forceinline__ void rt_step(const RtLoad& L, const bf16_t* bh, const bf16_t* bl, f32x4 (&acc)[2][5], float (&ss)[2], int ko) {
;     RtW W;
; #pragma unroll
;     for (int n = 0; n < 5; ++n) { W.wh[n] = *(const bf16x8*)(bh + (size_t)n * 16 * D + ko); W.wl[n] = *(const bf16x8*)(bl + (size_t)n * 16 * D + ko); }
;     bf16x8 ahi[2], alo[2];
; #pragma unroll
;     for (int mi = 0; mi < 2; ++mi) { const u32x4 xw = L.x[mi]; const f32x4 xa = (f32x4){bflo(xw.x), bfhi(xw.x), bflo(xw.y), bfhi(xw.y)}, xb = (f32x4){bflo(xw.z), bfhi(xw.z), bflo(xw.w), bfhi(xw.w)};
;         ss[mi] += (xa.x * xa.x + xa.y * xa.y) + (xa.z * xa.z + xa.w * xa.w) + (xb.x * xb.x + xb.y * xb.y) + (xb.z * xb.z + xb.w * xb.w);
;         const float u[8] = {xa.x * L.g[0].x, xa.y * L.g[0].y, xa.z * L.g[0].z, xa.w * L.g[0].w, xb.x * L.g[1].x, xb.y * L.g[1].y, xb.z * L.g[1].z, xb.w * L.g[1].w};
;         unsigned hb[8]; float lo[8];
; #pragma unroll
;         for (int j = 0; j < 8; ++j) { hb[j] = f2bf(u[j]); lo[j] = u[j] - __builtin_bit_cast(float, hb[j] << 16); }
;         const u32x4 hw = (u32x4){hb[0] | (hb[1] << 16), hb[2] | (hb[3] << 16), hb[4] | (hb[5] << 16), hb[6] | (hb[7] << 16)};
;         const u32x4 lw = (u32x4){pk2(lo[0], lo[1]), pk2(lo[2], lo[3]), pk2(lo[4], lo[5]), pk2(lo[6], lo[7])};
;         ahi[mi] = __builtin_bit_cast(bf16x8, hw); alo[mi] = __builtin_bit_cast(bf16x8, lw); }
; #pragma unroll
;     for (int n = 0; n < 5; ++n)
; #pragma unroll
;         for (int mi = 0; mi < 2; ++mi) { acc[mi][n] = __builtin_amdgcn_mfma_f32_16x16x32_bf16(ahi[mi], W.wh[n], acc[mi][n], 0, 0, 0);
;             acc[mi][n] = __builtin_amdgcn_mfma_f32_16x16x32_bf16(alo[mi], W.wh[n], acc[mi][n], 0, 0, 0);
;             acc[mi][n] = __builtin_amdgcn_mfma_f32_16x16x32_bf16(ahi[mi], W.wl[n], acc[mi][n], 0, 0, 0); }
; }
; __device__ __forceinline__ void p5_router(Frame& F) {
;     ...
; #pragma unroll 1
;           for (int ks = 0; ks < 32; ks += 2) {
;               rt_load(Lb, h0, h1, gp, (ks + 1) * 32); rt_step(La, bh, bl, acc, ss, ks * 32);
;               if (ks + 2 < 32) rt_load(La, h0, h1, gp, (ks + 2) * 32);
;               rt_step(Lb, bh, bl, acc, ss, (ks + 1) * 32); }
	s_mov_b32 s33, s94
	s_mov_b32 s94, s95
	s_mov_b32 s95, s91
	s_mov_b32 s91, s25
	s_mov_b32 s25, s33
	s_add_i32 s39, s39, 0x80
	s_and_b32 s39, s39, 0x1fff
	s_add_u32 s40, s86, s39
	s_addc_u32 s41, s87, 0
	s_lshl_b32 s33, s39, 1
	s_add_u32 s44, s66, s33
	s_addc_u32 s45, s67, 0
	global_load_dwordx4 v[50:53], v216, s[44:45]
	global_load_dwordx4 v[54:57], v216, s[44:45] offset:16
	s_add_i32 m0, s94, s98
	s_nop 0
	global_load_lds_dwordx4 v208, s[40:41]
	s_add_i32 m0, s94, s99
	s_nop 0
	global_load_lds_dwordx4 v209, s[40:41]
	s_add_i32 m0, s94, s100
	s_nop 0
	global_load_lds_dwordx4 v210, s[40:41]
	s_add_i32 m0, s94, s101
	s_nop 0
	global_load_lds_dwordx4 v211, s[40:41]
	v_add_u32_e32 v214, s95, v212
	v_add_u32_e32 v215, s95, v213
	ds_read_b128 v[38:41], v215
	ds_read_b128 v[58:61], v214 offset:0
	ds_read_b128 v[62:65], v214 offset:2048
	ds_read_b128 v[66:69], v214 offset:4096
	ds_read_b128 v[70:73], v214 offset:6144
	ds_read_b128 v[74:77], v214 offset:8192
	ds_read_b128 v[100:103], v214 offset:10240
	ds_read_b128 v[104:107], v214 offset:12288
	ds_read_b128 v[108:111], v214 offset:14336
	ds_read_b128 v[112:115], v214 offset:16384
	ds_read_b128 v[116:119], v214 offset:18432
	v_mfma_f32_16x16x32_bf16 v[18:21], v[158:161], v[230:233], v[18:21]
	v_mfma_f32_16x16x32_bf16 v[22:25], v[158:161], v[234:237], v[22:25]
	s_waitcnt lgkmcnt(10)
	v_lshlrev_b32_e32 v172, 16, v38
	v_and_b32_e32 v173, 0xffff0000, v38
	v_lshlrev_b32_e32 v174, 16, v39
	v_and_b32_e32 v175, 0xffff0000, v39
	v_mfma_f32_16x16x32_bf16 v[26:29], v[158:161], v[238:241], v[26:29]
	v_lshlrev_b32_e32 v176, 16, v40
	v_and_b32_e32 v177, 0xffff0000, v40
	v_lshlrev_b32_e32 v178, 16, v41
	v_and_b32_e32 v179, 0xffff0000, v41
	v_mfma_f32_16x16x32_bf16 v[30:33], v[158:161], v[242:245], v[30:33]
	v_mul_f32_e32 v180, v2, v172
	v_mul_f32_e32 v181, v3, v173
	v_mul_f32_e32 v182, v4, v174
	v_mul_f32_e32 v183, v5, v175
	v_mfma_f32_16x16x32_bf16 v[34:37], v[158:161], v[246:249], v[34:37]
	v_mul_f32_e32 v184, v6, v176
	v_mul_f32_e32 v185, v7, v177
	v_mul_f32_e32 v186, v8, v178
	v_mul_f32_e32 v187, v9, v179
	v_mfma_f32_16x16x32_bf16 v[18:21], v[162:165], v[230:233], v[18:21]
	v_cvt_pk_bf16_f32 v200, v180, v181
	v_cvt_pk_bf16_f32 v201, v182, v183
	v_cvt_pk_bf16_f32 v202, v184, v185
	v_cvt_pk_bf16_f32 v203, v186, v187
	v_mfma_f32_16x16x32_bf16 v[22:25], v[162:165], v[234:237], v[22:25]
	v_mul_f32_e32 v196, v172, v172
	v_mul_f32_e32 v197, v174, v174
	v_mul_f32_e32 v198, v176, v176
	v_mul_f32_e32 v199, v178, v178
	v_mfma_f32_16x16x32_bf16 v[26:29], v[162:165], v[238:241], v[26:29]
	v_fma_f32 v196, v173, v173, v196
	v_fma_f32 v197, v175, v175, v197
	v_fma_f32 v198, v177, v177, v198
	v_fma_f32 v199, v179, v179, v199
	v_mfma_f32_16x16x32_bf16 v[30:33], v[162:165], v[242:245], v[30:33]
	v_lshlrev_b32_e32 v188, 16, v200
	v_and_b32_e32 v189, 0xffff0000, v200
	v_lshlrev_b32_e32 v190, 16, v201
	v_and_b32_e32 v191, 0xffff0000, v201
	v_mfma_f32_16x16x32_bf16 v[34:37], v[162:165], v[246:249], v[34:37]
	v_lshlrev_b32_e32 v192, 16, v202
	v_and_b32_e32 v193, 0xffff0000, v202
	v_lshlrev_b32_e32 v194, 16, v203
	v_and_b32_e32 v195, 0xffff0000, v203
	v_mfma_f32_16x16x32_bf16 v[18:21], v[158:161], v[120:123], v[18:21]
	v_fma_f32 v180, v2, v172, -v188
	v_fma_f32 v181, v3, v173, -v189
	v_fma_f32 v182, v4, v174, -v190
	v_fma_f32 v183, v5, v175, -v191
	v_mfma_f32_16x16x32_bf16 v[22:25], v[158:161], v[124:127], v[22:25]
	v_fma_f32 v184, v6, v176, -v192
	v_fma_f32 v185, v7, v177, -v193
	v_fma_f32 v186, v8, v178, -v194
	v_fma_f32 v187, v9, v179, -v195
	v_mfma_f32_16x16x32_bf16 v[26:29], v[158:161], v[132:135], v[26:29]
	v_add_f32_e32 v196, v196, v197
	v_add_f32_e32 v196, v196, v198
	v_add_f32_e32 v196, v196, v199
	v_add_f32_e32 v224, v224, v196
	v_mfma_f32_16x16x32_bf16 v[30:33], v[158:161], v[136:139], v[30:33]
	v_cvt_pk_bf16_f32 v204, v180, v181
	v_cvt_pk_bf16_f32 v205, v182, v183
	v_cvt_pk_bf16_f32 v206, v184, v185
	v_cvt_pk_bf16_f32 v207, v186, v187
	v_mfma_f32_16x16x32_bf16 v[34:37], v[158:161], v[140:143], v[34:37]
	s_waitcnt vmcnt(12)
	s_waitcnt lgkmcnt(0)
	s_barrier
	s_mov_b32 s33, s94
	s_mov_b32 s94, s95
	s_mov_b32 s95, s91
	s_mov_b32 s91, s25
	s_mov_b32 s25, s33
	s_add_i32 s39, s39, 0x80
	s_and_b32 s39, s39, 0x1fff
	s_add_u32 s40, s86, s39
	s_addc_u32 s41, s87, 0
	s_lshl_b32 s33, s39, 1
	s_add_u32 s44, s66, s33
	s_addc_u32 s45, s67, 0
	global_load_dwordx4 v[2:5], v216, s[44:45]
	global_load_dwordx4 v[6:9], v216, s[44:45] offset:16
	s_add_i32 m0, s94, s98
	s_nop 0
	global_load_lds_dwordx4 v208, s[40:41]
	s_add_i32 m0, s94, s99
	s_nop 0
	global_load_lds_dwordx4 v209, s[40:41]
	s_add_i32 m0, s94, s100
	s_nop 0
	global_load_lds_dwordx4 v210, s[40:41]
	s_add_i32 m0, s94, s101
	s_nop 0
	global_load_lds_dwordx4 v211, s[40:41]
	v_add_u32_e32 v214, s95, v212
	v_add_u32_e32 v215, s95, v213
	ds_read_b128 v[226:229], v215
	ds_read_b128 v[230:233], v214 offset:0
	ds_read_b128 v[234:237], v214 offset:2048
	ds_read_b128 v[238:241], v214 offset:4096
	ds_read_b128 v[242:245], v214 offset:6144
	ds_read_b128 v[246:249], v214 offset:8192
	ds_read_b128 v[120:123], v214 offset:10240
	ds_read_b128 v[124:127], v214 offset:12288
	ds_read_b128 v[132:135], v214 offset:14336
	ds_read_b128 v[136:139], v214 offset:16384
	ds_read_b128 v[140:143], v214 offset:18432
	v_mfma_f32_16x16x32_bf16 v[18:21], v[200:203], v[58:61], v[18:21]
	v_mfma_f32_16x16x32_bf16 v[22:25], v[200:203], v[62:65], v[22:25]
	s_waitcnt lgkmcnt(10)
; __device__ __forceinline__ unsigned f2bf(float f) { unsigned u = __builtin_bit_cast(unsigned, f); return (u + 0x7fffu + ((u >> 16) & 1u)) >> 16; }
; __device__ __forceinline__ void rt_step(const RtLoad& L, const bf16_t* bh, const bf16_t* bl, f32x4 (&acc)[2][5], float (&ss)[2], int ko) {
;     RtW W;
; #pragma unroll
;     for (int n = 0; n < 5; ++n) { W.wh[n] = *(const bf16x8*)(bh + (size_t)n * 16 * D + ko); W.wl[n] = *(const bf16x8*)(bl + (size_t)n * 16 * D + ko); }
;     bf16x8 ahi[2], alo[2];
; #pragma unroll
;     for (int mi = 0; mi < 2; ++mi) { const u32x4 xw = L.x[mi]; const f32x4 xa = (f32x4){bflo(xw.x), bfhi(xw.x), bflo(xw.y), bfhi(xw.y)}, xb = (f32x4){bflo(xw.z), bfhi(xw.z), bflo(xw.w), bfhi(xw.w)};
;         ss[mi] += (xa.x * xa.x + xa.y * xa.y) + (xa.z * xa.z + xa.w * xa.w) + (xb.x * xb.x + xb.y * xb.y) + (xb.z * xb.z + xb.w * xb.w);
;         const float u[8] = {xa.x * L.g[0].x, xa.y * L.g[0].y, xa.z * L.g[0].z, xa.w * L.g[0].w, xb.x * L.g[1].x, xb.y * L.g[1].y, xb.z * L.g[1].z, xb.w * L.g[1].w};
;         unsigned hb[8]; float lo[8];
; #pragma unroll
;         for (int j = 0; j < 8; ++j) { hb[j] = f2bf(u[j]); lo[j] = u[j] - __builtin_bit_cast(float, hb[j] << 16); }
;         const u32x4 hw = (u32x4){hb[0] | (hb[1] << 16), hb[2] | (hb[3] << 16), hb[4] | (hb[5] << 16), hb[6] | (hb[7] << 16)};
;         const u32x4 lw = (u32x4){pk2(lo[0], lo[1]), pk2(lo[2], lo[3]), pk2(lo[4], lo[5]), pk2(lo[6], lo[7])};
;         ahi[mi] = __builtin_bit_cast(bf16x8, hw); alo[mi] = __builtin_bit_cast(bf16x8, lw); }
; #pragma unroll
;     for (int n = 0; n < 5; ++n)
; #pragma unroll
;         for (int mi = 0; mi < 2; ++mi) { acc[mi][n] = __builtin_amdgcn_mfma_f32_16x16x32_bf16(ahi[mi], W.wh[n], acc[mi][n], 0, 0, 0);
;             acc[mi][n] = __builtin_amdgcn_mfma_f32_16x16x32_bf16(alo[mi], W.wh[n], acc[mi][n], 0, 0, 0);
;             acc[mi][n] = __builtin_amdgcn_mfma_f32_16x16x32_bf16(ahi[mi], W.wl[n], acc[mi][n], 0, 0, 0); }
; __device__ __forceinline__ void p5_router(Frame& F) {
;     ...
;           RtLoad La, Lb; rt_load(La, h0, h1, gp, 0);
; #pragma unroll 1
;           for (int ks = 0; ks < 32; ks += 2) {
;               rt_load(Lb, h0, h1, gp, (ks + 1) * 32); rt_step(La, bh, bl, acc, ss, ks * 32);
;               if (ks + 2 < 32) rt_load(La, h0, h1, gp, (ks + 2) * 32);
;               rt_step(Lb, bh, bl, acc, ss, (ks + 1) * 32); }
	v_lshlrev_b32_e32 v172, 16, v226
	v_and_b32_e32 v173, 0xffff0000, v226
	v_lshlrev_b32_e32 v174, 16, v227
	v_and_b32_e32 v175, 0xffff0000, v227
	v_mfma_f32_16x16x32_bf16 v[26:29], v[200:203], v[66:69], v[26:29]
	v_lshlrev_b32_e32 v176, 16, v228
	v_and_b32_e32 v177, 0xffff0000, v228
	v_lshlrev_b32_e32 v178, 16, v229
	v_and_b32_e32 v179, 0xffff0000, v229
	v_mfma_f32_16x16x32_bf16 v[30:33], v[200:203], v[70:73], v[30:33]
	v_mul_f32_e32 v180, v10, v172
	v_mul_f32_e32 v181, v11, v173
	v_mul_f32_e32 v182, v12, v174
	v_mul_f32_e32 v183, v13, v175
	v_mfma_f32_16x16x32_bf16 v[34:37], v[200:203], v[74:77], v[34:37]
	v_mul_f32_e32 v184, v14, v176
	v_mul_f32_e32 v185, v15, v177
	v_mul_f32_e32 v186, v16, v178
	v_mul_f32_e32 v187, v17, v179
	v_mfma_f32_16x16x32_bf16 v[18:21], v[204:207], v[58:61], v[18:21]
	v_cvt_pk_bf16_f32 v158, v180, v181
	v_cvt_pk_bf16_f32 v159, v182, v183
	v_cvt_pk_bf16_f32 v160, v184, v185
	v_cvt_pk_bf16_f32 v161, v186, v187
	v_mfma_f32_16x16x32_bf16 v[22:25], v[204:207], v[62:65], v[22:25]
	v_mul_f32_e32 v196, v172, v172
	v_mul_f32_e32 v197, v174, v174
	v_mul_f32_e32 v198, v176, v176
	v_mul_f32_e32 v199, v178, v178
	v_mfma_f32_16x16x32_bf16 v[26:29], v[204:207], v[66:69], v[26:29]
	v_fma_f32 v196, v173, v173, v196
	v_fma_f32 v197, v175, v175, v197
	v_fma_f32 v198, v177, v177, v198
	v_fma_f32 v199, v179, v179, v199
	v_mfma_f32_16x16x32_bf16 v[30:33], v[204:207], v[70:73], v[30:33]
	v_lshlrev_b32_e32 v188, 16, v158
	v_and_b32_e32 v189, 0xffff0000, v158
	v_lshlrev_b32_e32 v190, 16, v159
	v_and_b32_e32 v191, 0xffff0000, v159
	v_mfma_f32_16x16x32_bf16 v[34:37], v[204:207], v[74:77], v[34:37]
	v_lshlrev_b32_e32 v192, 16, v160
	v_and_b32_e32 v193, 0xffff0000, v160
	v_lshlrev_b32_e32 v194, 16, v161
	v_and_b32_e32 v195, 0xffff0000, v161
	v_mfma_f32_16x16x32_bf16 v[18:21], v[200:203], v[100:103], v[18:21]
	v_fma_f32 v180, v10, v172, -v188
	v_fma_f32 v181, v11, v173, -v189
	v_fma_f32 v182, v12, v174, -v190
	v_fma_f32 v183, v13, v175, -v191
	v_mfma_f32_16x16x32_bf16 v[22:25], v[200:203], v[104:107], v[22:25]
	v_fma_f32 v184, v14, v176, -v192
	v_fma_f32 v185, v15, v177, -v193
	v_fma_f32 v186, v16, v178, -v194
	v_fma_f32 v187, v17, v179, -v195
	v_mfma_f32_16x16x32_bf16 v[26:29], v[200:203], v[108:111], v[26:29]
	v_add_f32_e32 v196, v196, v197
	v_add_f32_e32 v196, v196, v198
	v_add_f32_e32 v196, v196, v199
	v_add_f32_e32 v224, v224, v196
	v_mfma_f32_16x16x32_bf16 v[30:33], v[200:203], v[112:115], v[30:33]
	v_cvt_pk_bf16_f32 v162, v180, v181
	v_cvt_pk_bf16_f32 v163, v182, v183
	v_cvt_pk_bf16_f32 v164, v184, v185
	v_cvt_pk_bf16_f32 v165, v186, v187
	v_mfma_f32_16x16x32_bf16 v[34:37], v[200:203], v[116:119], v[34:37]
	s_waitcnt vmcnt(12)
	s_waitcnt lgkmcnt(0)
	s_barrier
	s_mov_b32 s33, s94
	s_mov_b32 s94, s95
	s_mov_b32 s95, s91
	s_mov_b32 s91, s25
	s_mov_b32 s25, s33
	s_add_i32 s39, s39, 0x80
	s_and_b32 s39, s39, 0x1fff
	s_add_u32 s40, s86, s39
	s_addc_u32 s41, s87, 0
	s_lshl_b32 s33, s39, 1
	s_add_u32 s44, s66, s33
	s_addc_u32 s45, s67, 0
	global_load_dwordx4 v[10:13], v216, s[44:45]
	global_load_dwordx4 v[14:17], v216, s[44:45] offset:16
	s_add_i32 m0, s94, s98
	s_nop 0
	global_load_lds_dwordx4 v208, s[40:41]
	s_add_i32 m0, s94, s99
	s_nop 0
	global_load_lds_dwordx4 v209, s[40:41]
	s_add_i32 m0, s94, s100
	s_nop 0
	global_load_lds_dwordx4 v210, s[40:41]
	s_add_i32 m0, s94, s101
	s_nop 0
	global_load_lds_dwordx4 v211, s[40:41]
	v_add_u32_e32 v214, s95, v212
	v_add_u32_e32 v215, s95, v213
	ds_read_b128 v[38:41], v215
	ds_read_b128 v[58:61], v214 offset:0
	ds_read_b128 v[62:65], v214 offset:2048
	ds_read_b128 v[66:69], v214 offset:4096
	ds_read_b128 v[70:73], v214 offset:6144
	ds_read_b128 v[74:77], v214 offset:8192
	ds_read_b128 v[100:103], v214 offset:10240
	ds_read_b128 v[104:107], v214 offset:12288
	ds_read_b128 v[108:111], v214 offset:14336
	ds_read_b128 v[112:115], v214 offset:16384
	ds_read_b128 v[116:119], v214 offset:18432
	v_mfma_f32_16x16x32_bf16 v[18:21], v[158:161], v[230:233], v[18:21]
	v_mfma_f32_16x16x32_bf16 v[22:25], v[158:161], v[234:237], v[22:25]
	s_waitcnt lgkmcnt(10)
	v_lshlrev_b32_e32 v172, 16, v38
	v_and_b32_e32 v173, 0xffff0000, v38
	v_lshlrev_b32_e32 v174, 16, v39
	v_and_b32_e32 v175, 0xffff0000, v39
	v_mfma_f32_16x16x32_bf16 v[26:29], v[158:161], v[238:241], v[26:29]
	v_lshlrev_b32_e32 v176, 16, v40
	v_and_b32_e32 v177, 0xffff0000, v40
	v_lshlrev_b32_e32 v178, 16, v41
	v_and_b32_e32 v179, 0xffff0000, v41
	v_mfma_f32_16x16x32_bf16 v[30:33], v[158:161], v[242:245], v[30:33]
	v_mul_f32_e32 v180, v42, v172
	v_mul_f32_e32 v181, v43, v173
	v_mul_f32_e32 v182, v44, v174
	v_mul_f32_e32 v183, v45, v175
	v_mfma_f32_16x16x32_bf16 v[34:37], v[158:161], v[246:249], v[34:37]
	v_mul_f32_e32 v184, v46, v176
	v_mul_f32_e32 v185, v47, v177
	v_mul_f32_e32 v186, v48, v178
	v_mul_f32_e32 v187, v49, v179
	v_mfma_f32_16x16x32_bf16 v[18:21], v[162:165], v[230:233], v[18:21]
	v_cvt_pk_bf16_f32 v200, v180, v181
	v_cvt_pk_bf16_f32 v201, v182, v183
	v_cvt_pk_bf16_f32 v202, v184, v185
	v_cvt_pk_bf16_f32 v203, v186, v187
	v_mfma_f32_16x16x32_bf16 v[22:25], v[162:165], v[234:237], v[22:25]
	v_mul_f32_e32 v196, v172, v172
	v_mul_f32_e32 v197, v174, v174
	v_mul_f32_e32 v198, v176, v176
	v_mul_f32_e32 v199, v178, v178
	v_mfma_f32_16x16x32_bf16 v[26:29], v[162:165], v[238:241], v[26:29]
	v_fma_f32 v196, v173, v173, v196
	v_fma_f32 v197, v175, v175, v197
	v_fma_f32 v198, v177, v177, v198
	v_fma_f32 v199, v179, v179, v199
	v_mfma_f32_16x16x32_bf16 v[30:33], v[162:165], v[242:245], v[30:33]
	v_lshlrev_b32_e32 v188, 16, v200
	v_and_b32_e32 v189, 0xffff0000, v200
	v_lshlrev_b32_e32 v190, 16, v201
	v_and_b32_e32 v191, 0xffff0000, v201
	v_mfma_f32_16x16x32_bf16 v[34:37], v[162:165], v[246:249], v[34:37]
	v_lshlrev_b32_e32 v192, 16, v202
	v_and_b32_e32 v193, 0xffff0000, v202
	v_lshlrev_b32_e32 v194, 16, v203
	v_and_b32_e32 v195, 0xffff0000, v203
	v_mfma_f32_16x16x32_bf16 v[18:21], v[158:161], v[120:123], v[18:21]
	v_fma_f32 v180, v42, v172, -v188
	v_fma_f32 v181, v43, v173, -v189
	v_fma_f32 v182, v44, v174, -v190
	v_fma_f32 v183, v45, v175, -v191
	v_mfma_f32_16x16x32_bf16 v[22:25], v[158:161], v[124:127], v[22:25]
	v_fma_f32 v184, v46, v176, -v192
	v_fma_f32 v185, v47, v177, -v193
	v_fma_f32 v186, v48, v178, -v194
	v_fma_f32 v187, v49, v179, -v195
	v_mfma_f32_16x16x32_bf16 v[26:29], v[158:161], v[132:135], v[26:29]
	v_add_f32_e32 v196, v196, v197
	v_add_f32_e32 v196, v196, v198
	v_add_f32_e32 v196, v196, v199
	v_add_f32_e32 v224, v224, v196
	v_mfma_f32_16x16x32_bf16 v[30:33], v[158:161], v[136:139], v[30:33]
	v_cvt_pk_bf16_f32 v204, v180, v181
	v_cvt_pk_bf16_f32 v205, v182, v183
	v_cvt_pk_bf16_f32 v206, v184, v185
	v_cvt_pk_bf16_f32 v207, v186, v187
	v_mfma_f32_16x16x32_bf16 v[34:37], v[158:161], v[140:143], v[34:37]
	s_waitcnt vmcnt(12)
	s_waitcnt lgkmcnt(0)
	s_barrier
; __device__ __forceinline__ unsigned f2bf(float f) { unsigned u = __builtin_bit_cast(unsigned, f); return (u + 0x7fffu + ((u >> 16) & 1u)) >> 16; }
; __device__ __forceinline__ void rt_step(const RtLoad& L, const bf16_t* bh, const bf16_t* bl, f32x4 (&acc)[2][5], float (&ss)[2], int ko) {
;     RtW W;
; #pragma unroll
;     for (int n = 0; n < 5; ++n) { W.wh[n] = *(const bf16x8*)(bh + (size_t)n * 16 * D + ko); W.wl[n] = *(const bf16x8*)(bl + (size_t)n * 16 * D + ko); }
;     bf16x8 ahi[2], alo[2];
; #pragma unroll
;     for (int mi = 0; mi < 2; ++mi) { const u32x4 xw = L.x[mi]; const f32x4 xa = (f32x4){bflo(xw.x), bfhi(xw.x), bflo(xw.y), bfhi(xw.y)}, xb = (f32x4){bflo(xw.z), bfhi(xw.z), bflo(xw.w), bfhi(xw.w)};
;         ss[mi] += (xa.x * xa.x + xa.y * xa.y) + (xa.z * xa.z + xa.w * xa.w) + (xb.x * xb.x + xb.y * xb.y) + (xb.z * xb.z + xb.w * xb.w);
;         const float u[8] = {xa.x * L.g[0].x, xa.y * L.g[0].y, xa.z * L.g[0].z, xa.w * L.g[0].w, xb.x * L.g[1].x, xb.y * L.g[1].y, xb.z * L.g[1].z, xb.w * L.g[1].w};
;         unsigned hb[8]; float lo[8];
; #pragma unroll
;         for (int j = 0; j < 8; ++j) { hb[j] = f2bf(u[j]); lo[j] = u[j] - __builtin_bit_cast(float, hb[j] << 16); }
;         const u32x4 hw = (u32x4){hb[0] | (hb[1] << 16), hb[2] | (hb[3] << 16), hb[4] | (hb[5] << 16), hb[6] | (hb[7] << 16)};
;         const u32x4 lw = (u32x4){pk2(lo[0], lo[1]), pk2(lo[2], lo[3]), pk2(lo[4], lo[5]), pk2(lo[6], lo[7])};
;         ahi[mi] = __builtin_bit_cast(bf16x8, hw); alo[mi] = __builtin_bit_cast(bf16x8, lw); }
; #pragma unroll
;     for (int n = 0; n < 5; ++n)
; #pragma unroll
;         for (int mi = 0; mi < 2; ++mi) { acc[mi][n] = __builtin_amdgcn_mfma_f32_16x16x32_bf16(ahi[mi], W.wh[n], acc[mi][n], 0, 0, 0);
;             acc[mi][n] = __builtin_amdgcn_mfma_f32_16x16x32_bf16(alo[mi], W.wh[n], acc[mi][n], 0, 0, 0);
;             acc[mi][n] = __builtin_amdgcn_mfma_f32_16x16x32_bf16(ahi[mi], W.wl[n], acc[mi][n], 0, 0, 0); }
; __device__ __forceinline__ void p5_router(Frame& F) {
;     ...
;           RtLoad La, Lb; rt_load(La, h0, h1, gp, 0);
; #pragma unroll 1
;           for (int ks = 0; ks < 32; ks += 2) {
;               rt_load(Lb, h0, h1, gp, (ks + 1) * 32); rt_step(La, bh, bl, acc, ss, ks * 32);
;               if (ks + 2 < 32) rt_load(La, h0, h1, gp, (ks + 2) * 32);
;               rt_step(Lb, bh, bl, acc, ss, (ks + 1) * 32); }
	s_mov_b32 s33, s94
	s_mov_b32 s94, s95
	s_mov_b32 s95, s91
	s_mov_b32 s91, s25
	s_mov_b32 s25, s33
	s_sub_u32 s85, s85, 1
	s_cmp_lg_u32 s85, 0
	s_cbranch_scc1 .Lrt_loop_p4
	s_add_i32 s39, s39, 0x80
	s_and_b32 s39, s39, 0x1fff
	s_add_u32 s40, s86, s39
	s_addc_u32 s41, s87, 0
	s_lshl_b32 s33, s39, 1
	s_add_u32 s44, s66, s33
	s_addc_u32 s45, s67, 0
	global_load_dwordx4 v[42:45], v216, s[44:45]
	global_load_dwordx4 v[46:49], v216, s[44:45] offset:16
	s_add_i32 m0, s94, s98
	s_nop 0
	global_load_lds_dwordx4 v208, s[40:41]
	s_add_i32 m0, s94, s99
	s_nop 0
	global_load_lds_dwordx4 v209, s[40:41]
	s_add_i32 m0, s94, s100
	s_nop 0
	global_load_lds_dwordx4 v210, s[40:41]
	s_add_i32 m0, s94, s101
	s_nop 0
	global_load_lds_dwordx4 v211, s[40:41]
	v_add_u32_e32 v214, s95, v212
	v_add_u32_e32 v215, s95, v213
	ds_read_b128 v[226:229], v215
	ds_read_b128 v[230:233], v214 offset:0
	ds_read_b128 v[234:237], v214 offset:2048
	ds_read_b128 v[238:241], v214 offset:4096
	ds_read_b128 v[242:245], v214 offset:6144
	ds_read_b128 v[246:249], v214 offset:8192
	ds_read_b128 v[120:123], v214 offset:10240
	ds_read_b128 v[124:127], v214 offset:12288
	ds_read_b128 v[132:135], v214 offset:14336
	ds_read_b128 v[136:139], v214 offset:16384
	ds_read_b128 v[140:143], v214 offset:18432
	v_mfma_f32_16x16x32_bf16 v[18:21], v[200:203], v[58:61], v[18:21]
	v_mfma_f32_16x16x32_bf16 v[22:25], v[200:203], v[62:65], v[22:25]
	s_waitcnt lgkmcnt(10)
	v_lshlrev_b32_e32 v172, 16, v226
	v_and_b32_e32 v173, 0xffff0000, v226
	v_lshlrev_b32_e32 v174, 16, v227
	v_and_b32_e32 v175, 0xffff0000, v227
	v_mfma_f32_16x16x32_bf16 v[26:29], v[200:203], v[66:69], v[26:29]
	v_lshlrev_b32_e32 v176, 16, v228
	v_and_b32_e32 v177, 0xffff0000, v228
	v_lshlrev_b32_e32 v178, 16, v229
	v_and_b32_e32 v179, 0xffff0000, v229
	v_mfma_f32_16x16x32_bf16 v[30:33], v[200:203], v[70:73], v[30:33]
	v_mul_f32_e32 v180, v50, v172
	v_mul_f32_e32 v181, v51, v173
	v_mul_f32_e32 v182, v52, v174
	v_mul_f32_e32 v183, v53, v175
	v_mfma_f32_16x16x32_bf16 v[34:37], v[200:203], v[74:77], v[34:37]
	v_mul_f32_e32 v184, v54, v176
	v_mul_f32_e32 v185, v55, v177
	v_mul_f32_e32 v186, v56, v178
	v_mul_f32_e32 v187, v57, v179
	v_mfma_f32_16x16x32_bf16 v[18:21], v[204:207], v[58:61], v[18:21]
	v_cvt_pk_bf16_f32 v158, v180, v181
	v_cvt_pk_bf16_f32 v159, v182, v183
	v_cvt_pk_bf16_f32 v160, v184, v185
	v_cvt_pk_bf16_f32 v161, v186, v187
	v_mfma_f32_16x16x32_bf16 v[22:25], v[204:207], v[62:65], v[22:25]
	v_mul_f32_e32 v196, v172, v172
	v_mul_f32_e32 v197, v174, v174
	v_mul_f32_e32 v198, v176, v176
	v_mul_f32_e32 v199, v178, v178
	v_mfma_f32_16x16x32_bf16 v[26:29], v[204:207], v[66:69], v[26:29]
	v_fma_f32 v196, v173, v173, v196
	v_fma_f32 v197, v175, v175, v197
	v_fma_f32 v198, v177, v177, v198
	v_fma_f32 v199, v179, v179, v199
	v_mfma_f32_16x16x32_bf16 v[30:33], v[204:207], v[70:73], v[30:33]
	v_lshlrev_b32_e32 v188, 16, v158
	v_and_b32_e32 v189, 0xffff0000, v158
	v_lshlrev_b32_e32 v190, 16, v159
	v_and_b32_e32 v191, 0xffff0000, v159
	v_mfma_f32_16x16x32_bf16 v[34:37], v[204:207], v[74:77], v[34:37]
	v_lshlrev_b32_e32 v192, 16, v160
	v_and_b32_e32 v193, 0xffff0000, v160
	v_lshlrev_b32_e32 v194, 16, v161
	v_and_b32_e32 v195, 0xffff0000, v161
	v_mfma_f32_16x16x32_bf16 v[18:21], v[200:203], v[100:103], v[18:21]
	v_fma_f32 v180, v50, v172, -v188
	v_fma_f32 v181, v51, v173, -v189
	v_fma_f32 v182, v52, v174, -v190
	v_fma_f32 v183, v53, v175, -v191
	v_mfma_f32_16x16x32_bf16 v[22:25], v[200:203], v[104:107], v[22:25]
	v_fma_f32 v184, v54, v176, -v192
	v_fma_f32 v185, v55, v177, -v193
	v_fma_f32 v186, v56, v178, -v194
	v_fma_f32 v187, v57, v179, -v195
	v_mfma_f32_16x16x32_bf16 v[26:29], v[200:203], v[108:111], v[26:29]
	v_add_f32_e32 v196, v196, v197
	v_add_f32_e32 v196, v196, v198
	v_add_f32_e32 v196, v196, v199
	v_add_f32_e32 v224, v224, v196
	v_mfma_f32_16x16x32_bf16 v[30:33], v[200:203], v[112:115], v[30:33]
	v_cvt_pk_bf16_f32 v162, v180, v181
	v_cvt_pk_bf16_f32 v163, v182, v183
	v_cvt_pk_bf16_f32 v164, v184, v185
	v_cvt_pk_bf16_f32 v165, v186, v187
	v_mfma_f32_16x16x32_bf16 v[34:37], v[200:203], v[116:119], v[34:37]
	s_waitcnt vmcnt(12)
	s_waitcnt lgkmcnt(0)
	s_barrier
	s_mov_b32 s33, s94
	s_mov_b32 s94, s95
	s_mov_b32 s95, s91
	s_mov_b32 s91, s25
	s_mov_b32 s25, s33
	s_add_i32 s39, s39, 0x80
	s_and_b32 s39, s39, 0x1fff
	s_add_u32 s40, s86, s39
	s_addc_u32 s41, s87, 0
	s_lshl_b32 s33, s39, 1
	s_add_u32 s44, s66, s33
	s_addc_u32 s45, s67, 0
	global_load_dwordx4 v[50:53], v216, s[44:45]
	global_load_dwordx4 v[54:57], v216, s[44:45] offset:16
	s_add_i32 m0, s94, s98
	s_nop 0
	global_load_lds_dwordx4 v208, s[40:41]
	s_add_i32 m0, s94, s99
	s_nop 0
	global_load_lds_dwordx4 v209, s[40:41]
	s_add_i32 m0, s94, s100
	s_nop 0
	global_load_lds_dwordx4 v210, s[40:41]
	s_add_i32 m0, s94, s101
	s_nop 0
	global_load_lds_dwordx4 v211, s[40:41]
	v_add_u32_e32 v214, s95, v212
	v_add_u32_e32 v215, s95, v213
	ds_read_b128 v[38:41], v215
	ds_read_b128 v[58:61], v214 offset:0
	ds_read_b128 v[62:65], v214 offset:2048
	ds_read_b128 v[66:69], v214 offset:4096
	ds_read_b128 v[70:73], v214 offset:6144
	ds_read_b128 v[74:77], v214 offset:8192
	ds_read_b128 v[100:103], v214 offset:10240
	ds_read_b128 v[104:107], v214 offset:12288
	ds_read_b128 v[108:111], v214 offset:14336
	ds_read_b128 v[112:115], v214 offset:16384
	ds_read_b128 v[116:119], v214 offset:18432
	v_mfma_f32_16x16x32_bf16 v[18:21], v[158:161], v[230:233], v[18:21]
	v_mfma_f32_16x16x32_bf16 v[22:25], v[158:161], v[234:237], v[22:25]
	s_waitcnt lgkmcnt(10)
; __device__ __forceinline__ unsigned f2bf(float f) { unsigned u = __builtin_bit_cast(unsigned, f); return (u + 0x7fffu + ((u >> 16) & 1u)) >> 16; }
; __device__ __forceinline__ void rt_step(const RtLoad& L, const bf16_t* bh, const bf16_t* bl, f32x4 (&acc)[2][5], float (&ss)[2], int ko) {
;     RtW W;
; #pragma unroll
;     for (int n = 0; n < 5; ++n) { W.wh[n] = *(const bf16x8*)(bh + (size_t)n * 16 * D + ko); W.wl[n] = *(const bf16x8*)(bl + (size_t)n * 16 * D + ko); }
;     bf16x8 ahi[2], alo[2];
; #pragma unroll
;     for (int mi = 0; mi < 2; ++mi) { const u32x4 xw = L.x[mi]; const f32x4 xa = (f32x4){bflo(xw.x), bfhi(xw.x), bflo(xw.y), bfhi(xw.y)}, xb = (f32x4){bflo(xw.z), bfhi(xw.z), bflo(xw.w), bfhi(xw.w)};
;         ss[mi] += (xa.x * xa.x + xa.y * xa.y) + (xa.z * xa.z + xa.w * xa.w) + (xb.x * xb.x + xb.y * xb.y) + (xb.z * xb.z + xb.w * xb.w);
;         const float u[8] = {xa.x * L.g[0].x, xa.y * L.g[0].y, xa.z * L.g[0].z, xa.w * L.g[0].w, xb.x * L.g[1].x, xb.y * L.g[1].y, xb.z * L.g[1].z, xb.w * L.g[1].w};
;         unsigned hb[8]; float lo[8];
; #pragma unroll
;         for (int j = 0; j < 8; ++j) { hb[j] = f2bf(u[j]); lo[j] = u[j] - __builtin_bit_cast(float, hb[j] << 16); }
;         const u32x4 hw = (u32x4){hb[0] | (hb[1] << 16), hb[2] | (hb[3] << 16), hb[4] | (hb[5] << 16), hb[6] | (hb[7] << 16)};
;         const u32x4 lw = (u32x4){pk2(lo[0], lo[1]), pk2(lo[2], lo[3]), pk2(lo[4], lo[5]), pk2(lo[6], lo[7])};
;         ahi[mi] = __builtin_bit_cast(bf16x8, hw); alo[mi] = __builtin_bit_cast(bf16x8, lw); }
; #pragma unroll
;     for (int n = 0; n < 5; ++n)
; #pragma unroll
;         for (int mi = 0; mi < 2; ++mi) { acc[mi][n] = __builtin_amdgcn_mfma_f32_16x16x32_bf16(ahi[mi], W.wh[n], acc[mi][n], 0, 0, 0);
;             acc[mi][n] = __builtin_amdgcn_mfma_f32_16x16x32_bf16(alo[mi], W.wh[n], acc[mi][n], 0, 0, 0);
;             acc[mi][n] = __builtin_amdgcn_mfma_f32_16x16x32_bf16(ahi[mi], W.wl[n], acc[mi][n], 0, 0, 0); }
; __device__ __forceinline__ void p5_router(Frame& F) {
;     ...
;           RtLoad La, Lb; rt_load(La, h0, h1, gp, 0);
; #pragma unroll 1
;           for (int ks = 0; ks < 32; ks += 2) {
;               rt_load(Lb, h0, h1, gp, (ks + 1) * 32); rt_step(La, bh, bl, acc, ss, ks * 32);
;               if (ks + 2 < 32) rt_load(La, h0, h1, gp, (ks + 2) * 32);
;               rt_step(Lb, bh, bl, acc, ss, (ks + 1) * 32); }
	v_lshlrev_b32_e32 v172, 16, v38
	v_and_b32_e32 v173, 0xffff0000, v38
	v_lshlrev_b32_e32 v174, 16, v39
	v_and_b32_e32 v175, 0xffff0000, v39
	v_mfma_f32_16x16x32_bf16 v[26:29], v[158:161], v[238:241], v[26:29]
	v_lshlrev_b32_e32 v176, 16, v40
	v_and_b32_e32 v177, 0xffff0000, v40
	v_lshlrev_b32_e32 v178, 16, v41
	v_and_b32_e32 v179, 0xffff0000, v41
	v_mfma_f32_16x16x32_bf16 v[30:33], v[158:161], v[242:245], v[30:33]
	v_mul_f32_e32 v180, v2, v172
	v_mul_f32_e32 v181, v3, v173
	v_mul_f32_e32 v182, v4, v174
	v_mul_f32_e32 v183, v5, v175
	v_mfma_f32_16x16x32_bf16 v[34:37], v[158:161], v[246:249], v[34:37]
	v_mul_f32_e32 v184, v6, v176
	v_mul_f32_e32 v185, v7, v177
	v_mul_f32_e32 v186, v8, v178
	v_mul_f32_e32 v187, v9, v179
	v_mfma_f32_16x16x32_bf16 v[18:21], v[162:165], v[230:233], v[18:21]
	v_cvt_pk_bf16_f32 v200, v180, v181
	v_cvt_pk_bf16_f32 v201, v182, v183
	v_cvt_pk_bf16_f32 v202, v184, v185
	v_cvt_pk_bf16_f32 v203, v186, v187
	v_mfma_f32_16x16x32_bf16 v[22:25], v[162:165], v[234:237], v[22:25]
	v_mul_f32_e32 v196, v172, v172
	v_mul_f32_e32 v197, v174, v174
	v_mul_f32_e32 v198, v176, v176
	v_mul_f32_e32 v199, v178, v178
	v_mfma_f32_16x16x32_bf16 v[26:29], v[162:165], v[238:241], v[26:29]
	v_fma_f32 v196, v173, v173, v196
	v_fma_f32 v197, v175, v175, v197
	v_fma_f32 v198, v177, v177, v198
	v_fma_f32 v199, v179, v179, v199
	v_mfma_f32_16x16x32_bf16 v[30:33], v[162:165], v[242:245], v[30:33]
	v_lshlrev_b32_e32 v188, 16, v200
	v_and_b32_e32 v189, 0xffff0000, v200
	v_lshlrev_b32_e32 v190, 16, v201
	v_and_b32_e32 v191, 0xffff0000, v201
	v_mfma_f32_16x16x32_bf16 v[34:37], v[162:165], v[246:249], v[34:37]
	v_lshlrev_b32_e32 v192, 16, v202
	v_and_b32_e32 v193, 0xffff0000, v202
	v_lshlrev_b32_e32 v194, 16, v203
	v_and_b32_e32 v195, 0xffff0000, v203
	v_mfma_f32_16x16x32_bf16 v[18:21], v[158:161], v[120:123], v[18:21]
	v_fma_f32 v180, v2, v172, -v188
	v_fma_f32 v181, v3, v173, -v189
	v_fma_f32 v182, v4, v174, -v190
	v_fma_f32 v183, v5, v175, -v191
	v_mfma_f32_16x16x32_bf16 v[22:25], v[158:161], v[124:127], v[22:25]
	v_fma_f32 v184, v6, v176, -v192
	v_fma_f32 v185, v7, v177, -v193
	v_fma_f32 v186, v8, v178, -v194
	v_fma_f32 v187, v9, v179, -v195
	v_mfma_f32_16x16x32_bf16 v[26:29], v[158:161], v[132:135], v[26:29]
	v_add_f32_e32 v196, v196, v197
	v_add_f32_e32 v196, v196, v198
	v_add_f32_e32 v196, v196, v199
	v_add_f32_e32 v224, v224, v196
	v_mfma_f32_16x16x32_bf16 v[30:33], v[158:161], v[136:139], v[30:33]
	v_cvt_pk_bf16_f32 v204, v180, v181
	v_cvt_pk_bf16_f32 v205, v182, v183
	v_cvt_pk_bf16_f32 v206, v184, v185
	v_cvt_pk_bf16_f32 v207, v186, v187
	v_mfma_f32_16x16x32_bf16 v[34:37], v[158:161], v[140:143], v[34:37]
	s_waitcnt vmcnt(12)
	s_waitcnt lgkmcnt(0)
	s_barrier
	s_mov_b32 s33, s94
	s_mov_b32 s94, s95
	s_mov_b32 s95, s91
	s_mov_b32 s91, s25
	s_mov_b32 s25, s33
	s_add_i32 s39, s39, 0x80
	s_and_b32 s39, s39, 0x1fff
	s_add_u32 s40, s86, s39
	s_addc_u32 s41, s87, 0
	s_lshl_b32 s33, s39, 1
	s_add_u32 s44, s66, s33
	s_addc_u32 s45, s67, 0
	global_load_dwordx4 v[2:5], v216, s[44:45]
	global_load_dwordx4 v[6:9], v216, s[44:45] offset:16
	s_add_i32 m0, s94, s98
	s_nop 0
	global_load_lds_dwordx4 v208, s[40:41]
	s_add_i32 m0, s94, s99
	s_nop 0
	global_load_lds_dwordx4 v209, s[40:41]
	s_add_i32 m0, s94, s100
	s_nop 0
	global_load_lds_dwordx4 v210, s[40:41]
	s_add_i32 m0, s94, s101
	s_nop 0
	global_load_lds_dwordx4 v211, s[40:41]
	v_add_u32_e32 v214, s95, v212
	v_add_u32_e32 v215, s95, v213
	ds_read_b128 v[226:229], v215
	ds_read_b128 v[230:233], v214 offset:0
	ds_read_b128 v[234:237], v214 offset:2048
	ds_read_b128 v[238:241], v214 offset:4096
	ds_read_b128 v[242:245], v214 offset:6144
	ds_read_b128 v[246:249], v214 offset:8192
	ds_read_b128 v[120:123], v214 offset:10240
	ds_read_b128 v[124:127], v214 offset:12288
	ds_read_b128 v[132:135], v214 offset:14336
	ds_read_b128 v[136:139], v214 offset:16384
	ds_read_b128 v[140:143], v214 offset:18432
	v_mfma_f32_16x16x32_bf16 v[18:21], v[200:203], v[58:61], v[18:21]
	v_mfma_f32_16x16x32_bf16 v[22:25], v[200:203], v[62:65], v[22:25]
	s_waitcnt lgkmcnt(10)
	v_lshlrev_b32_e32 v172, 16, v226
	v_and_b32_e32 v173, 0xffff0000, v226
	v_lshlrev_b32_e32 v174, 16, v227
	v_and_b32_e32 v175, 0xffff0000, v227
	v_mfma_f32_16x16x32_bf16 v[26:29], v[200:203], v[66:69], v[26:29]
	v_lshlrev_b32_e32 v176, 16, v228
	v_and_b32_e32 v177, 0xffff0000, v228
	v_lshlrev_b32_e32 v178, 16, v229
	v_and_b32_e32 v179, 0xffff0000, v229
	v_mfma_f32_16x16x32_bf16 v[30:33], v[200:203], v[70:73], v[30:33]
	v_mul_f32_e32 v180, v10, v172
	v_mul_f32_e32 v181, v11, v173
	v_mul_f32_e32 v182, v12, v174
	v_mul_f32_e32 v183, v13, v175
	v_mfma_f32_16x16x32_bf16 v[34:37], v[200:203], v[74:77], v[34:37]
	v_mul_f32_e32 v184, v14, v176
	v_mul_f32_e32 v185, v15, v177
	v_mul_f32_e32 v186, v16, v178
	v_mul_f32_e32 v187, v17, v179
	v_mfma_f32_16x16x32_bf16 v[18:21], v[204:207], v[58:61], v[18:21]
	v_cvt_pk_bf16_f32 v158, v180, v181
	v_cvt_pk_bf16_f32 v159, v182, v183
	v_cvt_pk_bf16_f32 v160, v184, v185
	v_cvt_pk_bf16_f32 v161, v186, v187
	v_mfma_f32_16x16x32_bf16 v[22:25], v[204:207], v[62:65], v[22:25]
	v_mul_f32_e32 v196, v172, v172
	v_mul_f32_e32 v197, v174, v174
	v_mul_f32_e32 v198, v176, v176
	v_mul_f32_e32 v199, v178, v178
	v_mfma_f32_16x16x32_bf16 v[26:29], v[204:207], v[66:69], v[26:29]
	v_fma_f32 v196, v173, v173, v196
	v_fma_f32 v197, v175, v175, v197
	v_fma_f32 v198, v177, v177, v198
	v_fma_f32 v199, v179, v179, v199
	v_mfma_f32_16x16x32_bf16 v[30:33], v[204:207], v[70:73], v[30:33]
	v_lshlrev_b32_e32 v188, 16, v158
	v_and_b32_e32 v189, 0xffff0000, v158
	v_lshlrev_b32_e32 v190, 16, v159
	v_and_b32_e32 v191, 0xffff0000, v159
	v_mfma_f32_16x16x32_bf16 v[34:37], v[204:207], v[74:77], v[34:37]
	v_lshlrev_b32_e32 v192, 16, v160
	v_and_b32_e32 v193, 0xffff0000, v160
	v_lshlrev_b32_e32 v194, 16, v161
	v_and_b32_e32 v195, 0xffff0000, v161
	v_mfma_f32_16x16x32_bf16 v[18:21], v[200:203], v[100:103], v[18:21]
	v_fma_f32 v180, v10, v172, -v188
	v_fma_f32 v181, v11, v173, -v189
	v_fma_f32 v182, v12, v174, -v190
	v_fma_f32 v183, v13, v175, -v191
	v_mfma_f32_16x16x32_bf16 v[22:25], v[200:203], v[104:107], v[22:25]
	v_fma_f32 v184, v14, v176, -v192
	v_fma_f32 v185, v15, v177, -v193
	v_fma_f32 v186, v16, v178, -v194
	v_fma_f32 v187, v17, v179, -v195
	v_mfma_f32_16x16x32_bf16 v[26:29], v[200:203], v[108:111], v[26:29]
	v_add_f32_e32 v196, v196, v197
	v_add_f32_e32 v196, v196, v198
	v_add_f32_e32 v196, v196, v199
	v_add_f32_e32 v224, v224, v196
	v_mfma_f32_16x16x32_bf16 v[30:33], v[200:203], v[112:115], v[30:33]
	v_cvt_pk_bf16_f32 v162, v180, v181
	v_cvt_pk_bf16_f32 v163, v182, v183
	v_cvt_pk_bf16_f32 v164, v184, v185
	v_cvt_pk_bf16_f32 v165, v186, v187
	v_mfma_f32_16x16x32_bf16 v[34:37], v[200:203], v[116:119], v[34:37]
	s_waitcnt vmcnt(12)
	s_waitcnt lgkmcnt(0)
	s_barrier
; __device__ __forceinline__ unsigned f2bf(float f) { unsigned u = __builtin_bit_cast(unsigned, f); return (u + 0x7fffu + ((u >> 16) & 1u)) >> 16; }
; __device__ __forceinline__ void rt_step(const RtLoad& L, const bf16_t* bh, const bf16_t* bl, f32x4 (&acc)[2][5], float (&ss)[2], int ko) {
;     RtW W;
; #pragma unroll
;     for (int n = 0; n < 5; ++n) { W.wh[n] = *(const bf16x8*)(bh + (size_t)n * 16 * D + ko); W.wl[n] = *(const bf16x8*)(bl + (size_t)n * 16 * D + ko); }
;     bf16x8 ahi[2], alo[2];
; #pragma unroll
;     for (int mi = 0; mi < 2; ++mi) { const u32x4 xw = L.x[mi]; const f32x4 xa = (f32x4){bflo(xw.x), bfhi(xw.x), bflo(xw.y), bfhi(xw.y)}, xb = (f32x4){bflo(xw.z), bfhi(xw.z), bflo(xw.w), bfhi(xw.w)};
;         ss[mi] += (xa.x * xa.x + xa.y * xa.y) + (xa.z * xa.z + xa.w * xa.w) + (xb.x * xb.x + xb.y * xb.y) + (xb.z * xb.z + xb.w * xb.w);
;         const float u[8] = {xa.x * L.g[0].x, xa.y * L.g[0].y, xa.z * L.g[0].z, xa.w * L.g[0].w, xb.x * L.g[1].x, xb.y * L.g[1].y, xb.z * L.g[1].z, xb.w * L.g[1].w};
;         unsigned hb[8]; float lo[8];
; #pragma unroll
;         for (int j = 0; j < 8; ++j) { hb[j] = f2bf(u[j]); lo[j] = u[j] - __builtin_bit_cast(float, hb[j] << 16); }
;         const u32x4 hw = (u32x4){hb[0] | (hb[1] << 16), hb[2] | (hb[3] << 16), hb[4] | (hb[5] << 16), hb[6] | (hb[7] << 16)};
;         const u32x4 lw = (u32x4){pk2(lo[0], lo[1]), pk2(lo[2], lo[3]), pk2(lo[4], lo[5]), pk2(lo[6], lo[7])};
;         ahi[mi] = __builtin_bit_cast(bf16x8, hw); alo[mi] = __builtin_bit_cast(bf16x8, lw); }
; #pragma unroll
;     for (int n = 0; n < 5; ++n)
; #pragma unroll
;         for (int mi = 0; mi < 2; ++mi) { acc[mi][n] = __builtin_amdgcn_mfma_f32_16x16x32_bf16(ahi[mi], W.wh[n], acc[mi][n], 0, 0, 0);
;             acc[mi][n] = __builtin_amdgcn_mfma_f32_16x16x32_bf16(alo[mi], W.wh[n], acc[mi][n], 0, 0, 0);
;             acc[mi][n] = __builtin_amdgcn_mfma_f32_16x16x32_bf16(ahi[mi], W.wl[n], acc[mi][n], 0, 0, 0); }
; __device__ __forceinline__ void p5_router(Frame& F) {
;     ...
;           RtLoad La, Lb; rt_load(La, h0, h1, gp, 0);
; #pragma unroll 1
;           for (int ks = 0; ks < 32; ks += 2) {
;               rt_load(Lb, h0, h1, gp, (ks + 1) * 32); rt_step(La, bh, bl, acc, ss, ks * 32);
;               if (ks + 2 < 32) rt_load(La, h0, h1, gp, (ks + 2) * 32);
;               rt_step(Lb, bh, bl, acc, ss, (ks + 1) * 32); }
	s_mov_b32 s33, s94
	s_mov_b32 s94, s95
	s_mov_b32 s95, s91
	s_mov_b32 s91, s25
	s_mov_b32 s25, s33
	s_add_i32 s39, s39, 0x80
	s_and_b32 s39, s39, 0x1fff
	s_add_u32 s40, s86, s39
	s_addc_u32 s41, s87, 0
	s_lshl_b32 s33, s39, 1
	s_add_u32 s44, s66, s33
	s_addc_u32 s45, s67, 0
	global_load_dwordx4 v[10:13], v216, s[44:45]
	global_load_dwordx4 v[14:17], v216, s[44:45] offset:16
	s_add_i32 m0, s94, s98
	s_nop 0
	global_load_lds_dwordx4 v208, s[40:41]
	s_add_i32 m0, s94, s99
	s_nop 0
	global_load_lds_dwordx4 v209, s[40:41]
	s_add_i32 m0, s94, s100
	s_nop 0
	global_load_lds_dwordx4 v210, s[40:41]
	s_add_i32 m0, s94, s101
	s_nop 0
	global_load_lds_dwordx4 v211, s[40:41]
	v_add_u32_e32 v214, s95, v212
	v_add_u32_e32 v215, s95, v213
	ds_read_b128 v[38:41], v215
	ds_read_b128 v[58:61], v214 offset:0
	ds_read_b128 v[62:65], v214 offset:2048
	ds_read_b128 v[66:69], v214 offset:4096
	ds_read_b128 v[70:73], v214 offset:6144
	ds_read_b128 v[74:77], v214 offset:8192
	ds_read_b128 v[100:103], v214 offset:10240
	ds_read_b128 v[104:107], v214 offset:12288
	ds_read_b128 v[108:111], v214 offset:14336
	ds_read_b128 v[112:115], v214 offset:16384
	ds_read_b128 v[116:119], v214 offset:18432
	v_mfma_f32_16x16x32_bf16 v[18:21], v[158:161], v[230:233], v[18:21]
	v_mfma_f32_16x16x32_bf16 v[22:25], v[158:161], v[234:237], v[22:25]
	s_waitcnt lgkmcnt(10)
	v_lshlrev_b32_e32 v172, 16, v38
	v_and_b32_e32 v173, 0xffff0000, v38
	v_lshlrev_b32_e32 v174, 16, v39
	v_and_b32_e32 v175, 0xffff0000, v39
	v_mfma_f32_16x16x32_bf16 v[26:29], v[158:161], v[238:241], v[26:29]
	v_lshlrev_b32_e32 v176, 16, v40
	v_and_b32_e32 v177, 0xffff0000, v40
	v_lshlrev_b32_e32 v178, 16, v41
	v_and_b32_e32 v179, 0xffff0000, v41
	v_mfma_f32_16x16x32_bf16 v[30:33], v[158:161], v[242:245], v[30:33]
	v_mul_f32_e32 v180, v42, v172
	v_mul_f32_e32 v181, v43, v173
	v_mul_f32_e32 v182, v44, v174
	v_mul_f32_e32 v183, v45, v175
	v_mfma_f32_16x16x32_bf16 v[34:37], v[158:161], v[246:249], v[34:37]
	v_mul_f32_e32 v184, v46, v176
	v_mul_f32_e32 v185, v47, v177
	v_mul_f32_e32 v186, v48, v178
	v_mul_f32_e32 v187, v49, v179
	v_mfma_f32_16x16x32_bf16 v[18:21], v[162:165], v[230:233], v[18:21]
	v_cvt_pk_bf16_f32 v200, v180, v181
	v_cvt_pk_bf16_f32 v201, v182, v183
	v_cvt_pk_bf16_f32 v202, v184, v185
	v_cvt_pk_bf16_f32 v203, v186, v187
	v_mfma_f32_16x16x32_bf16 v[22:25], v[162:165], v[234:237], v[22:25]
	v_mul_f32_e32 v196, v172, v172
	v_mul_f32_e32 v197, v174, v174
	v_mul_f32_e32 v198, v176, v176
	v_mul_f32_e32 v199, v178, v178
	v_mfma_f32_16x16x32_bf16 v[26:29], v[162:165], v[238:241], v[26:29]
	v_fma_f32 v196, v173, v173, v196
	v_fma_f32 v197, v175, v175, v197
	v_fma_f32 v198, v177, v177, v198
	v_fma_f32 v199, v179, v179, v199
	v_mfma_f32_16x16x32_bf16 v[30:33], v[162:165], v[242:245], v[30:33]
	v_lshlrev_b32_e32 v188, 16, v200
	v_and_b32_e32 v189, 0xffff0000, v200
	v_lshlrev_b32_e32 v190, 16, v201
	v_and_b32_e32 v191, 0xffff0000, v201
	v_mfma_f32_16x16x32_bf16 v[34:37], v[162:165], v[246:249], v[34:37]
	v_lshlrev_b32_e32 v192, 16, v202
	v_and_b32_e32 v193, 0xffff0000, v202
	v_lshlrev_b32_e32 v194, 16, v203
	v_and_b32_e32 v195, 0xffff0000, v203
	v_mfma_f32_16x16x32_bf16 v[18:21], v[158:161], v[120:123], v[18:21]
	v_fma_f32 v180, v42, v172, -v188
	v_fma_f32 v181, v43, v173, -v189
	v_fma_f32 v182, v44, v174, -v190
	v_fma_f32 v183, v45, v175, -v191
	v_mfma_f32_16x16x32_bf16 v[22:25], v[158:161], v[124:127], v[22:25]
	v_fma_f32 v184, v46, v176, -v192
	v_fma_f32 v185, v47, v177, -v193
	v_fma_f32 v186, v48, v178, -v194
	v_fma_f32 v187, v49, v179, -v195
	v_mfma_f32_16x16x32_bf16 v[26:29], v[158:161], v[132:135], v[26:29]
	v_add_f32_e32 v196, v196, v197
	v_add_f32_e32 v196, v196, v198
	v_add_f32_e32 v196, v196, v199
	v_add_f32_e32 v224, v224, v196
	v_mfma_f32_16x16x32_bf16 v[30:33], v[158:161], v[136:139], v[30:33]
	v_cvt_pk_bf16_f32 v204, v180, v181
	v_cvt_pk_bf16_f32 v205, v182, v183
	v_cvt_pk_bf16_f32 v206, v184, v185
	v_cvt_pk_bf16_f32 v207, v186, v187
	v_mfma_f32_16x16x32_bf16 v[34:37], v[158:161], v[140:143], v[34:37]
	s_waitcnt vmcnt(12)
	s_waitcnt lgkmcnt(0)
	s_barrier
	s_mov_b32 s33, s94
	s_mov_b32 s94, s95
	s_mov_b32 s95, s91
	s_mov_b32 s91, s25
	s_mov_b32 s25, s33
	v_add_u32_e32 v214, s95, v212
	v_add_u32_e32 v215, s95, v213
	ds_read_b128 v[226:229], v215
	ds_read_b128 v[230:233], v214 offset:0
	ds_read_b128 v[234:237], v214 offset:2048
	ds_read_b128 v[238:241], v214 offset:4096
	ds_read_b128 v[242:245], v214 offset:6144
	ds_read_b128 v[246:249], v214 offset:8192
	ds_read_b128 v[120:123], v214 offset:10240
	ds_read_b128 v[124:127], v214 offset:12288
	ds_read_b128 v[132:135], v214 offset:14336
	ds_read_b128 v[136:139], v214 offset:16384
	ds_read_b128 v[140:143], v214 offset:18432
	v_mfma_f32_16x16x32_bf16 v[18:21], v[200:203], v[58:61], v[18:21]
	v_mfma_f32_16x16x32_bf16 v[22:25], v[200:203], v[62:65], v[22:25]
	s_waitcnt lgkmcnt(10)
; __device__ __forceinline__ unsigned f2bf(float f) { unsigned u = __builtin_bit_cast(unsigned, f); return (u + 0x7fffu + ((u >> 16) & 1u)) >> 16; }
; __device__ __forceinline__ void rt_step(const RtLoad& L, const bf16_t* bh, const bf16_t* bl, f32x4 (&acc)[2][5], float (&ss)[2], int ko) {
;     RtW W;
; #pragma unroll
;     for (int n = 0; n < 5; ++n) { W.wh[n] = *(const bf16x8*)(bh + (size_t)n * 16 * D + ko); W.wl[n] = *(const bf16x8*)(bl + (size_t)n * 16 * D + ko); }
;     bf16x8 ahi[2], alo[2];
; #pragma unroll
;     for (int mi = 0; mi < 2; ++mi) { const u32x4 xw = L.x[mi]; const f32x4 xa = (f32x4){bflo(xw.x), bfhi(xw.x), bflo(xw.y), bfhi(xw.y)}, xb = (f32x4){bflo(xw.z), bfhi(xw.z), bflo(xw.w), bfhi(xw.w)};
;         ss[mi] += (xa.x * xa.x + xa.y * xa.y) + (xa.z * xa.z + xa.w * xa.w) + (xb.x * xb.x + xb.y * xb.y) + (xb.z * xb.z + xb.w * xb.w);
;         const float u[8] = {xa.x * L.g[0].x, xa.y * L.g[0].y, xa.z * L.g[0].z, xa.w * L.g[0].w, xb.x * L.g[1].x, xb.y * L.g[1].y, xb.z * L.g[1].z, xb.w * L.g[1].w};
;         unsigned hb[8]; float lo[8];
; #pragma unroll
;         for (int j = 0; j < 8; ++j) { hb[j] = f2bf(u[j]); lo[j] = u[j] - __builtin_bit_cast(float, hb[j] << 16); }
;         const u32x4 hw = (u32x4){hb[0] | (hb[1] << 16), hb[2] | (hb[3] << 16), hb[4] | (hb[5] << 16), hb[6] | (hb[7] << 16)};
;         const u32x4 lw = (u32x4){pk2(lo[0], lo[1]), pk2(lo[2], lo[3]), pk2(lo[4], lo[5]), pk2(lo[6], lo[7])};
;         ahi[mi] = __builtin_bit_cast(bf16x8, hw); alo[mi] = __builtin_bit_cast(bf16x8, lw); }
; #pragma unroll
;     for (int n = 0; n < 5; ++n)
; #pragma unroll
;         for (int mi = 0; mi < 2; ++mi) { acc[mi][n] = __builtin_amdgcn_mfma_f32_16x16x32_bf16(ahi[mi], W.wh[n], acc[mi][n], 0, 0, 0);
;             acc[mi][n] = __builtin_amdgcn_mfma_f32_16x16x32_bf16(alo[mi], W.wh[n], acc[mi][n], 0, 0, 0);
;             acc[mi][n] = __builtin_amdgcn_mfma_f32_16x16x32_bf16(ahi[mi], W.wl[n], acc[mi][n], 0, 0, 0); }
; __device__ __forceinline__ void p5_router(Frame& F) {
;     ...
;           RtLoad La, Lb; rt_load(La, h0, h1, gp, 0);
; #pragma unroll 1
;           for (int ks = 0; ks < 32; ks += 2) {
;               rt_load(Lb, h0, h1, gp, (ks + 1) * 32); rt_step(La, bh, bl, acc, ss, ks * 32);
;               if (ks + 2 < 32) rt_load(La, h0, h1, gp, (ks + 2) * 32);
;               rt_step(Lb, bh, bl, acc, ss, (ks + 1) * 32); }
	v_lshlrev_b32_e32 v172, 16, v226
	v_and_b32_e32 v173, 0xffff0000, v226
	v_lshlrev_b32_e32 v174, 16, v227
	v_and_b32_e32 v175, 0xffff0000, v227
	v_mfma_f32_16x16x32_bf16 v[26:29], v[200:203], v[66:69], v[26:29]
	v_lshlrev_b32_e32 v176, 16, v228
	v_and_b32_e32 v177, 0xffff0000, v228
	v_lshlrev_b32_e32 v178, 16, v229
	v_and_b32_e32 v179, 0xffff0000, v229
	v_mfma_f32_16x16x32_bf16 v[30:33], v[200:203], v[70:73], v[30:33]
	v_mul_f32_e32 v180, v50, v172
	v_mul_f32_e32 v181, v51, v173
	v_mul_f32_e32 v182, v52, v174
	v_mul_f32_e32 v183, v53, v175
	v_mfma_f32_16x16x32_bf16 v[34:37], v[200:203], v[74:77], v[34:37]
	v_mul_f32_e32 v184, v54, v176
	v_mul_f32_e32 v185, v55, v177
	v_mul_f32_e32 v186, v56, v178
	v_mul_f32_e32 v187, v57, v179
	v_mfma_f32_16x16x32_bf16 v[18:21], v[204:207], v[58:61], v[18:21]
	v_cvt_pk_bf16_f32 v158, v180, v181
	v_cvt_pk_bf16_f32 v159, v182, v183
	v_cvt_pk_bf16_f32 v160, v184, v185
	v_cvt_pk_bf16_f32 v161, v186, v187
	v_mfma_f32_16x16x32_bf16 v[22:25], v[204:207], v[62:65], v[22:25]
	v_mul_f32_e32 v196, v172, v172
	v_mul_f32_e32 v197, v174, v174
	v_mul_f32_e32 v198, v176, v176
	v_mul_f32_e32 v199, v178, v178
	v_mfma_f32_16x16x32_bf16 v[26:29], v[204:207], v[66:69], v[26:29]
	v_fma_f32 v196, v173, v173, v196
	v_fma_f32 v197, v175, v175, v197
	v_fma_f32 v198, v177, v177, v198
	v_fma_f32 v199, v179, v179, v199
	v_mfma_f32_16x16x32_bf16 v[30:33], v[204:207], v[70:73], v[30:33]
	v_lshlrev_b32_e32 v188, 16, v158
	v_and_b32_e32 v189, 0xffff0000, v158
	v_lshlrev_b32_e32 v190, 16, v159
	v_and_b32_e32 v191, 0xffff0000, v159
	v_mfma_f32_16x16x32_bf16 v[34:37], v[204:207], v[74:77], v[34:37]
	v_lshlrev_b32_e32 v192, 16, v160
	v_and_b32_e32 v193, 0xffff0000, v160
	v_lshlrev_b32_e32 v194, 16, v161
	v_and_b32_e32 v195, 0xffff0000, v161
	v_mfma_f32_16x16x32_bf16 v[18:21], v[200:203], v[100:103], v[18:21]
	v_fma_f32 v180, v50, v172, -v188
	v_fma_f32 v181, v51, v173, -v189
	v_fma_f32 v182, v52, v174, -v190
	v_fma_f32 v183, v53, v175, -v191
	v_mfma_f32_16x16x32_bf16 v[22:25], v[200:203], v[104:107], v[22:25]
	v_fma_f32 v184, v54, v176, -v192
	v_fma_f32 v185, v55, v177, -v193
	v_fma_f32 v186, v56, v178, -v194
	v_fma_f32 v187, v57, v179, -v195
	v_mfma_f32_16x16x32_bf16 v[26:29], v[200:203], v[108:111], v[26:29]
	v_add_f32_e32 v196, v196, v197
	v_add_f32_e32 v196, v196, v198
	v_add_f32_e32 v196, v196, v199
	v_add_f32_e32 v224, v224, v196
	v_mfma_f32_16x16x32_bf16 v[30:33], v[200:203], v[112:115], v[30:33]
	v_cvt_pk_bf16_f32 v162, v180, v181
	v_cvt_pk_bf16_f32 v163, v182, v183
	v_cvt_pk_bf16_f32 v164, v184, v185
	v_cvt_pk_bf16_f32 v165, v186, v187
	v_mfma_f32_16x16x32_bf16 v[34:37], v[200:203], v[116:119], v[34:37]
	s_waitcnt vmcnt(6)
	s_waitcnt lgkmcnt(0)
	s_barrier
	s_mov_b32 s33, s94
	s_mov_b32 s94, s95
	s_mov_b32 s95, s91
	s_mov_b32 s91, s25
	s_mov_b32 s25, s33
	v_add_u32_e32 v214, s95, v212
	v_add_u32_e32 v215, s95, v213
	ds_read_b128 v[38:41], v215
	ds_read_b128 v[58:61], v214 offset:0
	ds_read_b128 v[62:65], v214 offset:2048
	ds_read_b128 v[66:69], v214 offset:4096
	ds_read_b128 v[70:73], v214 offset:6144
	ds_read_b128 v[74:77], v214 offset:8192
	ds_read_b128 v[100:103], v214 offset:10240
	ds_read_b128 v[104:107], v214 offset:12288
	ds_read_b128 v[108:111], v214 offset:14336
	ds_read_b128 v[112:115], v214 offset:16384
	ds_read_b128 v[116:119], v214 offset:18432
	v_mfma_f32_16x16x32_bf16 v[18:21], v[158:161], v[230:233], v[18:21]
	v_mfma_f32_16x16x32_bf16 v[22:25], v[158:161], v[234:237], v[22:25]
	s_waitcnt lgkmcnt(10)
	v_lshlrev_b32_e32 v172, 16, v38
	v_and_b32_e32 v173, 0xffff0000, v38
	v_lshlrev_b32_e32 v174, 16, v39
	v_and_b32_e32 v175, 0xffff0000, v39
	v_mfma_f32_16x16x32_bf16 v[26:29], v[158:161], v[238:241], v[26:29]
	v_lshlrev_b32_e32 v176, 16, v40
	v_and_b32_e32 v177, 0xffff0000, v40
	v_lshlrev_b32_e32 v178, 16, v41
	v_and_b32_e32 v179, 0xffff0000, v41
	v_mfma_f32_16x16x32_bf16 v[30:33], v[158:161], v[242:245], v[30:33]
	v_mul_f32_e32 v180, v2, v172
	v_mul_f32_e32 v181, v3, v173
	v_mul_f32_e32 v182, v4, v174
	v_mul_f32_e32 v183, v5, v175
	v_mfma_f32_16x16x32_bf16 v[34:37], v[158:161], v[246:249], v[34:37]
	v_mul_f32_e32 v184, v6, v176
	v_mul_f32_e32 v185, v7, v177
	v_mul_f32_e32 v186, v8, v178
	v_mul_f32_e32 v187, v9, v179
	v_mfma_f32_16x16x32_bf16 v[18:21], v[162:165], v[230:233], v[18:21]
	v_cvt_pk_bf16_f32 v200, v180, v181
	v_cvt_pk_bf16_f32 v201, v182, v183
	v_cvt_pk_bf16_f32 v202, v184, v185
	v_cvt_pk_bf16_f32 v203, v186, v187
	v_mfma_f32_16x16x32_bf16 v[22:25], v[162:165], v[234:237], v[22:25]
	v_mul_f32_e32 v196, v172, v172
	v_mul_f32_e32 v197, v174, v174
	v_mul_f32_e32 v198, v176, v176
	v_mul_f32_e32 v199, v178, v178
	v_mfma_f32_16x16x32_bf16 v[26:29], v[162:165], v[238:241], v[26:29]
	v_fma_f32 v196, v173, v173, v196
	v_fma_f32 v197, v175, v175, v197
	v_fma_f32 v198, v177, v177, v198
	v_fma_f32 v199, v179, v179, v199
	v_mfma_f32_16x16x32_bf16 v[30:33], v[162:165], v[242:245], v[30:33]
	v_lshlrev_b32_e32 v188, 16, v200
	v_and_b32_e32 v189, 0xffff0000, v200
	v_lshlrev_b32_e32 v190, 16, v201
	v_and_b32_e32 v191, 0xffff0000, v201
	v_mfma_f32_16x16x32_bf16 v[34:37], v[162:165], v[246:249], v[34:37]
	v_lshlrev_b32_e32 v192, 16, v202
	v_and_b32_e32 v193, 0xffff0000, v202
	v_lshlrev_b32_e32 v194, 16, v203
	v_and_b32_e32 v195, 0xffff0000, v203
	v_mfma_f32_16x16x32_bf16 v[18:21], v[158:161], v[120:123], v[18:21]
	v_fma_f32 v180, v2, v172, -v188
	v_fma_f32 v181, v3, v173, -v189
	v_fma_f32 v182, v4, v174, -v190
	v_fma_f32 v183, v5, v175, -v191
	v_mfma_f32_16x16x32_bf16 v[22:25], v[158:161], v[124:127], v[22:25]
	v_fma_f32 v184, v6, v176, -v192
	v_fma_f32 v185, v7, v177, -v193
	v_fma_f32 v186, v8, v178, -v194
	v_fma_f32 v187, v9, v179, -v195
	v_mfma_f32_16x16x32_bf16 v[26:29], v[158:161], v[132:135], v[26:29]
	v_add_f32_e32 v196, v196, v197
	v_add_f32_e32 v196, v196, v198
	v_add_f32_e32 v196, v196, v199
	v_add_f32_e32 v224, v224, v196
	v_mfma_f32_16x16x32_bf16 v[30:33], v[158:161], v[136:139], v[30:33]
	v_cvt_pk_bf16_f32 v204, v180, v181
	v_cvt_pk_bf16_f32 v205, v182, v183
	v_cvt_pk_bf16_f32 v206, v184, v185
	v_cvt_pk_bf16_f32 v207, v186, v187
	v_mfma_f32_16x16x32_bf16 v[34:37], v[158:161], v[140:143], v[34:37]
	s_waitcnt vmcnt(0)
	s_waitcnt lgkmcnt(0)
	s_barrier
; __device__ __forceinline__ unsigned f2bf(float f) { unsigned u = __builtin_bit_cast(unsigned, f); return (u + 0x7fffu + ((u >> 16) & 1u)) >> 16; }
; __device__ __forceinline__ void rt_step(const RtLoad& L, const bf16_t* bh, const bf16_t* bl, f32x4 (&acc)[2][5], float (&ss)[2], int ko) {
;     RtW W;
; #pragma unroll
;     for (int n = 0; n < 5; ++n) { W.wh[n] = *(const bf16x8*)(bh + (size_t)n * 16 * D + ko); W.wl[n] = *(const bf16x8*)(bl + (size_t)n * 16 * D + ko); }
;     bf16x8 ahi[2], alo[2];
; #pragma unroll
;     for (int mi = 0; mi < 2; ++mi) { const u32x4 xw = L.x[mi]; const f32x4 xa = (f32x4){bflo(xw.x), bfhi(xw.x), bflo(xw.y), bfhi(xw.y)}, xb = (f32x4){bflo(xw.z), bfhi(xw.z), bflo(xw.w), bfhi(xw.w)};
;         ss[mi] += (xa.x * xa.x + xa.y * xa.y) + (xa.z * xa.z + xa.w * xa.w) + (xb.x * xb.x + xb.y * xb.y) + (xb.z * xb.z + xb.w * xb.w);
;         const float u[8] = {xa.x * L.g[0].x, xa.y * L.g[0].y, xa.z * L.g[0].z, xa.w * L.g[0].w, xb.x * L.g[1].x, xb.y * L.g[1].y, xb.z * L.g[1].z, xb.w * L.g[1].w};
;         unsigned hb[8]; float lo[8];
; #pragma unroll
;         for (int j = 0; j < 8; ++j) { hb[j] = f2bf(u[j]); lo[j] = u[j] - __builtin_bit_cast(float, hb[j] << 16); }
;         const u32x4 hw = (u32x4){hb[0] | (hb[1] << 16), hb[2] | (hb[3] << 16), hb[4] | (hb[5] << 16), hb[6] | (hb[7] << 16)};
;         const u32x4 lw = (u32x4){pk2(lo[0], lo[1]), pk2(lo[2], lo[3]), pk2(lo[4], lo[5]), pk2(lo[6], lo[7])};
;         ahi[mi] = __builtin_bit_cast(bf16x8, hw); alo[mi] = __builtin_bit_cast(bf16x8, lw); }
; #pragma unroll
;     for (int n = 0; n < 5; ++n)
; #pragma unroll
;         for (int mi = 0; mi < 2; ++mi) { acc[mi][n] = __builtin_amdgcn_mfma_f32_16x16x32_bf16(ahi[mi], W.wh[n], acc[mi][n], 0, 0, 0);
;             acc[mi][n] = __builtin_amdgcn_mfma_f32_16x16x32_bf16(alo[mi], W.wh[n], acc[mi][n], 0, 0, 0);
;             acc[mi][n] = __builtin_amdgcn_mfma_f32_16x16x32_bf16(ahi[mi], W.wl[n], acc[mi][n], 0, 0, 0); }
; __device__ __forceinline__ void p5_router(Frame& F) {
;     ...
;           RtLoad La, Lb; rt_load(La, h0, h1, gp, 0);
; #pragma unroll 1
;           for (int ks = 0; ks < 32; ks += 2) {
;               rt_load(Lb, h0, h1, gp, (ks + 1) * 32); rt_step(La, bh, bl, acc, ss, ks * 32);
;               if (ks + 2 < 32) rt_load(La, h0, h1, gp, (ks + 2) * 32);
;               rt_step(Lb, bh, bl, acc, ss, (ks + 1) * 32); }
	s_mov_b32 s33, s94
	s_mov_b32 s94, s95
	s_mov_b32 s95, s91
	s_mov_b32 s91, s25
	s_mov_b32 s25, s33
	v_add_u32_e32 v214, s95, v212
	v_add_u32_e32 v215, s95, v213
	ds_read_b128 v[226:229], v215
	ds_read_b128 v[230:233], v214 offset:0
	ds_read_b128 v[234:237], v214 offset:2048
	ds_read_b128 v[238:241], v214 offset:4096
	ds_read_b128 v[242:245], v214 offset:6144
	ds_read_b128 v[246:249], v214 offset:8192
	ds_read_b128 v[120:123], v214 offset:10240
	ds_read_b128 v[124:127], v214 offset:12288
	ds_read_b128 v[132:135], v214 offset:14336
	ds_read_b128 v[136:139], v214 offset:16384
	ds_read_b128 v[140:143], v214 offset:18432
	v_mfma_f32_16x16x32_bf16 v[18:21], v[200:203], v[58:61], v[18:21]
	v_mfma_f32_16x16x32_bf16 v[22:25], v[200:203], v[62:65], v[22:25]
	s_waitcnt lgkmcnt(10)
	v_lshlrev_b32_e32 v172, 16, v226
	v_and_b32_e32 v173, 0xffff0000, v226
	v_lshlrev_b32_e32 v174, 16, v227
	v_and_b32_e32 v175, 0xffff0000, v227
	v_mfma_f32_16x16x32_bf16 v[26:29], v[200:203], v[66:69], v[26:29]
	v_lshlrev_b32_e32 v176, 16, v228
	v_and_b32_e32 v177, 0xffff0000, v228
	v_lshlrev_b32_e32 v178, 16, v229
	v_and_b32_e32 v179, 0xffff0000, v229
	v_mfma_f32_16x16x32_bf16 v[30:33], v[200:203], v[70:73], v[30:33]
	v_mul_f32_e32 v180, v10, v172
	v_mul_f32_e32 v181, v11, v173
	v_mul_f32_e32 v182, v12, v174
	v_mul_f32_e32 v183, v13, v175
	v_mfma_f32_16x16x32_bf16 v[34:37], v[200:203], v[74:77], v[34:37]
	v_mul_f32_e32 v184, v14, v176
	v_mul_f32_e32 v185, v15, v177
	v_mul_f32_e32 v186, v16, v178
	v_mul_f32_e32 v187, v17, v179
	v_mfma_f32_16x16x32_bf16 v[18:21], v[204:207], v[58:61], v[18:21]
	v_cvt_pk_bf16_f32 v158, v180, v181
	v_cvt_pk_bf16_f32 v159, v182, v183
	v_cvt_pk_bf16_f32 v160, v184, v185
	v_cvt_pk_bf16_f32 v161, v186, v187
	v_mfma_f32_16x16x32_bf16 v[22:25], v[204:207], v[62:65], v[22:25]
	v_mul_f32_e32 v196, v172, v172
	v_mul_f32_e32 v197, v174, v174
	v_mul_f32_e32 v198, v176, v176
	v_mul_f32_e32 v199, v178, v178
	v_mfma_f32_16x16x32_bf16 v[26:29], v[204:207], v[66:69], v[26:29]
	v_fma_f32 v196, v173, v173, v196
	v_fma_f32 v197, v175, v175, v197
	v_fma_f32 v198, v177, v177, v198
	v_fma_f32 v199, v179, v179, v199
	v_mfma_f32_16x16x32_bf16 v[30:33], v[204:207], v[70:73], v[30:33]
	v_lshlrev_b32_e32 v188, 16, v158
	v_and_b32_e32 v189, 0xffff0000, v158
	v_lshlrev_b32_e32 v190, 16, v159
	v_and_b32_e32 v191, 0xffff0000, v159
	v_mfma_f32_16x16x32_bf16 v[34:37], v[204:207], v[74:77], v[34:37]
	v_lshlrev_b32_e32 v192, 16, v160
	v_and_b32_e32 v193, 0xffff0000, v160
	v_lshlrev_b32_e32 v194, 16, v161
	v_and_b32_e32 v195, 0xffff0000, v161
	v_mfma_f32_16x16x32_bf16 v[18:21], v[200:203], v[100:103], v[18:21]
	v_fma_f32 v180, v10, v172, -v188
	v_fma_f32 v181, v11, v173, -v189
	v_fma_f32 v182, v12, v174, -v190
	v_fma_f32 v183, v13, v175, -v191
	v_mfma_f32_16x16x32_bf16 v[22:25], v[200:203], v[104:107], v[22:25]
	v_fma_f32 v184, v14, v176, -v192
	v_fma_f32 v185, v15, v177, -v193
	v_fma_f32 v186, v16, v178, -v194
	v_fma_f32 v187, v17, v179, -v195
	v_mfma_f32_16x16x32_bf16 v[26:29], v[200:203], v[108:111], v[26:29]
	v_add_f32_e32 v196, v196, v197
	v_add_f32_e32 v196, v196, v198
	v_add_f32_e32 v196, v196, v199
	v_add_f32_e32 v224, v224, v196
	v_mfma_f32_16x16x32_bf16 v[30:33], v[200:203], v[112:115], v[30:33]
	v_cvt_pk_bf16_f32 v162, v180, v181
	v_cvt_pk_bf16_f32 v163, v182, v183
	v_cvt_pk_bf16_f32 v164, v184, v185
	v_cvt_pk_bf16_f32 v165, v186, v187
	v_mfma_f32_16x16x32_bf16 v[34:37], v[200:203], v[116:119], v[34:37]
	s_waitcnt lgkmcnt(0)
	s_barrier
	s_mov_b32 s33, s94
	s_mov_b32 s94, s95
	s_mov_b32 s95, s91
	s_mov_b32 s91, s25
	s_mov_b32 s25, s33
	v_mfma_f32_16x16x32_bf16 v[18:21], v[158:161], v[230:233], v[18:21]
	v_mfma_f32_16x16x32_bf16 v[22:25], v[158:161], v[234:237], v[22:25]
	v_mfma_f32_16x16x32_bf16 v[26:29], v[158:161], v[238:241], v[26:29]
	v_mfma_f32_16x16x32_bf16 v[30:33], v[158:161], v[242:245], v[30:33]
	v_mfma_f32_16x16x32_bf16 v[34:37], v[158:161], v[246:249], v[34:37]
	v_mfma_f32_16x16x32_bf16 v[18:21], v[162:165], v[230:233], v[18:21]
	v_mfma_f32_16x16x32_bf16 v[22:25], v[162:165], v[234:237], v[22:25]
	v_mfma_f32_16x16x32_bf16 v[26:29], v[162:165], v[238:241], v[26:29]
	v_mfma_f32_16x16x32_bf16 v[30:33], v[162:165], v[242:245], v[30:33]
	v_mfma_f32_16x16x32_bf16 v[34:37], v[162:165], v[246:249], v[34:37]
	v_mfma_f32_16x16x32_bf16 v[18:21], v[158:161], v[120:123], v[18:21]
	v_mfma_f32_16x16x32_bf16 v[22:25], v[158:161], v[124:127], v[22:25]
	v_mfma_f32_16x16x32_bf16 v[26:29], v[158:161], v[132:135], v[26:29]
	v_mfma_f32_16x16x32_bf16 v[30:33], v[158:161], v[136:139], v[30:33]
	v_mfma_f32_16x16x32_bf16 v[34:37], v[158:161], v[140:143], v[34:37]
	s_branch .Lrt_out
; __device__ __forceinline__ unsigned f2bf(float f) { unsigned u = __builtin_bit_cast(unsigned, f); return (u + 0x7fffu + ((u >> 16) & 1u)) >> 16; }
; __device__ __forceinline__ void rt_step(const RtLoad& L, const bf16_t* bh, const bf16_t* bl, f32x4 (&acc)[2][5], float (&ss)[2], int ko) {
;     RtW W;
; #pragma unroll
;     for (int n = 0; n < 5; ++n) { W.wh[n] = *(const bf16x8*)(bh + (size_t)n * 16 * D + ko); W.wl[n] = *(const bf16x8*)(bl + (size_t)n * 16 * D + ko); }
;     bf16x8 ahi[2], alo[2];
; #pragma unroll
;     for (int mi = 0; mi < 2; ++mi) { const u32x4 xw = L.x[mi]; const f32x4 xa = (f32x4){bflo(xw.x), bfhi(xw.x), bflo(xw.y), bfhi(xw.y)}, xb = (f32x4){bflo(xw.z), bfhi(xw.z), bflo(xw.w), bfhi(xw.w)};
;         ss[mi] += (xa.x * xa.x + xa.y * xa.y) + (xa.z * xa.z + xa.w * xa.w) + (xb.x * xb.x + xb.y * xb.y) + (xb.z * xb.z + xb.w * xb.w);
;         const float u[8] = {xa.x * L.g[0].x, xa.y * L.g[0].y, xa.z * L.g[0].z, xa.w * L.g[0].w, xb.x * L.g[1].x, xb.y * L.g[1].y, xb.z * L.g[1].z, xb.w * L.g[1].w};
;         unsigned hb[8]; float lo[8];
; #pragma unroll
;         for (int j = 0; j < 8; ++j) { hb[j] = f2bf(u[j]); lo[j] = u[j] - __builtin_bit_cast(float, hb[j] << 16); }
;         const u32x4 hw = (u32x4){hb[0] | (hb[1] << 16), hb[2] | (hb[3] << 16), hb[4] | (hb[5] << 16), hb[6] | (hb[7] << 16)};
;         const u32x4 lw = (u32x4){pk2(lo[0], lo[1]), pk2(lo[2], lo[3]), pk2(lo[4], lo[5]), pk2(lo[6], lo[7])};
;         ahi[mi] = __builtin_bit_cast(bf16x8, hw); alo[mi] = __builtin_bit_cast(bf16x8, lw); }
; #pragma unroll
;     for (int n = 0; n < 5; ++n)
; #pragma unroll
;         for (int mi = 0; mi < 2; ++mi) { acc[mi][n] = __builtin_amdgcn_mfma_f32_16x16x32_bf16(ahi[mi], W.wh[n], acc[mi][n], 0, 0, 0);
;             acc[mi][n] = __builtin_amdgcn_mfma_f32_16x16x32_bf16(alo[mi], W.wh[n], acc[mi][n], 0, 0, 0);
;             acc[mi][n] = __builtin_amdgcn_mfma_f32_16x16x32_bf16(ahi[mi], W.wl[n], acc[mi][n], 0, 0, 0); }
; __device__ __forceinline__ void p5_router(Frame& F) {
;     ...
;           RtLoad La, Lb; rt_load(La, h0, h1, gp, 0);
; #pragma unroll 1
;           for (int ks = 0; ks < 32; ks += 2) {
;               rt_load(Lb, h0, h1, gp, (ks + 1) * 32); rt_step(La, bh, bl, acc, ss, ks * 32);
;               if (ks + 2 < 32) rt_load(La, h0, h1, gp, (ks + 2) * 32);
;               rt_step(Lb, bh, bl, acc, ss, (ks + 1) * 32); }
.Lrt_path3:
	s_add_i32 s39, s39, 0x80
	s_and_b32 s39, s39, 0x1fff
	s_add_u32 s40, s86, s39
	s_addc_u32 s41, s87, 0
	s_lshl_b32 s33, s39, 1
	s_add_u32 s44, s66, s33
	s_addc_u32 s45, s67, 0
	global_load_dwordx4 v[10:13], v216, s[44:45]
	global_load_dwordx4 v[14:17], v216, s[44:45] offset:16
	s_add_i32 m0, s94, s98
	s_nop 0
	global_load_lds_dwordx4 v208, s[40:41]
	s_add_i32 m0, s94, s99
	s_nop 0
	global_load_lds_dwordx4 v209, s[40:41]
	s_add_i32 m0, s94, s100
	s_nop 0
	global_load_lds_dwordx4 v210, s[40:41]
	v_add_u32_e32 v214, s95, v212
	v_add_u32_e32 v215, s95, v213
	ds_read_b128 v[38:41], v215
	ds_read_b128 v[58:61], v214 offset:0
	ds_read_b128 v[62:65], v214 offset:2048
	ds_read_b128 v[66:69], v214 offset:4096
	ds_read_b128 v[70:73], v214 offset:6144
	ds_read_b128 v[74:77], v214 offset:8192
	ds_read_b128 v[100:103], v214 offset:10240
	ds_read_b128 v[104:107], v214 offset:12288
	ds_read_b128 v[108:111], v214 offset:14336
	ds_read_b128 v[112:115], v214 offset:16384
	ds_read_b128 v[116:119], v214 offset:18432
	s_waitcnt lgkmcnt(10)
	v_lshlrev_b32_e32 v172, 16, v38
	v_and_b32_e32 v173, 0xffff0000, v38
	v_lshlrev_b32_e32 v174, 16, v39
	v_and_b32_e32 v175, 0xffff0000, v39
	v_lshlrev_b32_e32 v176, 16, v40
	v_and_b32_e32 v177, 0xffff0000, v40
	v_lshlrev_b32_e32 v178, 16, v41
	v_and_b32_e32 v179, 0xffff0000, v41
	v_mul_f32_e32 v180, v42, v172
	v_mul_f32_e32 v181, v43, v173
	v_mul_f32_e32 v182, v44, v174
	v_mul_f32_e32 v183, v45, v175
	v_mul_f32_e32 v184, v46, v176
	v_mul_f32_e32 v185, v47, v177
	v_mul_f32_e32 v186, v48, v178
	v_mul_f32_e32 v187, v49, v179
	v_cvt_pk_bf16_f32 v200, v180, v181
	v_cvt_pk_bf16_f32 v201, v182, v183
	v_cvt_pk_bf16_f32 v202, v184, v185
	v_cvt_pk_bf16_f32 v203, v186, v187
	v_mul_f32_e32 v196, v172, v172
	v_mul_f32_e32 v197, v174, v174
	v_mul_f32_e32 v198, v176, v176
	v_mul_f32_e32 v199, v178, v178
	v_fma_f32 v196, v173, v173, v196
	v_fma_f32 v197, v175, v175, v197
	v_fma_f32 v198, v177, v177, v198
	v_fma_f32 v199, v179, v179, v199
	v_lshlrev_b32_e32 v188, 16, v200
	v_and_b32_e32 v189, 0xffff0000, v200
	v_lshlrev_b32_e32 v190, 16, v201
	v_and_b32_e32 v191, 0xffff0000, v201
	v_lshlrev_b32_e32 v192, 16, v202
	v_and_b32_e32 v193, 0xffff0000, v202
	v_lshlrev_b32_e32 v194, 16, v203
	v_and_b32_e32 v195, 0xffff0000, v203
	v_fma_f32 v180, v42, v172, -v188
	v_fma_f32 v181, v43, v173, -v189
	v_fma_f32 v182, v44, v174, -v190
	v_fma_f32 v183, v45, v175, -v191
	v_fma_f32 v184, v46, v176, -v192
	v_fma_f32 v185, v47, v177, -v193
	v_fma_f32 v186, v48, v178, -v194
	v_fma_f32 v187, v49, v179, -v195
	v_add_f32_e32 v196, v196, v197
	v_add_f32_e32 v196, v196, v198
	v_add_f32_e32 v196, v196, v199
	v_add_f32_e32 v224, v224, v196
	v_cvt_pk_bf16_f32 v204, v180, v181
	v_cvt_pk_bf16_f32 v205, v182, v183
	v_cvt_pk_bf16_f32 v206, v184, v185
	v_cvt_pk_bf16_f32 v207, v186, v187
	s_waitcnt vmcnt(10)
	s_waitcnt lgkmcnt(0)
	s_barrier
	s_mov_b32 s33, s94
	s_mov_b32 s94, s95
	s_mov_b32 s95, s91
	s_mov_b32 s91, s25
	s_mov_b32 s25, s33
	s_add_i32 s39, s39, 0x80
	s_and_b32 s39, s39, 0x1fff
	s_add_u32 s40, s86, s39
	s_addc_u32 s41, s87, 0
	s_lshl_b32 s33, s39, 1
	s_add_u32 s44, s66, s33
	s_addc_u32 s45, s67, 0
	global_load_dwordx4 v[42:45], v216, s[44:45]
	global_load_dwordx4 v[46:49], v216, s[44:45] offset:16
	s_add_i32 m0, s94, s98
	s_nop 0
	global_load_lds_dwordx4 v208, s[40:41]
	s_add_i32 m0, s94, s99
	s_nop 0
	global_load_lds_dwordx4 v209, s[40:41]
	s_add_i32 m0, s94, s100
	s_nop 0
	global_load_lds_dwordx4 v210, s[40:41]
	v_add_u32_e32 v214, s95, v212
	v_add_u32_e32 v215, s95, v213
	ds_read_b128 v[226:229], v215
	ds_read_b128 v[230:233], v214 offset:0
	ds_read_b128 v[234:237], v214 offset:2048
	ds_read_b128 v[238:241], v214 offset:4096
	ds_read_b128 v[242:245], v214 offset:6144
	ds_read_b128 v[246:249], v214 offset:8192
	ds_read_b128 v[120:123], v214 offset:10240
	ds_read_b128 v[124:127], v214 offset:12288
	ds_read_b128 v[132:135], v214 offset:14336
	ds_read_b128 v[136:139], v214 offset:16384
	ds_read_b128 v[140:143], v214 offset:18432
	v_mfma_f32_16x16x32_bf16 v[18:21], v[200:203], v[58:61], v[18:21]
	v_mfma_f32_16x16x32_bf16 v[22:25], v[200:203], v[62:65], v[22:25]
	s_waitcnt lgkmcnt(10)
	v_lshlrev_b32_e32 v172, 16, v226
	v_and_b32_e32 v173, 0xffff0000, v226
	v_lshlrev_b32_e32 v174, 16, v227
	v_and_b32_e32 v175, 0xffff0000, v227
	v_mfma_f32_16x16x32_bf16 v[26:29], v[200:203], v[66:69], v[26:29]
	v_lshlrev_b32_e32 v176, 16, v228
	v_and_b32_e32 v177, 0xffff0000, v228
	v_lshlrev_b32_e32 v178, 16, v229
	v_and_b32_e32 v179, 0xffff0000, v229
	v_mfma_f32_16x16x32_bf16 v[30:33], v[200:203], v[70:73], v[30:33]
	v_mul_f32_e32 v180, v50, v172
	v_mul_f32_e32 v181, v51, v173
	v_mul_f32_e32 v182, v52, v174
	v_mul_f32_e32 v183, v53, v175
	v_mfma_f32_16x16x32_bf16 v[34:37], v[200:203], v[74:77], v[34:37]
	v_mul_f32_e32 v184, v54, v176
	v_mul_f32_e32 v185, v55, v177
	v_mul_f32_e32 v186, v56, v178
	v_mul_f32_e32 v187, v57, v179
	v_mfma_f32_16x16x32_bf16 v[18:21], v[204:207], v[58:61], v[18:21]
	v_cvt_pk_bf16_f32 v158, v180, v181
	v_cvt_pk_bf16_f32 v159, v182, v183
	v_cvt_pk_bf16_f32 v160, v184, v185
	v_cvt_pk_bf16_f32 v161, v186, v187
	v_mfma_f32_16x16x32_bf16 v[22:25], v[204:207], v[62:65], v[22:25]
	v_mul_f32_e32 v196, v172, v172
	v_mul_f32_e32 v197, v174, v174
	v_mul_f32_e32 v198, v176, v176
	v_mul_f32_e32 v199, v178, v178
	v_mfma_f32_16x16x32_bf16 v[26:29], v[204:207], v[66:69], v[26:29]
	v_fma_f32 v196, v173, v173, v196
	v_fma_f32 v197, v175, v175, v197
	v_fma_f32 v198, v177, v177, v198
	v_fma_f32 v199, v179, v179, v199
	v_mfma_f32_16x16x32_bf16 v[30:33], v[204:207], v[70:73], v[30:33]
	v_lshlrev_b32_e32 v188, 16, v158
	v_and_b32_e32 v189, 0xffff0000, v158
	v_lshlrev_b32_e32 v190, 16, v159
	v_and_b32_e32 v191, 0xffff0000, v159
	v_mfma_f32_16x16x32_bf16 v[34:37], v[204:207], v[74:77], v[34:37]
	v_lshlrev_b32_e32 v192, 16, v160
	v_and_b32_e32 v193, 0xffff0000, v160
	v_lshlrev_b32_e32 v194, 16, v161
	v_and_b32_e32 v195, 0xffff0000, v161
	v_mfma_f32_16x16x32_bf16 v[18:21], v[200:203], v[100:103], v[18:21]
	v_fma_f32 v180, v50, v172, -v188
	v_fma_f32 v181, v51, v173, -v189
	v_fma_f32 v182, v52, v174, -v190
	v_fma_f32 v183, v53, v175, -v191
	v_mfma_f32_16x16x32_bf16 v[22:25], v[200:203], v[104:107], v[22:25]
	v_fma_f32 v184, v54, v176, -v192
	v_fma_f32 v185, v55, v177, -v193
	v_fma_f32 v186, v56, v178, -v194
	v_fma_f32 v187, v57, v179, -v195
	v_mfma_f32_16x16x32_bf16 v[26:29], v[200:203], v[108:111], v[26:29]
	v_add_f32_e32 v196, v196, v197
	v_add_f32_e32 v196, v196, v198
	v_add_f32_e32 v196, v196, v199
	v_add_f32_e32 v224, v224, v196
	v_mfma_f32_16x16x32_bf16 v[30:33], v[200:203], v[112:115], v[30:33]
	v_cvt_pk_bf16_f32 v162, v180, v181
	v_cvt_pk_bf16_f32 v163, v182, v183
	v_cvt_pk_bf16_f32 v164, v184, v185
	v_cvt_pk_bf16_f32 v165, v186, v187
	v_mfma_f32_16x16x32_bf16 v[34:37], v[200:203], v[116:119], v[34:37]
	s_waitcnt vmcnt(10)
	s_waitcnt lgkmcnt(0)
	s_barrier
; __device__ __forceinline__ unsigned f2bf(float f) { unsigned u = __builtin_bit_cast(unsigned, f); return (u + 0x7fffu + ((u >> 16) & 1u)) >> 16; }
; __device__ __forceinline__ void rt_step(const RtLoad& L, const bf16_t* bh, const bf16_t* bl, f32x4 (&acc)[2][5], float (&ss)[2], int ko) {
;     RtW W;
; #pragma unroll
;     for (int n = 0; n < 5; ++n) { W.wh[n] = *(const bf16x8*)(bh + (size_t)n * 16 * D + ko); W.wl[n] = *(const bf16x8*)(bl + (size_t)n * 16 * D + ko); }
;     bf16x8 ahi[2], alo[2];
; #pragma unroll
;     for (int mi = 0; mi < 2; ++mi) { const u32x4 xw = L.x[mi]; const f32x4 xa = (f32x4){bflo(xw.x), bfhi(xw.x), bflo(xw.y), bfhi(xw.y)}, xb = (f32x4){bflo(xw.z), bfhi(xw.z), bflo(xw.w), bfhi(xw.w)};
;         ss[mi] += (xa.x * xa.x + xa.y * xa.y) + (xa.z * xa.z + xa.w * xa.w) + (xb.x * xb.x + xb.y * xb.y) + (xb.z * xb.z + xb.w * xb.w);
;         const float u[8] = {xa.x * L.g[0].x, xa.y * L.g[0].y, xa.z * L.g[0].z, xa.w * L.g[0].w, xb.x * L.g[1].x, xb.y * L.g[1].y, xb.z * L.g[1].z, xb.w * L.g[1].w};
;         unsigned hb[8]; float lo[8];
; #pragma unroll
;         for (int j = 0; j < 8; ++j) { hb[j] = f2bf(u[j]); lo[j] = u[j] - __builtin_bit_cast(float, hb[j] << 16); }
;         const u32x4 hw = (u32x4){hb[0] | (hb[1] << 16), hb[2] | (hb[3] << 16), hb[4] | (hb[5] << 16), hb[6] | (hb[7] << 16)};
;         const u32x4 lw = (u32x4){pk2(lo[0], lo[1]), pk2(lo[2], lo[3]), pk2(lo[4], lo[5]), pk2(lo[6], lo[7])};
;         ahi[mi] = __builtin_bit_cast(bf16x8, hw); alo[mi] = __builtin_bit_cast(bf16x8, lw); }
; #pragma unroll
;     for (int n = 0; n < 5; ++n)
; #pragma unroll
;         for (int mi = 0; mi < 2; ++mi) { acc[mi][n] = __builtin_amdgcn_mfma_f32_16x16x32_bf16(ahi[mi], W.wh[n], acc[mi][n], 0, 0, 0);
;             acc[mi][n] = __builtin_amdgcn_mfma_f32_16x16x32_bf16(alo[mi], W.wh[n], acc[mi][n], 0, 0, 0);
;             acc[mi][n] = __builtin_amdgcn_mfma_f32_16x16x32_bf16(ahi[mi], W.wl[n], acc[mi][n], 0, 0, 0); }
; __device__ __forceinline__ void p5_router(Frame& F) {
;     ...
;           RtLoad La, Lb; rt_load(La, h0, h1, gp, 0);
; #pragma unroll 1
;           for (int ks = 0; ks < 32; ks += 2) {
;               rt_load(Lb, h0, h1, gp, (ks + 1) * 32); rt_step(La, bh, bl, acc, ss, ks * 32);
;               if (ks + 2 < 32) rt_load(La, h0, h1, gp, (ks + 2) * 32);
;               rt_step(Lb, bh, bl, acc, ss, (ks + 1) * 32); }
	s_mov_b32 s33, s94
	s_mov_b32 s94, s95
	s_mov_b32 s95, s91
	s_mov_b32 s91, s25
	s_mov_b32 s25, s33
	s_add_i32 s39, s39, 0x80
	s_and_b32 s39, s39, 0x1fff
	s_add_u32 s40, s86, s39
	s_addc_u32 s41, s87, 0
	s_lshl_b32 s33, s39, 1
	s_add_u32 s44, s66, s33
	s_addc_u32 s45, s67, 0
	global_load_dwordx4 v[50:53], v216, s[44:45]
	global_load_dwordx4 v[54:57], v216, s[44:45] offset:16
	s_add_i32 m0, s94, s98
	s_nop 0
	global_load_lds_dwordx4 v208, s[40:41]
	s_add_i32 m0, s94, s99
	s_nop 0
	global_load_lds_dwordx4 v209, s[40:41]
	s_add_i32 m0, s94, s100
	s_nop 0
	global_load_lds_dwordx4 v210, s[40:41]
	v_add_u32_e32 v214, s95, v212
	v_add_u32_e32 v215, s95, v213
	ds_read_b128 v[38:41], v215
	ds_read_b128 v[58:61], v214 offset:0
	ds_read_b128 v[62:65], v214 offset:2048
	ds_read_b128 v[66:69], v214 offset:4096
	ds_read_b128 v[70:73], v214 offset:6144
	ds_read_b128 v[74:77], v214 offset:8192
	ds_read_b128 v[100:103], v214 offset:10240
	ds_read_b128 v[104:107], v214 offset:12288
	ds_read_b128 v[108:111], v214 offset:14336
	ds_read_b128 v[112:115], v214 offset:16384
	ds_read_b128 v[116:119], v214 offset:18432
	v_mfma_f32_16x16x32_bf16 v[18:21], v[158:161], v[230:233], v[18:21]
	v_mfma_f32_16x16x32_bf16 v[22:25], v[158:161], v[234:237], v[22:25]
	s_waitcnt lgkmcnt(10)
	v_lshlrev_b32_e32 v172, 16, v38
	v_and_b32_e32 v173, 0xffff0000, v38
	v_lshlrev_b32_e32 v174, 16, v39
	v_and_b32_e32 v175, 0xffff0000, v39
	v_mfma_f32_16x16x32_bf16 v[26:29], v[158:161], v[238:241], v[26:29]
	v_lshlrev_b32_e32 v176, 16, v40
	v_and_b32_e32 v177, 0xffff0000, v40
	v_lshlrev_b32_e32 v178, 16, v41
	v_and_b32_e32 v179, 0xffff0000, v41
	v_mfma_f32_16x16x32_bf16 v[30:33], v[158:161], v[242:245], v[30:33]
	v_mul_f32_e32 v180, v2, v172
	v_mul_f32_e32 v181, v3, v173
	v_mul_f32_e32 v182, v4, v174
	v_mul_f32_e32 v183, v5, v175
	v_mfma_f32_16x16x32_bf16 v[34:37], v[158:161], v[246:249], v[34:37]
	v_mul_f32_e32 v184, v6, v176
	v_mul_f32_e32 v185, v7, v177
	v_mul_f32_e32 v186, v8, v178
	v_mul_f32_e32 v187, v9, v179
	v_mfma_f32_16x16x32_bf16 v[18:21], v[162:165], v[230:233], v[18:21]
	v_cvt_pk_bf16_f32 v200, v180, v181
	v_cvt_pk_bf16_f32 v201, v182, v183
	v_cvt_pk_bf16_f32 v202, v184, v185
	v_cvt_pk_bf16_f32 v203, v186, v187
	v_mfma_f32_16x16x32_bf16 v[22:25], v[162:165], v[234:237], v[22:25]
	v_mul_f32_e32 v196, v172, v172
	v_mul_f32_e32 v197, v174, v174
	v_mul_f32_e32 v198, v176, v176
	v_mul_f32_e32 v199, v178, v178
	v_mfma_f32_16x16x32_bf16 v[26:29], v[162:165], v[238:241], v[26:29]
	v_fma_f32 v196, v173, v173, v196
	v_fma_f32 v197, v175, v175, v197
	v_fma_f32 v198, v177, v177, v198
	v_fma_f32 v199, v179, v179, v199
	v_mfma_f32_16x16x32_bf16 v[30:33], v[162:165], v[242:245], v[30:33]
	v_lshlrev_b32_e32 v188, 16, v200
	v_and_b32_e32 v189, 0xffff0000, v200
	v_lshlrev_b32_e32 v190, 16, v201
	v_and_b32_e32 v191, 0xffff0000, v201
	v_mfma_f32_16x16x32_bf16 v[34:37], v[162:165], v[246:249], v[34:37]
	v_lshlrev_b32_e32 v192, 16, v202
	v_and_b32_e32 v193, 0xffff0000, v202
	v_lshlrev_b32_e32 v194, 16, v203
	v_and_b32_e32 v195, 0xffff0000, v203
	v_mfma_f32_16x16x32_bf16 v[18:21], v[158:161], v[120:123], v[18:21]
	v_fma_f32 v180, v2, v172, -v188
	v_fma_f32 v181, v3, v173, -v189
	v_fma_f32 v182, v4, v174, -v190
	v_fma_f32 v183, v5, v175, -v191
	v_mfma_f32_16x16x32_bf16 v[22:25], v[158:161], v[124:127], v[22:25]
	v_fma_f32 v184, v6, v176, -v192
	v_fma_f32 v185, v7, v177, -v193
	v_fma_f32 v186, v8, v178, -v194
	v_fma_f32 v187, v9, v179, -v195
	v_mfma_f32_16x16x32_bf16 v[26:29], v[158:161], v[132:135], v[26:29]
	v_add_f32_e32 v196, v196, v197
	v_add_f32_e32 v196, v196, v198
	v_add_f32_e32 v196, v196, v199
	v_add_f32_e32 v224, v224, v196
	v_mfma_f32_16x16x32_bf16 v[30:33], v[158:161], v[136:139], v[30:33]
	v_cvt_pk_bf16_f32 v204, v180, v181
	v_cvt_pk_bf16_f32 v205, v182, v183
	v_cvt_pk_bf16_f32 v206, v184, v185
	v_cvt_pk_bf16_f32 v207, v186, v187
	v_mfma_f32_16x16x32_bf16 v[34:37], v[158:161], v[140:143], v[34:37]
	s_waitcnt vmcnt(10)
	s_waitcnt lgkmcnt(0)
	s_barrier
	s_mov_b32 s33, s94
	s_mov_b32 s94, s95
	s_mov_b32 s95, s91
	s_mov_b32 s91, s25
	s_mov_b32 s25, s33
	s_add_i32 s39, s39, 0x80
	s_and_b32 s39, s39, 0x1fff
	s_add_u32 s40, s86, s39
	s_addc_u32 s41, s87, 0
	s_lshl_b32 s33, s39, 1
	s_add_u32 s44, s66, s33
	s_addc_u32 s45, s67, 0
	global_load_dwordx4 v[2:5], v216, s[44:45]
	global_load_dwordx4 v[6:9], v216, s[44:45] offset:16
	s_add_i32 m0, s94, s98
	s_nop 0
	global_load_lds_dwordx4 v208, s[40:41]
	s_add_i32 m0, s94, s99
	s_nop 0
	global_load_lds_dwordx4 v209, s[40:41]
	s_add_i32 m0, s94, s100
	s_nop 0
	global_load_lds_dwordx4 v210, s[40:41]
	v_add_u32_e32 v214, s95, v212
	v_add_u32_e32 v215, s95, v213
	ds_read_b128 v[226:229], v215
	ds_read_b128 v[230:233], v214 offset:0
	ds_read_b128 v[234:237], v214 offset:2048
	ds_read_b128 v[238:241], v214 offset:4096
	ds_read_b128 v[242:245], v214 offset:6144
	ds_read_b128 v[246:249], v214 offset:8192
	ds_read_b128 v[120:123], v214 offset:10240
	ds_read_b128 v[124:127], v214 offset:12288
	ds_read_b128 v[132:135], v214 offset:14336
	ds_read_b128 v[136:139], v214 offset:16384
	ds_read_b128 v[140:143], v214 offset:18432
	v_mfma_f32_16x16x32_bf16 v[18:21], v[200:203], v[58:61], v[18:21]
	v_mfma_f32_16x16x32_bf16 v[22:25], v[200:203], v[62:65], v[22:25]
	s_waitcnt lgkmcnt(10)
; __device__ __forceinline__ unsigned f2bf(float f) { unsigned u = __builtin_bit_cast(unsigned, f); return (u + 0x7fffu + ((u >> 16) & 1u)) >> 16; }
; __device__ __forceinline__ void rt_step(const RtLoad& L, const bf16_t* bh, const bf16_t* bl, f32x4 (&acc)[2][5], float (&ss)[2], int ko) {
;     RtW W;
; #pragma unroll
;     for (int n = 0; n < 5; ++n) { W.wh[n] = *(const bf16x8*)(bh + (size_t)n * 16 * D + ko); W.wl[n] = *(const bf16x8*)(bl + (size_t)n * 16 * D + ko); }
;     bf16x8 ahi[2], alo[2];
; #pragma unroll
;     for (int mi = 0; mi < 2; ++mi) { const u32x4 xw = L.x[mi]; const f32x4 xa = (f32x4){bflo(xw.x), bfhi(xw.x), bflo(xw.y), bfhi(xw.y)}, xb = (f32x4){bflo(xw.z), bfhi(xw.z), bflo(xw.w), bfhi(xw.w)};
;         ss[mi] += (xa.x * xa.x + xa.y * xa.y) + (xa.z * xa.z + xa.w * xa.w) + (xb.x * xb.x + xb.y * xb.y) + (xb.z * xb.z + xb.w * xb.w);
;         const float u[8] = {xa.x * L.g[0].x, xa.y * L.g[0].y, xa.z * L.g[0].z, xa.w * L.g[0].w, xb.x * L.g[1].x, xb.y * L.g[1].y, xb.z * L.g[1].z, xb.w * L.g[1].w};
;         unsigned hb[8]; float lo[8];
; #pragma unroll
;         for (int j = 0; j < 8; ++j) { hb[j] = f2bf(u[j]); lo[j] = u[j] - __builtin_bit_cast(float, hb[j] << 16); }
;         const u32x4 hw = (u32x4){hb[0] | (hb[1] << 16), hb[2] | (hb[3] << 16), hb[4] | (hb[5] << 16), hb[6] | (hb[7] << 16)};
;         const u32x4 lw = (u32x4){pk2(lo[0], lo[1]), pk2(lo[2], lo[3]), pk2(lo[4], lo[5]), pk2(lo[6], lo[7])};
;         ahi[mi] = __builtin_bit_cast(bf16x8, hw); alo[mi] = __builtin_bit_cast(bf16x8, lw); }
; #pragma unroll
;     for (int n = 0; n < 5; ++n)
; #pragma unroll
;         for (int mi = 0; mi < 2; ++mi) { acc[mi][n] = __builtin_amdgcn_mfma_f32_16x16x32_bf16(ahi[mi], W.wh[n], acc[mi][n], 0, 0, 0);
;             acc[mi][n] = __builtin_amdgcn_mfma_f32_16x16x32_bf16(alo[mi], W.wh[n], acc[mi][n], 0, 0, 0);
;             acc[mi][n] = __builtin_amdgcn_mfma_f32_16x16x32_bf16(ahi[mi], W.wl[n], acc[mi][n], 0, 0, 0); }
; __device__ __forceinline__ void p5_router(Frame& F) {
;     ...
;           RtLoad La, Lb; rt_load(La, h0, h1, gp, 0);
; #pragma unroll 1
;           for (int ks = 0; ks < 32; ks += 2) {
;               rt_load(Lb, h0, h1, gp, (ks + 1) * 32); rt_step(La, bh, bl, acc, ss, ks * 32);
;               if (ks + 2 < 32) rt_load(La, h0, h1, gp, (ks + 2) * 32);
;               rt_step(Lb, bh, bl, acc, ss, (ks + 1) * 32); }
	v_lshlrev_b32_e32 v172, 16, v226
	v_and_b32_e32 v173, 0xffff0000, v226
	v_lshlrev_b32_e32 v174, 16, v227
	v_and_b32_e32 v175, 0xffff0000, v227
	v_mfma_f32_16x16x32_bf16 v[26:29], v[200:203], v[66:69], v[26:29]
	v_lshlrev_b32_e32 v176, 16, v228
	v_and_b32_e32 v177, 0xffff0000, v228
	v_lshlrev_b32_e32 v178, 16, v229
	v_and_b32_e32 v179, 0xffff0000, v229
	v_mfma_f32_16x16x32_bf16 v[30:33], v[200:203], v[70:73], v[30:33]
	v_mul_f32_e32 v180, v10, v172
	v_mul_f32_e32 v181, v11, v173
	v_mul_f32_e32 v182, v12, v174
	v_mul_f32_e32 v183, v13, v175
	v_mfma_f32_16x16x32_bf16 v[34:37], v[200:203], v[74:77], v[34:37]
	v_mul_f32_e32 v184, v14, v176
	v_mul_f32_e32 v185, v15, v177
	v_mul_f32_e32 v186, v16, v178
	v_mul_f32_e32 v187, v17, v179
	v_mfma_f32_16x16x32_bf16 v[18:21], v[204:207], v[58:61], v[18:21]
	v_cvt_pk_bf16_f32 v158, v180, v181
	v_cvt_pk_bf16_f32 v159, v182, v183
	v_cvt_pk_bf16_f32 v160, v184, v185
	v_cvt_pk_bf16_f32 v161, v186, v187
	v_mfma_f32_16x16x32_bf16 v[22:25], v[204:207], v[62:65], v[22:25]
	v_mul_f32_e32 v196, v172, v172
	v_mul_f32_e32 v197, v174, v174
	v_mul_f32_e32 v198, v176, v176
	v_mul_f32_e32 v199, v178, v178
	v_mfma_f32_16x16x32_bf16 v[26:29], v[204:207], v[66:69], v[26:29]
	v_fma_f32 v196, v173, v173, v196
	v_fma_f32 v197, v175, v175, v197
	v_fma_f32 v198, v177, v177, v198
	v_fma_f32 v199, v179, v179, v199
	v_mfma_f32_16x16x32_bf16 v[30:33], v[204:207], v[70:73], v[30:33]
	v_lshlrev_b32_e32 v188, 16, v158
	v_and_b32_e32 v189, 0xffff0000, v158
	v_lshlrev_b32_e32 v190, 16, v159
	v_and_b32_e32 v191, 0xffff0000, v159
	v_mfma_f32_16x16x32_bf16 v[34:37], v[204:207], v[74:77], v[34:37]
	v_lshlrev_b32_e32 v192, 16, v160
	v_and_b32_e32 v193, 0xffff0000, v160
	v_lshlrev_b32_e32 v194, 16, v161
	v_and_b32_e32 v195, 0xffff0000, v161
	v_mfma_f32_16x16x32_bf16 v[18:21], v[200:203], v[100:103], v[18:21]
	v_fma_f32 v180, v10, v172, -v188
	v_fma_f32 v181, v11, v173, -v189
	v_fma_f32 v182, v12, v174, -v190
	v_fma_f32 v183, v13, v175, -v191
	v_mfma_f32_16x16x32_bf16 v[22:25], v[200:203], v[104:107], v[22:25]
	v_fma_f32 v184, v14, v176, -v192
	v_fma_f32 v185, v15, v177, -v193
	v_fma_f32 v186, v16, v178, -v194
	v_fma_f32 v187, v17, v179, -v195
	v_mfma_f32_16x16x32_bf16 v[26:29], v[200:203], v[108:111], v[26:29]
	v_add_f32_e32 v196, v196, v197
	v_add_f32_e32 v196, v196, v198
	v_add_f32_e32 v196, v196, v199
	v_add_f32_e32 v224, v224, v196
	v_mfma_f32_16x16x32_bf16 v[30:33], v[200:203], v[112:115], v[30:33]
	v_cvt_pk_bf16_f32 v162, v180, v181
	v_cvt_pk_bf16_f32 v163, v182, v183
	v_cvt_pk_bf16_f32 v164, v184, v185
	v_cvt_pk_bf16_f32 v165, v186, v187
	v_mfma_f32_16x16x32_bf16 v[34:37], v[200:203], v[116:119], v[34:37]
	s_waitcnt vmcnt(10)
	s_waitcnt lgkmcnt(0)
	s_barrier
	s_mov_b32 s33, s94
	s_mov_b32 s94, s95
	s_mov_b32 s95, s91
	s_mov_b32 s91, s25
	s_mov_b32 s25, s33
	s_add_i32 s39, s39, 0x80
	s_and_b32 s39, s39, 0x1fff
	s_add_u32 s40, s86, s39
	s_addc_u32 s41, s87, 0
	s_lshl_b32 s33, s39, 1
	s_add_u32 s44, s66, s33
	s_addc_u32 s45, s67, 0
	global_load_dwordx4 v[10:13], v216, s[44:45]
	global_load_dwordx4 v[14:17], v216, s[44:45] offset:16
	s_add_i32 m0, s94, s98
	s_nop 0
	global_load_lds_dwordx4 v208, s[40:41]
	s_add_i32 m0, s94, s99
	s_nop 0
	global_load_lds_dwordx4 v209, s[40:41]
	s_add_i32 m0, s94, s100
	s_nop 0
	global_load_lds_dwordx4 v210, s[40:41]
	v_add_u32_e32 v214, s95, v212
	v_add_u32_e32 v215, s95, v213
	ds_read_b128 v[38:41], v215
	ds_read_b128 v[58:61], v214 offset:0
	ds_read_b128 v[62:65], v214 offset:2048
	ds_read_b128 v[66:69], v214 offset:4096
	ds_read_b128 v[70:73], v214 offset:6144
	ds_read_b128 v[74:77], v214 offset:8192
	ds_read_b128 v[100:103], v214 offset:10240
	ds_read_b128 v[104:107], v214 offset:12288
	ds_read_b128 v[108:111], v214 offset:14336
	ds_read_b128 v[112:115], v214 offset:16384
	ds_read_b128 v[116:119], v214 offset:18432
	v_mfma_f32_16x16x32_bf16 v[18:21], v[158:161], v[230:233], v[18:21]
	v_mfma_f32_16x16x32_bf16 v[22:25], v[158:161], v[234:237], v[22:25]
	s_waitcnt lgkmcnt(10)
	v_lshlrev_b32_e32 v172, 16, v38
	v_and_b32_e32 v173, 0xffff0000, v38
	v_lshlrev_b32_e32 v174, 16, v39
	v_and_b32_e32 v175, 0xffff0000, v39
	v_mfma_f32_16x16x32_bf16 v[26:29], v[158:161], v[238:241], v[26:29]
	v_lshlrev_b32_e32 v176, 16, v40
	v_and_b32_e32 v177, 0xffff0000, v40
	v_lshlrev_b32_e32 v178, 16, v41
	v_and_b32_e32 v179, 0xffff0000, v41
	v_mfma_f32_16x16x32_bf16 v[30:33], v[158:161], v[242:245], v[30:33]
	v_mul_f32_e32 v180, v42, v172
	v_mul_f32_e32 v181, v43, v173
	v_mul_f32_e32 v182, v44, v174
	v_mul_f32_e32 v183, v45, v175
	v_mfma_f32_16x16x32_bf16 v[34:37], v[158:161], v[246:249], v[34:37]
	v_mul_f32_e32 v184, v46, v176
	v_mul_f32_e32 v185, v47, v177
	v_mul_f32_e32 v186, v48, v178
	v_mul_f32_e32 v187, v49, v179
	v_mfma_f32_16x16x32_bf16 v[18:21], v[162:165], v[230:233], v[18:21]
	v_cvt_pk_bf16_f32 v200, v180, v181
	v_cvt_pk_bf16_f32 v201, v182, v183
	v_cvt_pk_bf16_f32 v202, v184, v185
	v_cvt_pk_bf16_f32 v203, v186, v187
	v_mfma_f32_16x16x32_bf16 v[22:25], v[162:165], v[234:237], v[22:25]
	v_mul_f32_e32 v196, v172, v172
	v_mul_f32_e32 v197, v174, v174
	v_mul_f32_e32 v198, v176, v176
	v_mul_f32_e32 v199, v178, v178
	v_mfma_f32_16x16x32_bf16 v[26:29], v[162:165], v[238:241], v[26:29]
	v_fma_f32 v196, v173, v173, v196
	v_fma_f32 v197, v175, v175, v197
	v_fma_f32 v198, v177, v177, v198
	v_fma_f32 v199, v179, v179, v199
	v_mfma_f32_16x16x32_bf16 v[30:33], v[162:165], v[242:245], v[30:33]
	v_lshlrev_b32_e32 v188, 16, v200
	v_and_b32_e32 v189, 0xffff0000, v200
	v_lshlrev_b32_e32 v190, 16, v201
	v_and_b32_e32 v191, 0xffff0000, v201
	v_mfma_f32_16x16x32_bf16 v[34:37], v[162:165], v[246:249], v[34:37]
	v_lshlrev_b32_e32 v192, 16, v202
	v_and_b32_e32 v193, 0xffff0000, v202
	v_lshlrev_b32_e32 v194, 16, v203
	v_and_b32_e32 v195, 0xffff0000, v203
	v_mfma_f32_16x16x32_bf16 v[18:21], v[158:161], v[120:123], v[18:21]
	v_fma_f32 v180, v42, v172, -v188
	v_fma_f32 v181, v43, v173, -v189
	v_fma_f32 v182, v44, v174, -v190
	v_fma_f32 v183, v45, v175, -v191
	v_mfma_f32_16x16x32_bf16 v[22:25], v[158:161], v[124:127], v[22:25]
	v_fma_f32 v184, v46, v176, -v192
	v_fma_f32 v185, v47, v177, -v193
	v_fma_f32 v186, v48, v178, -v194
	v_fma_f32 v187, v49, v179, -v195
	v_mfma_f32_16x16x32_bf16 v[26:29], v[158:161], v[132:135], v[26:29]
	v_add_f32_e32 v196, v196, v197
	v_add_f32_e32 v196, v196, v198
	v_add_f32_e32 v196, v196, v199
	v_add_f32_e32 v224, v224, v196
	v_mfma_f32_16x16x32_bf16 v[30:33], v[158:161], v[136:139], v[30:33]
	v_cvt_pk_bf16_f32 v204, v180, v181
	v_cvt_pk_bf16_f32 v205, v182, v183
	v_cvt_pk_bf16_f32 v206, v184, v185
	v_cvt_pk_bf16_f32 v207, v186, v187
	v_mfma_f32_16x16x32_bf16 v[34:37], v[158:161], v[140:143], v[34:37]
	s_waitcnt vmcnt(10)
	s_waitcnt lgkmcnt(0)
	s_barrier
	s_mov_b32 s33, s94
	s_mov_b32 s94, s95
	s_mov_b32 s95, s91
	s_mov_b32 s91, s25
	s_mov_b32 s25, s33
	s_mov_b32 s85, 13
; __device__ __forceinline__ unsigned f2bf(float f) { unsigned u = __builtin_bit_cast(unsigned, f); return (u + 0x7fffu + ((u >> 16) & 1u)) >> 16; }
; __device__ __forceinline__ void rt_step(const RtLoad& L, const bf16_t* bh, const bf16_t* bl, f32x4 (&acc)[2][5], float (&ss)[2], int ko) {
;     RtW W;
; #pragma unroll
;     for (int n = 0; n < 5; ++n) { W.wh[n] = *(const bf16x8*)(bh + (size_t)n * 16 * D + ko); W.wl[n] = *(const bf16x8*)(bl + (size_t)n * 16 * D + ko); }
;     bf16x8 ahi[2], alo[2];
; #pragma unroll
;     for (int mi = 0; mi < 2; ++mi) { const u32x4 xw = L.x[mi]; const f32x4 xa = (f32x4){bflo(xw.x), bfhi(xw.x), bflo(xw.y), bfhi(xw.y)}, xb = (f32x4){bflo(xw.z), bfhi(xw.z), bflo(xw.w), bfhi(xw.w)};
;         ss[mi] += (xa.x * xa.x + xa.y * xa.y) + (xa.z * xa.z + xa.w * xa.w) + (xb.x * xb.x + xb.y * xb.y) + (xb.z * xb.z + xb.w * xb.w);
;         const float u[8] = {xa.x * L.g[0].x, xa.y * L.g[0].y, xa.z * L.g[0].z, xa.w * L.g[0].w, xb.x * L.g[1].x, xb.y * L.g[1].y, xb.z * L.g[1].z, xb.w * L.g[1].w};
;         unsigned hb[8]; float lo[8];
; #pragma unroll
;         for (int j = 0; j < 8; ++j) { hb[j] = f2bf(u[j]); lo[j] = u[j] - __builtin_bit_cast(float, hb[j] << 16); }
;         const u32x4 hw = (u32x4){hb[0] | (hb[1] << 16), hb[2] | (hb[3] << 16), hb[4] | (hb[5] << 16), hb[6] | (hb[7] << 16)};
;         const u32x4 lw = (u32x4){pk2(lo[0], lo[1]), pk2(lo[2], lo[3]), pk2(lo[4], lo[5]), pk2(lo[6], lo[7])};
;         ahi[mi] = __builtin_bit_cast(bf16x8, hw); alo[mi] = __builtin_bit_cast(bf16x8, lw); }
; #pragma unroll
;     for (int n = 0; n < 5; ++n)
; #pragma unroll
;         for (int mi = 0; mi < 2; ++mi) { acc[mi][n] = __builtin_amdgcn_mfma_f32_16x16x32_bf16(ahi[mi], W.wh[n], acc[mi][n], 0, 0, 0);
;             acc[mi][n] = __builtin_amdgcn_mfma_f32_16x16x32_bf16(alo[mi], W.wh[n], acc[mi][n], 0, 0, 0);
;             acc[mi][n] = __builtin_amdgcn_mfma_f32_16x16x32_bf16(ahi[mi], W.wl[n], acc[mi][n], 0, 0, 0); }
; __device__ __forceinline__ void p5_router(Frame& F) {
;     ...
;           RtLoad La, Lb; rt_load(La, h0, h1, gp, 0);
; #pragma unroll 1
;           for (int ks = 0; ks < 32; ks += 2) {
;               rt_load(Lb, h0, h1, gp, (ks + 1) * 32); rt_step(La, bh, bl, acc, ss, ks * 32);
;               if (ks + 2 < 32) rt_load(La, h0, h1, gp, (ks + 2) * 32);
;               rt_step(Lb, bh, bl, acc, ss, (ks + 1) * 32); }
.Lrt_loop_p3:
	s_add_i32 s39, s39, 0x80
	s_and_b32 s39, s39, 0x1fff
	s_add_u32 s40, s86, s39
	s_addc_u32 s41, s87, 0
	s_lshl_b32 s33, s39, 1
	s_add_u32 s44, s66, s33
	s_addc_u32 s45, s67, 0
	global_load_dwordx4 v[42:45], v216, s[44:45]
	global_load_dwordx4 v[46:49], v216, s[44:45] offset:16
	s_add_i32 m0, s94, s98
	s_nop 0
	global_load_lds_dwordx4 v208, s[40:41]
	s_add_i32 m0, s94, s99
	s_nop 0
	global_load_lds_dwordx4 v209, s[40:41]
	s_add_i32 m0, s94, s100
	s_nop 0
	global_load_lds_dwordx4 v210, s[40:41]
	v_add_u32_e32 v214, s95, v212
	v_add_u32_e32 v215, s95, v213
	ds_read_b128 v[226:229], v215
	ds_read_b128 v[230:233], v214 offset:0
	ds_read_b128 v[234:237], v214 offset:2048
	ds_read_b128 v[238:241], v214 offset:4096
	ds_read_b128 v[242:245], v214 offset:6144
	ds_read_b128 v[246:249], v214 offset:8192
	ds_read_b128 v[120:123], v214 offset:10240
	ds_read_b128 v[124:127], v214 offset:12288
	ds_read_b128 v[132:135], v214 offset:14336
	ds_read_b128 v[136:139], v214 offset:16384
	ds_read_b128 v[140:143], v214 offset:18432
	v_mfma_f32_16x16x32_bf16 v[18:21], v[200:203], v[58:61], v[18:21]
	v_mfma_f32_16x16x32_bf16 v[22:25], v[200:203], v[62:65], v[22:25]
	s_waitcnt lgkmcnt(10)
	v_lshlrev_b32_e32 v172, 16, v226
	v_and_b32_e32 v173, 0xffff0000, v226
	v_lshlrev_b32_e32 v174, 16, v227
	v_and_b32_e32 v175, 0xffff0000, v227
	v_mfma_f32_16x16x32_bf16 v[26:29], v[200:203], v[66:69], v[26:29]
	v_lshlrev_b32_e32 v176, 16, v228
	v_and_b32_e32 v177, 0xffff0000, v228
	v_lshlrev_b32_e32 v178, 16, v229
	v_and_b32_e32 v179, 0xffff0000, v229
	v_mfma_f32_16x16x32_bf16 v[30:33], v[200:203], v[70:73], v[30:33]
	v_mul_f32_e32 v180, v50, v172
	v_mul_f32_e32 v181, v51, v173
	v_mul_f32_e32 v182, v52, v174
	v_mul_f32_e32 v183, v53, v175
	v_mfma_f32_16x16x32_bf16 v[34:37], v[200:203], v[74:77], v[34:37]
	v_mul_f32_e32 v184, v54, v176
	v_mul_f32_e32 v185, v55, v177
	v_mul_f32_e32 v186, v56, v178
	v_mul_f32_e32 v187, v57, v179
	v_mfma_f32_16x16x32_bf16 v[18:21], v[204:207], v[58:61], v[18:21]
	v_cvt_pk_bf16_f32 v158, v180, v181
	v_cvt_pk_bf16_f32 v159, v182, v183
	v_cvt_pk_bf16_f32 v160, v184, v185
	v_cvt_pk_bf16_f32 v161, v186, v187
	v_mfma_f32_16x16x32_bf16 v[22:25], v[204:207], v[62:65], v[22:25]
	v_mul_f32_e32 v196, v172, v172
	v_mul_f32_e32 v197, v174, v174
	v_mul_f32_e32 v198, v176, v176
	v_mul_f32_e32 v199, v178, v178
	v_mfma_f32_16x16x32_bf16 v[26:29], v[204:207], v[66:69], v[26:29]
	v_fma_f32 v196, v173, v173, v196
	v_fma_f32 v197, v175, v175, v197
	v_fma_f32 v198, v177, v177, v198
	v_fma_f32 v199, v179, v179, v199
	v_mfma_f32_16x16x32_bf16 v[30:33], v[204:207], v[70:73], v[30:33]
	v_lshlrev_b32_e32 v188, 16, v158
	v_and_b32_e32 v189, 0xffff0000, v158
	v_lshlrev_b32_e32 v190, 16, v159
	v_and_b32_e32 v191, 0xffff0000, v159
	v_mfma_f32_16x16x32_bf16 v[34:37], v[204:207], v[74:77], v[34:37]
	v_lshlrev_b32_e32 v192, 16, v160
	v_and_b32_e32 v193, 0xffff0000, v160
	v_lshlrev_b32_e32 v194, 16, v161
	v_and_b32_e32 v195, 0xffff0000, v161
	v_mfma_f32_16x16x32_bf16 v[18:21], v[200:203], v[100:103], v[18:21]
	v_fma_f32 v180, v50, v172, -v188
	v_fma_f32 v181, v51, v173, -v189
	v_fma_f32 v182, v52, v174, -v190
	v_fma_f32 v183, v53, v175, -v191
	v_mfma_f32_16x16x32_bf16 v[22:25], v[200:203], v[104:107], v[22:25]
	v_fma_f32 v184, v54, v176, -v192
	v_fma_f32 v185, v55, v177, -v193
	v_fma_f32 v186, v56, v178, -v194
	v_fma_f32 v187, v57, v179, -v195
	v_mfma_f32_16x16x32_bf16 v[26:29], v[200:203], v[108:111], v[26:29]
	v_add_f32_e32 v196, v196, v197
	v_add_f32_e32 v196, v196, v198
	v_add_f32_e32 v196, v196, v199
	v_add_f32_e32 v224, v224, v196
	v_mfma_f32_16x16x32_bf16 v[30:33], v[200:203], v[112:115], v[30:33]
	v_cvt_pk_bf16_f32 v162, v180, v181
	v_cvt_pk_bf16_f32 v163, v182, v183
	v_cvt_pk_bf16_f32 v164, v184, v185
	v_cvt_pk_bf16_f32 v165, v186, v187
	v_mfma_f32_16x16x32_bf16 v[34:37], v[200:203], v[116:119], v[34:37]
	s_waitcnt vmcnt(10)
	s_waitcnt lgkmcnt(0)
	s_barrier
	s_mov_b32 s33, s94
	s_mov_b32 s94, s95
	s_mov_b32 s95, s91
	s_mov_b32 s91, s25
	s_mov_b32 s25, s33
	s_add_i32 s39, s39, 0x80
	s_and_b32 s39, s39, 0x1fff
	s_add_u32 s40, s86, s39
	s_addc_u32 s41, s87, 0
	s_lshl_b32 s33, s39, 1
	s_add_u32 s44, s66, s33
	s_addc_u32 s45, s67, 0
	global_load_dwordx4 v[50:53], v216, s[44:45]
	global_load_dwordx4 v[54:57], v216, s[44:45] offset:16
	s_add_i32 m0, s94, s98
	s_nop 0
	global_load_lds_dwordx4 v208, s[40:41]
	s_add_i32 m0, s94, s99
	s_nop 0
	global_load_lds_dwordx4 v209, s[40:41]
	s_add_i32 m0, s94, s100
	s_nop 0
	global_load_lds_dwordx4 v210, s[40:41]
	v_add_u32_e32 v214, s95, v212
	v_add_u32_e32 v215, s95, v213
	ds_read_b128 v[38:41], v215
	ds_read_b128 v[58:61], v214 offset:0
	ds_read_b128 v[62:65], v214 offset:2048
	ds_read_b128 v[66:69], v214 offset:4096
	ds_read_b128 v[70:73], v214 offset:6144
	ds_read_b128 v[74:77], v214 offset:8192
	ds_read_b128 v[100:103], v214 offset:10240
	ds_read_b128 v[104:107], v214 offset:12288
	ds_read_b128 v[108:111], v214 offset:14336
	ds_read_b128 v[112:115], v214 offset:16384
	ds_read_b128 v[116:119], v214 offset:18432
	v_mfma_f32_16x16x32_bf16 v[18:21], v[158:161], v[230:233], v[18:21]
	v_mfma_f32_16x16x32_bf16 v[22:25], v[158:161], v[234:237], v[22:25]
	s_waitcnt lgkmcnt(10)
; __device__ __forceinline__ unsigned f2bf(float f) { unsigned u = __builtin_bit_cast(unsigned, f); return (u + 0x7fffu + ((u >> 16) & 1u)) >> 16; }
; __device__ __forceinline__ void rt_step(const RtLoad& L, const bf16_t* bh, const bf16_t* bl, f32x4 (&acc)[2][5], float (&ss)[2], int ko) {
;     RtW W;
; #pragma unroll
;     for (int n = 0; n < 5; ++n) { W.wh[n] = *(const bf16x8*)(bh + (size_t)n * 16 * D + ko); W.wl[n] = *(const bf16x8*)(bl + (size_t)n * 16 * D + ko); }
;     bf16x8 ahi[2], alo[2];
; #pragma unroll
;     for (int mi = 0; mi < 2; ++mi) { const u32x4 xw = L.x[mi]; const f32x4 xa = (f32x4){bflo(xw.x), bfhi(xw.x), bflo(xw.y), bfhi(xw.y)}, xb = (f32x4){bflo(xw.z), bfhi(xw.z), bflo(xw.w), bfhi(xw.w)};
;         ss[mi] += (xa.x * xa.x + xa.y * xa.y) + (xa.z * xa.z + xa.w * xa.w) + (xb.x * xb.x + xb.y * xb.y) + (xb.z * xb.z + xb.w * xb.w);
;         const float u[8] = {xa.x * L.g[0].x, xa.y * L.g[0].y, xa.z * L.g[0].z, xa.w * L.g[0].w, xb.x * L.g[1].x, xb.y * L.g[1].y, xb.z * L.g[1].z, xb.w * L.g[1].w};
;         unsigned hb[8]; float lo[8];
; #pragma unroll
;         for (int j = 0; j < 8; ++j) { hb[j] = f2bf(u[j]); lo[j] = u[j] - __builtin_bit_cast(float, hb[j] << 16); }
;         const u32x4 hw = (u32x4){hb[0] | (hb[1] << 16), hb[2] | (hb[3] << 16), hb[4] | (hb[5] << 16), hb[6] | (hb[7] << 16)};
;         const u32x4 lw = (u32x4){pk2(lo[0], lo[1]), pk2(lo[2], lo[3]), pk2(lo[4], lo[5]), pk2(lo[6], lo[7])};
;         ahi[mi] = __builtin_bit_cast(bf16x8, hw); alo[mi] = __builtin_bit_cast(bf16x8, lw); }
; #pragma unroll
;     for (int n = 0; n < 5; ++n)
; #pragma unroll
;         for (int mi = 0; mi < 2; ++mi) { acc[mi][n] = __builtin_amdgcn_mfma_f32_16x16x32_bf16(ahi[mi], W.wh[n], acc[mi][n], 0, 0, 0);
;             acc[mi][n] = __builtin_amdgcn_mfma_f32_16x16x32_bf16(alo[mi], W.wh[n], acc[mi][n], 0, 0, 0);
;             acc[mi][n] = __builtin_amdgcn_mfma_f32_16x16x32_bf16(ahi[mi], W.wl[n], acc[mi][n], 0, 0, 0); }
; __device__ __forceinline__ void p5_router(Frame& F) {
;     ...
;           RtLoad La, Lb; rt_load(La, h0, h1, gp, 0);
; #pragma unroll 1
;           for (int ks = 0; ks < 32; ks += 2) {
;               rt_load(Lb, h0, h1, gp, (ks + 1) * 32); rt_step(La, bh, bl, acc, ss, ks * 32);
;               if (ks + 2 < 32) rt_load(La, h0, h1, gp, (ks + 2) * 32);
;               rt_step(Lb, bh, bl, acc, ss, (ks + 1) * 32); }
	v_lshlrev_b32_e32 v172, 16, v38
	v_and_b32_e32 v173, 0xffff0000, v38
	v_lshlrev_b32_e32 v174, 16, v39
	v_and_b32_e32 v175, 0xffff0000, v39
	v_mfma_f32_16x16x32_bf16 v[26:29], v[158:161], v[238:241], v[26:29]
	v_lshlrev_b32_e32 v176, 16, v40
	v_and_b32_e32 v177, 0xffff0000, v40
	v_lshlrev_b32_e32 v178, 16, v41
	v_and_b32_e32 v179, 0xffff0000, v41
	v_mfma_f32_16x16x32_bf16 v[30:33], v[158:161], v[242:245], v[30:33]
	v_mul_f32_e32 v180, v2, v172
	v_mul_f32_e32 v181, v3, v173
	v_mul_f32_e32 v182, v4, v174
	v_mul_f32_e32 v183, v5, v175
	v_mfma_f32_16x16x32_bf16 v[34:37], v[158:161], v[246:249], v[34:37]
	v_mul_f32_e32 v184, v6, v176
	v_mul_f32_e32 v185, v7, v177
	v_mul_f32_e32 v186, v8, v178
	v_mul_f32_e32 v187, v9, v179
	v_mfma_f32_16x16x32_bf16 v[18:21], v[162:165], v[230:233], v[18:21]
	v_cvt_pk_bf16_f32 v200, v180, v181
	v_cvt_pk_bf16_f32 v201, v182, v183
	v_cvt_pk_bf16_f32 v202, v184, v185
	v_cvt_pk_bf16_f32 v203, v186, v187
	v_mfma_f32_16x16x32_bf16 v[22:25], v[162:165], v[234:237], v[22:25]
	v_mul_f32_e32 v196, v172, v172
	v_mul_f32_e32 v197, v174, v174
	v_mul_f32_e32 v198, v176, v176
	v_mul_f32_e32 v199, v178, v178
	v_mfma_f32_16x16x32_bf16 v[26:29], v[162:165], v[238:241], v[26:29]
	v_fma_f32 v196, v173, v173, v196
	v_fma_f32 v197, v175, v175, v197
	v_fma_f32 v198, v177, v177, v198
	v_fma_f32 v199, v179, v179, v199
	v_mfma_f32_16x16x32_bf16 v[30:33], v[162:165], v[242:245], v[30:33]
	v_lshlrev_b32_e32 v188, 16, v200
	v_and_b32_e32 v189, 0xffff0000, v200
	v_lshlrev_b32_e32 v190, 16, v201
	v_and_b32_e32 v191, 0xffff0000, v201
	v_mfma_f32_16x16x32_bf16 v[34:37], v[162:165], v[246:249], v[34:37]
	v_lshlrev_b32_e32 v192, 16, v202
	v_and_b32_e32 v193, 0xffff0000, v202
	v_lshlrev_b32_e32 v194, 16, v203
	v_and_b32_e32 v195, 0xffff0000, v203
	v_mfma_f32_16x16x32_bf16 v[18:21], v[158:161], v[120:123], v[18:21]
	v_fma_f32 v180, v2, v172, -v188
	v_fma_f32 v181, v3, v173, -v189
	v_fma_f32 v182, v4, v174, -v190
	v_fma_f32 v183, v5, v175, -v191
	v_mfma_f32_16x16x32_bf16 v[22:25], v[158:161], v[124:127], v[22:25]
	v_fma_f32 v184, v6, v176, -v192
	v_fma_f32 v185, v7, v177, -v193
	v_fma_f32 v186, v8, v178, -v194
	v_fma_f32 v187, v9, v179, -v195
	v_mfma_f32_16x16x32_bf16 v[26:29], v[158:161], v[132:135], v[26:29]
	v_add_f32_e32 v196, v196, v197
	v_add_f32_e32 v196, v196, v198
	v_add_f32_e32 v196, v196, v199
	v_add_f32_e32 v224, v224, v196
	v_mfma_f32_16x16x32_bf16 v[30:33], v[158:161], v[136:139], v[30:33]
	v_cvt_pk_bf16_f32 v204, v180, v181
	v_cvt_pk_bf16_f32 v205, v182, v183
	v_cvt_pk_bf16_f32 v206, v184, v185
	v_cvt_pk_bf16_f32 v207, v186, v187
	v_mfma_f32_16x16x32_bf16 v[34:37], v[158:161], v[140:143], v[34:37]
	s_waitcnt vmcnt(10)
	s_waitcnt lgkmcnt(0)
	s_barrier
	s_mov_b32 s33, s94
	s_mov_b32 s94, s95
	s_mov_b32 s95, s91
	s_mov_b32 s91, s25
	s_mov_b32 s25, s33
	s_add_i32 s39, s39, 0x80
	s_and_b32 s39, s39, 0x1fff
	s_add_u32 s40, s86, s39
	s_addc_u32 s41, s87, 0
	s_lshl_b32 s33, s39, 1
	s_add_u32 s44, s66, s33
	s_addc_u32 s45, s67, 0
	global_load_dwordx4 v[2:5], v216, s[44:45]
	global_load_dwordx4 v[6:9], v216, s[44:45] offset:16
	s_add_i32 m0, s94, s98
	s_nop 0
	global_load_lds_dwordx4 v208, s[40:41]
	s_add_i32 m0, s94, s99
	s_nop 0
	global_load_lds_dwordx4 v209, s[40:41]
	s_add_i32 m0, s94, s100
	s_nop 0
	global_load_lds_dwordx4 v210, s[40:41]
	v_add_u32_e32 v214, s95, v212
	v_add_u32_e32 v215, s95, v213
	ds_read_b128 v[226:229], v215
	ds_read_b128 v[230:233], v214 offset:0
	ds_read_b128 v[234:237], v214 offset:2048
	ds_read_b128 v[238:241], v214 offset:4096
	ds_read_b128 v[242:245], v214 offset:6144
	ds_read_b128 v[246:249], v214 offset:8192
	ds_read_b128 v[120:123], v214 offset:10240
	ds_read_b128 v[124:127], v214 offset:12288
	ds_read_b128 v[132:135], v214 offset:14336
	ds_read_b128 v[136:139], v214 offset:16384
	ds_read_b128 v[140:143], v214 offset:18432
	v_mfma_f32_16x16x32_bf16 v[18:21], v[200:203], v[58:61], v[18:21]
	v_mfma_f32_16x16x32_bf16 v[22:25], v[200:203], v[62:65], v[22:25]
	s_waitcnt lgkmcnt(10)
	v_lshlrev_b32_e32 v172, 16, v226
	v_and_b32_e32 v173, 0xffff0000, v226
	v_lshlrev_b32_e32 v174, 16, v227
	v_and_b32_e32 v175, 0xffff0000, v227
	v_mfma_f32_16x16x32_bf16 v[26:29], v[200:203], v[66:69], v[26:29]
	v_lshlrev_b32_e32 v176, 16, v228
	v_and_b32_e32 v177, 0xffff0000, v228
	v_lshlrev_b32_e32 v178, 16, v229
	v_and_b32_e32 v179, 0xffff0000, v229
	v_mfma_f32_16x16x32_bf16 v[30:33], v[200:203], v[70:73], v[30:33]
	v_mul_f32_e32 v180, v10, v172
	v_mul_f32_e32 v181, v11, v173
	v_mul_f32_e32 v182, v12, v174
	v_mul_f32_e32 v183, v13, v175
	v_mfma_f32_16x16x32_bf16 v[34:37], v[200:203], v[74:77], v[34:37]
	v_mul_f32_e32 v184, v14, v176
	v_mul_f32_e32 v185, v15, v177
	v_mul_f32_e32 v186, v16, v178
	v_mul_f32_e32 v187, v17, v179
	v_mfma_f32_16x16x32_bf16 v[18:21], v[204:207], v[58:61], v[18:21]
	v_cvt_pk_bf16_f32 v158, v180, v181
	v_cvt_pk_bf16_f32 v159, v182, v183
	v_cvt_pk_bf16_f32 v160, v184, v185
	v_cvt_pk_bf16_f32 v161, v186, v187
	v_mfma_f32_16x16x32_bf16 v[22:25], v[204:207], v[62:65], v[22:25]
	v_mul_f32_e32 v196, v172, v172
	v_mul_f32_e32 v197, v174, v174
	v_mul_f32_e32 v198, v176, v176
	v_mul_f32_e32 v199, v178, v178
	v_mfma_f32_16x16x32_bf16 v[26:29], v[204:207], v[66:69], v[26:29]
	v_fma_f32 v196, v173, v173, v196
	v_fma_f32 v197, v175, v175, v197
	v_fma_f32 v198, v177, v177, v198
	v_fma_f32 v199, v179, v179, v199
	v_mfma_f32_16x16x32_bf16 v[30:33], v[204:207], v[70:73], v[30:33]
	v_lshlrev_b32_e32 v188, 16, v158
	v_and_b32_e32 v189, 0xffff0000, v158
	v_lshlrev_b32_e32 v190, 16, v159
	v_and_b32_e32 v191, 0xffff0000, v159
	v_mfma_f32_16x16x32_bf16 v[34:37], v[204:207], v[74:77], v[34:37]
	v_lshlrev_b32_e32 v192, 16, v160
	v_and_b32_e32 v193, 0xffff0000, v160
	v_lshlrev_b32_e32 v194, 16, v161
	v_and_b32_e32 v195, 0xffff0000, v161
	v_mfma_f32_16x16x32_bf16 v[18:21], v[200:203], v[100:103], v[18:21]
	v_fma_f32 v180, v10, v172, -v188
	v_fma_f32 v181, v11, v173, -v189
	v_fma_f32 v182, v12, v174, -v190
	v_fma_f32 v183, v13, v175, -v191
	v_mfma_f32_16x16x32_bf16 v[22:25], v[200:203], v[104:107], v[22:25]
	v_fma_f32 v184, v14, v176, -v192
	v_fma_f32 v185, v15, v177, -v193
	v_fma_f32 v186, v16, v178, -v194
	v_fma_f32 v187, v17, v179, -v195
	v_mfma_f32_16x16x32_bf16 v[26:29], v[200:203], v[108:111], v[26:29]
	v_add_f32_e32 v196, v196, v197
	v_add_f32_e32 v196, v196, v198
	v_add_f32_e32 v196, v196, v199
	v_add_f32_e32 v224, v224, v196
	v_mfma_f32_16x16x32_bf16 v[30:33], v[200:203], v[112:115], v[30:33]
	v_cvt_pk_bf16_f32 v162, v180, v181
	v_cvt_pk_bf16_f32 v163, v182, v183
	v_cvt_pk_bf16_f32 v164, v184, v185
	v_cvt_pk_bf16_f32 v165, v186, v187
	v_mfma_f32_16x16x32_bf16 v[34:37], v[200:203], v[116:119], v[34:37]
	s_waitcnt vmcnt(10)
	s_waitcnt lgkmcnt(0)
	s_barrier
; __device__ __forceinline__ unsigned f2bf(float f) { unsigned u = __builtin_bit_cast(unsigned, f); return (u + 0x7fffu + ((u >> 16) & 1u)) >> 16; }
; __device__ __forceinline__ void rt_step(const RtLoad& L, const bf16_t* bh, const bf16_t* bl, f32x4 (&acc)[2][5], float (&ss)[2], int ko) {
;     RtW W;
; #pragma unroll
;     for (int n = 0; n < 5; ++n) { W.wh[n] = *(const bf16x8*)(bh + (size_t)n * 16 * D + ko); W.wl[n] = *(const bf16x8*)(bl + (size_t)n * 16 * D + ko); }
;     bf16x8 ahi[2], alo[2];
; #pragma unroll
;     for (int mi = 0; mi < 2; ++mi) { const u32x4 xw = L.x[mi]; const f32x4 xa = (f32x4){bflo(xw.x), bfhi(xw.x), bflo(xw.y), bfhi(xw.y)}, xb = (f32x4){bflo(xw.z), bfhi(xw.z), bflo(xw.w), bfhi(xw.w)};
;         ss[mi] += (xa.x * xa.x + xa.y * xa.y) + (xa.z * xa.z + xa.w * xa.w) + (xb.x * xb.x + xb.y * xb.y) + (xb.z * xb.z + xb.w * xb.w);
;         const float u[8] = {xa.x * L.g[0].x, xa.y * L.g[0].y, xa.z * L.g[0].z, xa.w * L.g[0].w, xb.x * L.g[1].x, xb.y * L.g[1].y, xb.z * L.g[1].z, xb.w * L.g[1].w};
;         unsigned hb[8]; float lo[8];
; #pragma unroll
;         for (int j = 0; j < 8; ++j) { hb[j] = f2bf(u[j]); lo[j] = u[j] - __builtin_bit_cast(float, hb[j] << 16); }
;         const u32x4 hw = (u32x4){hb[0] | (hb[1] << 16), hb[2] | (hb[3] << 16), hb[4] | (hb[5] << 16), hb[6] | (hb[7] << 16)};
;         const u32x4 lw = (u32x4){pk2(lo[0], lo[1]), pk2(lo[2], lo[3]), pk2(lo[4], lo[5]), pk2(lo[6], lo[7])};
;         ahi[mi] = __builtin_bit_cast(bf16x8, hw); alo[mi] = __builtin_bit_cast(bf16x8, lw); }
; #pragma unroll
;     for (int n = 0; n < 5; ++n)
; #pragma unroll
;         for (int mi = 0; mi < 2; ++mi) { acc[mi][n] = __builtin_amdgcn_mfma_f32_16x16x32_bf16(ahi[mi], W.wh[n], acc[mi][n], 0, 0, 0);
;             acc[mi][n] = __builtin_amdgcn_mfma_f32_16x16x32_bf16(alo[mi], W.wh[n], acc[mi][n], 0, 0, 0);
;             acc[mi][n] = __builtin_amdgcn_mfma_f32_16x16x32_bf16(ahi[mi], W.wl[n], acc[mi][n], 0, 0, 0); }
; __device__ __forceinline__ void p5_router(Frame& F) {
;     ...
;           RtLoad La, Lb; rt_load(La, h0, h1, gp, 0);
; #pragma unroll 1
;           for (int ks = 0; ks < 32; ks += 2) {
;               rt_load(Lb, h0, h1, gp, (ks + 1) * 32); rt_step(La, bh, bl, acc, ss, ks * 32);
;               if (ks + 2 < 32) rt_load(La, h0, h1, gp, (ks + 2) * 32);
;               rt_step(Lb, bh, bl, acc, ss, (ks + 1) * 32); }
	s_mov_b32 s33, s94
	s_mov_b32 s94, s95
	s_mov_b32 s95, s91
	s_mov_b32 s91, s25
	s_mov_b32 s25, s33
	s_add_i32 s39, s39, 0x80
	s_and_b32 s39, s39, 0x1fff
	s_add_u32 s40, s86, s39
	s_addc_u32 s41, s87, 0
	s_lshl_b32 s33, s39, 1
	s_add_u32 s44, s66, s33
	s_addc_u32 s45, s67, 0
	global_load_dwordx4 v[10:13], v216, s[44:45]
	global_load_dwordx4 v[14:17], v216, s[44:45] offset:16
	s_add_i32 m0, s94, s98
	s_nop 0
	global_load_lds_dwordx4 v208, s[40:41]
	s_add_i32 m0, s94, s99
	s_nop 0
	global_load_lds_dwordx4 v209, s[40:41]
	s_add_i32 m0, s94, s100
	s_nop 0
	global_load_lds_dwordx4 v210, s[40:41]
	v_add_u32_e32 v214, s95, v212
	v_add_u32_e32 v215, s95, v213
	ds_read_b128 v[38:41], v215
	ds_read_b128 v[58:61], v214 offset:0
	ds_read_b128 v[62:65], v214 offset:2048
	ds_read_b128 v[66:69], v214 offset:4096
	ds_read_b128 v[70:73], v214 offset:6144
	ds_read_b128 v[74:77], v214 offset:8192
	ds_read_b128 v[100:103], v214 offset:10240
	ds_read_b128 v[104:107], v214 offset:12288
	ds_read_b128 v[108:111], v214 offset:14336
	ds_read_b128 v[112:115], v214 offset:16384
	ds_read_b128 v[116:119], v214 offset:18432
	v_mfma_f32_16x16x32_bf16 v[18:21], v[158:161], v[230:233], v[18:21]
	v_mfma_f32_16x16x32_bf16 v[22:25], v[158:161], v[234:237], v[22:25]
	s_waitcnt lgkmcnt(10)
	v_lshlrev_b32_e32 v172, 16, v38
	v_and_b32_e32 v173, 0xffff0000, v38
	v_lshlrev_b32_e32 v174, 16, v39
	v_and_b32_e32 v175, 0xffff0000, v39
	v_mfma_f32_16x16x32_bf16 v[26:29], v[158:161], v[238:241], v[26:29]
	v_lshlrev_b32_e32 v176, 16, v40
	v_and_b32_e32 v177, 0xffff0000, v40
	v_lshlrev_b32_e32 v178, 16, v41
	v_and_b32_e32 v179, 0xffff0000, v41
	v_mfma_f32_16x16x32_bf16 v[30:33], v[158:161], v[242:245], v[30:33]
	v_mul_f32_e32 v180, v42, v172
	v_mul_f32_e32 v181, v43, v173
	v_mul_f32_e32 v182, v44, v174
	v_mul_f32_e32 v183, v45, v175
	v_mfma_f32_16x16x32_bf16 v[34:37], v[158:161], v[246:249], v[34:37]
	v_mul_f32_e32 v184, v46, v176
	v_mul_f32_e32 v185, v47, v177
	v_mul_f32_e32 v186, v48, v178
	v_mul_f32_e32 v187, v49, v179
	v_mfma_f32_16x16x32_bf16 v[18:21], v[162:165], v[230:233], v[18:21]
	v_cvt_pk_bf16_f32 v200, v180, v181
	v_cvt_pk_bf16_f32 v201, v182, v183
	v_cvt_pk_bf16_f32 v202, v184, v185
	v_cvt_pk_bf16_f32 v203, v186, v187
	v_mfma_f32_16x16x32_bf16 v[22:25], v[162:165], v[234:237], v[22:25]
	v_mul_f32_e32 v196, v172, v172
	v_mul_f32_e32 v197, v174, v174
	v_mul_f32_e32 v198, v176, v176
	v_mul_f32_e32 v199, v178, v178
	v_mfma_f32_16x16x32_bf16 v[26:29], v[162:165], v[238:241], v[26:29]
	v_fma_f32 v196, v173, v173, v196
	v_fma_f32 v197, v175, v175, v197
	v_fma_f32 v198, v177, v177, v198
	v_fma_f32 v199, v179, v179, v199
	v_mfma_f32_16x16x32_bf16 v[30:33], v[162:165], v[242:245], v[30:33]
	v_lshlrev_b32_e32 v188, 16, v200
	v_and_b32_e32 v189, 0xffff0000, v200
	v_lshlrev_b32_e32 v190, 16, v201
	v_and_b32_e32 v191, 0xffff0000, v201
	v_mfma_f32_16x16x32_bf16 v[34:37], v[162:165], v[246:249], v[34:37]
	v_lshlrev_b32_e32 v192, 16, v202
	v_and_b32_e32 v193, 0xffff0000, v202
	v_lshlrev_b32_e32 v194, 16, v203
	v_and_b32_e32 v195, 0xffff0000, v203
	v_mfma_f32_16x16x32_bf16 v[18:21], v[158:161], v[120:123], v[18:21]
	v_fma_f32 v180, v42, v172, -v188
	v_fma_f32 v181, v43, v173, -v189
	v_fma_f32 v182, v44, v174, -v190
	v_fma_f32 v183, v45, v175, -v191
	v_mfma_f32_16x16x32_bf16 v[22:25], v[158:161], v[124:127], v[22:25]
	v_fma_f32 v184, v46, v176, -v192
	v_fma_f32 v185, v47, v177, -v193
	v_fma_f32 v186, v48, v178, -v194
	v_fma_f32 v187, v49, v179, -v195
	v_mfma_f32_16x16x32_bf16 v[26:29], v[158:161], v[132:135], v[26:29]
	v_add_f32_e32 v196, v196, v197
	v_add_f32_e32 v196, v196, v198
	v_add_f32_e32 v196, v196, v199
	v_add_f32_e32 v224, v224, v196
	v_mfma_f32_16x16x32_bf16 v[30:33], v[158:161], v[136:139], v[30:33]
	v_cvt_pk_bf16_f32 v204, v180, v181
	v_cvt_pk_bf16_f32 v205, v182, v183
	v_cvt_pk_bf16_f32 v206, v184, v185
	v_cvt_pk_bf16_f32 v207, v186, v187
	v_mfma_f32_16x16x32_bf16 v[34:37], v[158:161], v[140:143], v[34:37]
	s_waitcnt vmcnt(10)
	s_waitcnt lgkmcnt(0)
	s_barrier
	s_mov_b32 s33, s94
	s_mov_b32 s94, s95
	s_mov_b32 s95, s91
	s_mov_b32 s91, s25
	s_mov_b32 s25, s33
	s_sub_u32 s85, s85, 1
	s_cmp_lg_u32 s85, 0
	s_cbranch_scc1 .Lrt_loop_p3
	s_add_i32 s39, s39, 0x80
	s_and_b32 s39, s39, 0x1fff
	s_add_u32 s40, s86, s39
	s_addc_u32 s41, s87, 0
	s_lshl_b32 s33, s39, 1
	s_add_u32 s44, s66, s33
	s_addc_u32 s45, s67, 0
	global_load_dwordx4 v[42:45], v216, s[44:45]
	global_load_dwordx4 v[46:49], v216, s[44:45] offset:16
	s_add_i32 m0, s94, s98
	s_nop 0
	global_load_lds_dwordx4 v208, s[40:41]
	s_add_i32 m0, s94, s99
	s_nop 0
	global_load_lds_dwordx4 v209, s[40:41]
	s_add_i32 m0, s94, s100
	s_nop 0
	global_load_lds_dwordx4 v210, s[40:41]
	v_add_u32_e32 v214, s95, v212
	v_add_u32_e32 v215, s95, v213
	ds_read_b128 v[226:229], v215
	ds_read_b128 v[230:233], v214 offset:0
	ds_read_b128 v[234:237], v214 offset:2048
	ds_read_b128 v[238:241], v214 offset:4096
	ds_read_b128 v[242:245], v214 offset:6144
	ds_read_b128 v[246:249], v214 offset:8192
	ds_read_b128 v[120:123], v214 offset:10240
	ds_read_b128 v[124:127], v214 offset:12288
	ds_read_b128 v[132:135], v214 offset:14336
	ds_read_b128 v[136:139], v214 offset:16384
	ds_read_b128 v[140:143], v214 offset:18432
	v_mfma_f32_16x16x32_bf16 v[18:21], v[200:203], v[58:61], v[18:21]
	v_mfma_f32_16x16x32_bf16 v[22:25], v[200:203], v[62:65], v[22:25]
	s_waitcnt lgkmcnt(10)
; __device__ __forceinline__ unsigned f2bf(float f) { unsigned u = __builtin_bit_cast(unsigned, f); return (u + 0x7fffu + ((u >> 16) & 1u)) >> 16; }
; __device__ __forceinline__ void rt_step(const RtLoad& L, const bf16_t* bh, const bf16_t* bl, f32x4 (&acc)[2][5], float (&ss)[2], int ko) {
;     RtW W;
; #pragma unroll
;     for (int n = 0; n < 5; ++n) { W.wh[n] = *(const bf16x8*)(bh + (size_t)n * 16 * D + ko); W.wl[n] = *(const bf16x8*)(bl + (size_t)n * 16 * D + ko); }
;     bf16x8 ahi[2], alo[2];
; #pragma unroll
;     for (int mi = 0; mi < 2; ++mi) { const u32x4 xw = L.x[mi]; const f32x4 xa = (f32x4){bflo(xw.x), bfhi(xw.x), bflo(xw.y), bfhi(xw.y)}, xb = (f32x4){bflo(xw.z), bfhi(xw.z), bflo(xw.w), bfhi(xw.w)};
;         ss[mi] += (xa.x * xa.x + xa.y * xa.y) + (xa.z * xa.z + xa.w * xa.w) + (xb.x * xb.x + xb.y * xb.y) + (xb.z * xb.z + xb.w * xb.w);
;         const float u[8] = {xa.x * L.g[0].x, xa.y * L.g[0].y, xa.z * L.g[0].z, xa.w * L.g[0].w, xb.x * L.g[1].x, xb.y * L.g[1].y, xb.z * L.g[1].z, xb.w * L.g[1].w};
;         unsigned hb[8]; float lo[8];
; #pragma unroll
;         for (int j = 0; j < 8; ++j) { hb[j] = f2bf(u[j]); lo[j] = u[j] - __builtin_bit_cast(float, hb[j] << 16); }
;         const u32x4 hw = (u32x4){hb[0] | (hb[1] << 16), hb[2] | (hb[3] << 16), hb[4] | (hb[5] << 16), hb[6] | (hb[7] << 16)};
;         const u32x4 lw = (u32x4){pk2(lo[0], lo[1]), pk2(lo[2], lo[3]), pk2(lo[4], lo[5]), pk2(lo[6], lo[7])};
;         ahi[mi] = __builtin_bit_cast(bf16x8, hw); alo[mi] = __builtin_bit_cast(bf16x8, lw); }
; #pragma unroll
;     for (int n = 0; n < 5; ++n)
; #pragma unroll
;         for (int mi = 0; mi < 2; ++mi) { acc[mi][n] = __builtin_amdgcn_mfma_f32_16x16x32_bf16(ahi[mi], W.wh[n], acc[mi][n], 0, 0, 0);
;             acc[mi][n] = __builtin_amdgcn_mfma_f32_16x16x32_bf16(alo[mi], W.wh[n], acc[mi][n], 0, 0, 0);
;             acc[mi][n] = __builtin_amdgcn_mfma_f32_16x16x32_bf16(ahi[mi], W.wl[n], acc[mi][n], 0, 0, 0); }
; __device__ __forceinline__ void p5_router(Frame& F) {
;     ...
;           RtLoad La, Lb; rt_load(La, h0, h1, gp, 0);
; #pragma unroll 1
;           for (int ks = 0; ks < 32; ks += 2) {
;               rt_load(Lb, h0, h1, gp, (ks + 1) * 32); rt_step(La, bh, bl, acc, ss, ks * 32);
;               if (ks + 2 < 32) rt_load(La, h0, h1, gp, (ks + 2) * 32);
;               rt_step(Lb, bh, bl, acc, ss, (ks + 1) * 32); }
	v_lshlrev_b32_e32 v172, 16, v226
	v_and_b32_e32 v173, 0xffff0000, v226
	v_lshlrev_b32_e32 v174, 16, v227
	v_and_b32_e32 v175, 0xffff0000, v227
	v_mfma_f32_16x16x32_bf16 v[26:29], v[200:203], v[66:69], v[26:29]
	v_lshlrev_b32_e32 v176, 16, v228
	v_and_b32_e32 v177, 0xffff0000, v228
	v_lshlrev_b32_e32 v178, 16, v229
	v_and_b32_e32 v179, 0xffff0000, v229
	v_mfma_f32_16x16x32_bf16 v[30:33], v[200:203], v[70:73], v[30:33]
	v_mul_f32_e32 v180, v50, v172
	v_mul_f32_e32 v181, v51, v173
	v_mul_f32_e32 v182, v52, v174
	v_mul_f32_e32 v183, v53, v175
	v_mfma_f32_16x16x32_bf16 v[34:37], v[200:203], v[74:77], v[34:37]
	v_mul_f32_e32 v184, v54, v176
	v_mul_f32_e32 v185, v55, v177
	v_mul_f32_e32 v186, v56, v178
	v_mul_f32_e32 v187, v57, v179
	v_mfma_f32_16x16x32_bf16 v[18:21], v[204:207], v[58:61], v[18:21]
	v_cvt_pk_bf16_f32 v158, v180, v181
	v_cvt_pk_bf16_f32 v159, v182, v183
	v_cvt_pk_bf16_f32 v160, v184, v185
	v_cvt_pk_bf16_f32 v161, v186, v187
	v_mfma_f32_16x16x32_bf16 v[22:25], v[204:207], v[62:65], v[22:25]
	v_mul_f32_e32 v196, v172, v172
	v_mul_f32_e32 v197, v174, v174
	v_mul_f32_e32 v198, v176, v176
	v_mul_f32_e32 v199, v178, v178
	v_mfma_f32_16x16x32_bf16 v[26:29], v[204:207], v[66:69], v[26:29]
	v_fma_f32 v196, v173, v173, v196
	v_fma_f32 v197, v175, v175, v197
	v_fma_f32 v198, v177, v177, v198
	v_fma_f32 v199, v179, v179, v199
	v_mfma_f32_16x16x32_bf16 v[30:33], v[204:207], v[70:73], v[30:33]
	v_lshlrev_b32_e32 v188, 16, v158
	v_and_b32_e32 v189, 0xffff0000, v158
	v_lshlrev_b32_e32 v190, 16, v159
	v_and_b32_e32 v191, 0xffff0000, v159
	v_mfma_f32_16x16x32_bf16 v[34:37], v[204:207], v[74:77], v[34:37]
	v_lshlrev_b32_e32 v192, 16, v160
	v_and_b32_e32 v193, 0xffff0000, v160
	v_lshlrev_b32_e32 v194, 16, v161
	v_and_b32_e32 v195, 0xffff0000, v161
	v_mfma_f32_16x16x32_bf16 v[18:21], v[200:203], v[100:103], v[18:21]
	v_fma_f32 v180, v50, v172, -v188
	v_fma_f32 v181, v51, v173, -v189
	v_fma_f32 v182, v52, v174, -v190
	v_fma_f32 v183, v53, v175, -v191
	v_mfma_f32_16x16x32_bf16 v[22:25], v[200:203], v[104:107], v[22:25]
	v_fma_f32 v184, v54, v176, -v192
	v_fma_f32 v185, v55, v177, -v193
	v_fma_f32 v186, v56, v178, -v194
	v_fma_f32 v187, v57, v179, -v195
	v_mfma_f32_16x16x32_bf16 v[26:29], v[200:203], v[108:111], v[26:29]
	v_add_f32_e32 v196, v196, v197
	v_add_f32_e32 v196, v196, v198
	v_add_f32_e32 v196, v196, v199
	v_add_f32_e32 v224, v224, v196
	v_mfma_f32_16x16x32_bf16 v[30:33], v[200:203], v[112:115], v[30:33]
	v_cvt_pk_bf16_f32 v162, v180, v181
	v_cvt_pk_bf16_f32 v163, v182, v183
	v_cvt_pk_bf16_f32 v164, v184, v185
	v_cvt_pk_bf16_f32 v165, v186, v187
	v_mfma_f32_16x16x32_bf16 v[34:37], v[200:203], v[116:119], v[34:37]
	s_waitcnt vmcnt(10)
	s_waitcnt lgkmcnt(0)
	s_barrier
	s_mov_b32 s33, s94
	s_mov_b32 s94, s95
	s_mov_b32 s95, s91
	s_mov_b32 s91, s25
	s_mov_b32 s25, s33
	s_add_i32 s39, s39, 0x80
	s_and_b32 s39, s39, 0x1fff
	s_add_u32 s40, s86, s39
	s_addc_u32 s41, s87, 0
	s_lshl_b32 s33, s39, 1
	s_add_u32 s44, s66, s33
	s_addc_u32 s45, s67, 0
	global_load_dwordx4 v[50:53], v216, s[44:45]
	global_load_dwordx4 v[54:57], v216, s[44:45] offset:16
	s_add_i32 m0, s94, s98
	s_nop 0
	global_load_lds_dwordx4 v208, s[40:41]
	s_add_i32 m0, s94, s99
	s_nop 0
	global_load_lds_dwordx4 v209, s[40:41]
	s_add_i32 m0, s94, s100
	s_nop 0
	global_load_lds_dwordx4 v210, s[40:41]
	v_add_u32_e32 v214, s95, v212
	v_add_u32_e32 v215, s95, v213
	ds_read_b128 v[38:41], v215
	ds_read_b128 v[58:61], v214 offset:0
	ds_read_b128 v[62:65], v214 offset:2048
	ds_read_b128 v[66:69], v214 offset:4096
	ds_read_b128 v[70:73], v214 offset:6144
	ds_read_b128 v[74:77], v214 offset:8192
	ds_read_b128 v[100:103], v214 offset:10240
	ds_read_b128 v[104:107], v214 offset:12288
	ds_read_b128 v[108:111], v214 offset:14336
	ds_read_b128 v[112:115], v214 offset:16384
	ds_read_b128 v[116:119], v214 offset:18432
	v_mfma_f32_16x16x32_bf16 v[18:21], v[158:161], v[230:233], v[18:21]
	v_mfma_f32_16x16x32_bf16 v[22:25], v[158:161], v[234:237], v[22:25]
	s_waitcnt lgkmcnt(10)
	v_lshlrev_b32_e32 v172, 16, v38
	v_and_b32_e32 v173, 0xffff0000, v38
	v_lshlrev_b32_e32 v174, 16, v39
	v_and_b32_e32 v175, 0xffff0000, v39
	v_mfma_f32_16x16x32_bf16 v[26:29], v[158:161], v[238:241], v[26:29]
	v_lshlrev_b32_e32 v176, 16, v40
	v_and_b32_e32 v177, 0xffff0000, v40
	v_lshlrev_b32_e32 v178, 16, v41
	v_and_b32_e32 v179, 0xffff0000, v41
	v_mfma_f32_16x16x32_bf16 v[30:33], v[158:161], v[242:245], v[30:33]
	v_mul_f32_e32 v180, v2, v172
	v_mul_f32_e32 v181, v3, v173
	v_mul_f32_e32 v182, v4, v174
	v_mul_f32_e32 v183, v5, v175
	v_mfma_f32_16x16x32_bf16 v[34:37], v[158:161], v[246:249], v[34:37]
	v_mul_f32_e32 v184, v6, v176
	v_mul_f32_e32 v185, v7, v177
	v_mul_f32_e32 v186, v8, v178
	v_mul_f32_e32 v187, v9, v179
	v_mfma_f32_16x16x32_bf16 v[18:21], v[162:165], v[230:233], v[18:21]
	v_cvt_pk_bf16_f32 v200, v180, v181
	v_cvt_pk_bf16_f32 v201, v182, v183
	v_cvt_pk_bf16_f32 v202, v184, v185
	v_cvt_pk_bf16_f32 v203, v186, v187
	v_mfma_f32_16x16x32_bf16 v[22:25], v[162:165], v[234:237], v[22:25]
	v_mul_f32_e32 v196, v172, v172
	v_mul_f32_e32 v197, v174, v174
	v_mul_f32_e32 v198, v176, v176
	v_mul_f32_e32 v199, v178, v178
	v_mfma_f32_16x16x32_bf16 v[26:29], v[162:165], v[238:241], v[26:29]
	v_fma_f32 v196, v173, v173, v196
	v_fma_f32 v197, v175, v175, v197
	v_fma_f32 v198, v177, v177, v198
	v_fma_f32 v199, v179, v179, v199
	v_mfma_f32_16x16x32_bf16 v[30:33], v[162:165], v[242:245], v[30:33]
	v_lshlrev_b32_e32 v188, 16, v200
	v_and_b32_e32 v189, 0xffff0000, v200
	v_lshlrev_b32_e32 v190, 16, v201
	v_and_b32_e32 v191, 0xffff0000, v201
	v_mfma_f32_16x16x32_bf16 v[34:37], v[162:165], v[246:249], v[34:37]
	v_lshlrev_b32_e32 v192, 16, v202
	v_and_b32_e32 v193, 0xffff0000, v202
	v_lshlrev_b32_e32 v194, 16, v203
	v_and_b32_e32 v195, 0xffff0000, v203
	v_mfma_f32_16x16x32_bf16 v[18:21], v[158:161], v[120:123], v[18:21]
	v_fma_f32 v180, v2, v172, -v188
	v_fma_f32 v181, v3, v173, -v189
	v_fma_f32 v182, v4, v174, -v190
	v_fma_f32 v183, v5, v175, -v191
	v_mfma_f32_16x16x32_bf16 v[22:25], v[158:161], v[124:127], v[22:25]
	v_fma_f32 v184, v6, v176, -v192
	v_fma_f32 v185, v7, v177, -v193
	v_fma_f32 v186, v8, v178, -v194
	v_fma_f32 v187, v9, v179, -v195
	v_mfma_f32_16x16x32_bf16 v[26:29], v[158:161], v[132:135], v[26:29]
	v_add_f32_e32 v196, v196, v197
	v_add_f32_e32 v196, v196, v198
	v_add_f32_e32 v196, v196, v199
	v_add_f32_e32 v224, v224, v196
	v_mfma_f32_16x16x32_bf16 v[30:33], v[158:161], v[136:139], v[30:33]
	v_cvt_pk_bf16_f32 v204, v180, v181
	v_cvt_pk_bf16_f32 v205, v182, v183
	v_cvt_pk_bf16_f32 v206, v184, v185
	v_cvt_pk_bf16_f32 v207, v186, v187
	v_mfma_f32_16x16x32_bf16 v[34:37], v[158:161], v[140:143], v[34:37]
	s_waitcnt vmcnt(10)
	s_waitcnt lgkmcnt(0)
	s_barrier
; __device__ __forceinline__ unsigned f2bf(float f) { unsigned u = __builtin_bit_cast(unsigned, f); return (u + 0x7fffu + ((u >> 16) & 1u)) >> 16; }
; __device__ __forceinline__ void rt_step(const RtLoad& L, const bf16_t* bh, const bf16_t* bl, f32x4 (&acc)[2][5], float (&ss)[2], int ko) {
;     RtW W;
; #pragma unroll
;     for (int n = 0; n < 5; ++n) { W.wh[n] = *(const bf16x8*)(bh + (size_t)n * 16 * D + ko); W.wl[n] = *(const bf16x8*)(bl + (size_t)n * 16 * D + ko); }
;     bf16x8 ahi[2], alo[2];
; #pragma unroll
;     for (int mi = 0; mi < 2; ++mi) { const u32x4 xw = L.x[mi]; const f32x4 xa = (f32x4){bflo(xw.x), bfhi(xw.x), bflo(xw.y), bfhi(xw.y)}, xb = (f32x4){bflo(xw.z), bfhi(xw.z), bflo(xw.w), bfhi(xw.w)};
;         ss[mi] += (xa.x * xa.x + xa.y * xa.y) + (xa.z * xa.z + xa.w * xa.w) + (xb.x * xb.x + xb.y * xb.y) + (xb.z * xb.z + xb.w * xb.w);
;         const float u[8] = {xa.x * L.g[0].x, xa.y * L.g[0].y, xa.z * L.g[0].z, xa.w * L.g[0].w, xb.x * L.g[1].x, xb.y * L.g[1].y, xb.z * L.g[1].z, xb.w * L.g[1].w};
;         unsigned hb[8]; float lo[8];
; #pragma unroll
;         for (int j = 0; j < 8; ++j) { hb[j] = f2bf(u[j]); lo[j] = u[j] - __builtin_bit_cast(float, hb[j] << 16); }
;         const u32x4 hw = (u32x4){hb[0] | (hb[1] << 16), hb[2] | (hb[3] << 16), hb[4] | (hb[5] << 16), hb[6] | (hb[7] << 16)};
;         const u32x4 lw = (u32x4){pk2(lo[0], lo[1]), pk2(lo[2], lo[3]), pk2(lo[4], lo[5]), pk2(lo[6], lo[7])};
;         ahi[mi] = __builtin_bit_cast(bf16x8, hw); alo[mi] = __builtin_bit_cast(bf16x8, lw); }
; #pragma unroll
;     for (int n = 0; n < 5; ++n)
; #pragma unroll
;         for (int mi = 0; mi < 2; ++mi) { acc[mi][n] = __builtin_amdgcn_mfma_f32_16x16x32_bf16(ahi[mi], W.wh[n], acc[mi][n], 0, 0, 0);
;             acc[mi][n] = __builtin_amdgcn_mfma_f32_16x16x32_bf16(alo[mi], W.wh[n], acc[mi][n], 0, 0, 0);
;             acc[mi][n] = __builtin_amdgcn_mfma_f32_16x16x32_bf16(ahi[mi], W.wl[n], acc[mi][n], 0, 0, 0); }
; __device__ __forceinline__ void p5_router(Frame& F) {
;     ...
;           RtLoad La, Lb; rt_load(La, h0, h1, gp, 0);
; #pragma unroll 1
;           for (int ks = 0; ks < 32; ks += 2) {
;               rt_load(Lb, h0, h1, gp, (ks + 1) * 32); rt_step(La, bh, bl, acc, ss, ks * 32);
;               if (ks + 2 < 32) rt_load(La, h0, h1, gp, (ks + 2) * 32);
;               rt_step(Lb, bh, bl, acc, ss, (ks + 1) * 32); }
	s_mov_b32 s33, s94
	s_mov_b32 s94, s95
	s_mov_b32 s95, s91
	s_mov_b32 s91, s25
	s_mov_b32 s25, s33
	s_add_i32 s39, s39, 0x80
	s_and_b32 s39, s39, 0x1fff
	s_add_u32 s40, s86, s39
	s_addc_u32 s41, s87, 0
	s_lshl_b32 s33, s39, 1
	s_add_u32 s44, s66, s33
	s_addc_u32 s45, s67, 0
	global_load_dwordx4 v[2:5], v216, s[44:45]
	global_load_dwordx4 v[6:9], v216, s[44:45] offset:16
	s_add_i32 m0, s94, s98
	s_nop 0
	global_load_lds_dwordx4 v208, s[40:41]
	s_add_i32 m0, s94, s99
	s_nop 0
	global_load_lds_dwordx4 v209, s[40:41]
	s_add_i32 m0, s94, s100
	s_nop 0
	global_load_lds_dwordx4 v210, s[40:41]
	v_add_u32_e32 v214, s95, v212
	v_add_u32_e32 v215, s95, v213
	ds_read_b128 v[226:229], v215
	ds_read_b128 v[230:233], v214 offset:0
	ds_read_b128 v[234:237], v214 offset:2048
	ds_read_b128 v[238:241], v214 offset:4096
	ds_read_b128 v[242:245], v214 offset:6144
	ds_read_b128 v[246:249], v214 offset:8192
	ds_read_b128 v[120:123], v214 offset:10240
	ds_read_b128 v[124:127], v214 offset:12288
	ds_read_b128 v[132:135], v214 offset:14336
	ds_read_b128 v[136:139], v214 offset:16384
	ds_read_b128 v[140:143], v214 offset:18432
	v_mfma_f32_16x16x32_bf16 v[18:21], v[200:203], v[58:61], v[18:21]
	v_mfma_f32_16x16x32_bf16 v[22:25], v[200:203], v[62:65], v[22:25]
	s_waitcnt lgkmcnt(10)
	v_lshlrev_b32_e32 v172, 16, v226
	v_and_b32_e32 v173, 0xffff0000, v226
	v_lshlrev_b32_e32 v174, 16, v227
	v_and_b32_e32 v175, 0xffff0000, v227
	v_mfma_f32_16x16x32_bf16 v[26:29], v[200:203], v[66:69], v[26:29]
	v_lshlrev_b32_e32 v176, 16, v228
	v_and_b32_e32 v177, 0xffff0000, v228
	v_lshlrev_b32_e32 v178, 16, v229
	v_and_b32_e32 v179, 0xffff0000, v229
	v_mfma_f32_16x16x32_bf16 v[30:33], v[200:203], v[70:73], v[30:33]
	v_mul_f32_e32 v180, v10, v172
	v_mul_f32_e32 v181, v11, v173
	v_mul_f32_e32 v182, v12, v174
	v_mul_f32_e32 v183, v13, v175
	v_mfma_f32_16x16x32_bf16 v[34:37], v[200:203], v[74:77], v[34:37]
	v_mul_f32_e32 v184, v14, v176
	v_mul_f32_e32 v185, v15, v177
	v_mul_f32_e32 v186, v16, v178
	v_mul_f32_e32 v187, v17, v179
	v_mfma_f32_16x16x32_bf16 v[18:21], v[204:207], v[58:61], v[18:21]
	v_cvt_pk_bf16_f32 v158, v180, v181
	v_cvt_pk_bf16_f32 v159, v182, v183
	v_cvt_pk_bf16_f32 v160, v184, v185
	v_cvt_pk_bf16_f32 v161, v186, v187
	v_mfma_f32_16x16x32_bf16 v[22:25], v[204:207], v[62:65], v[22:25]
	v_mul_f32_e32 v196, v172, v172
	v_mul_f32_e32 v197, v174, v174
	v_mul_f32_e32 v198, v176, v176
	v_mul_f32_e32 v199, v178, v178
	v_mfma_f32_16x16x32_bf16 v[26:29], v[204:207], v[66:69], v[26:29]
	v_fma_f32 v196, v173, v173, v196
	v_fma_f32 v197, v175, v175, v197
	v_fma_f32 v198, v177, v177, v198
	v_fma_f32 v199, v179, v179, v199
	v_mfma_f32_16x16x32_bf16 v[30:33], v[204:207], v[70:73], v[30:33]
	v_lshlrev_b32_e32 v188, 16, v158
	v_and_b32_e32 v189, 0xffff0000, v158
	v_lshlrev_b32_e32 v190, 16, v159
	v_and_b32_e32 v191, 0xffff0000, v159
	v_mfma_f32_16x16x32_bf16 v[34:37], v[204:207], v[74:77], v[34:37]
	v_lshlrev_b32_e32 v192, 16, v160
	v_and_b32_e32 v193, 0xffff0000, v160
	v_lshlrev_b32_e32 v194, 16, v161
	v_and_b32_e32 v195, 0xffff0000, v161
	v_mfma_f32_16x16x32_bf16 v[18:21], v[200:203], v[100:103], v[18:21]
	v_fma_f32 v180, v10, v172, -v188
	v_fma_f32 v181, v11, v173, -v189
	v_fma_f32 v182, v12, v174, -v190
	v_fma_f32 v183, v13, v175, -v191
	v_mfma_f32_16x16x32_bf16 v[22:25], v[200:203], v[104:107], v[22:25]
	v_fma_f32 v184, v14, v176, -v192
	v_fma_f32 v185, v15, v177, -v193
	v_fma_f32 v186, v16, v178, -v194
	v_fma_f32 v187, v17, v179, -v195
	v_mfma_f32_16x16x32_bf16 v[26:29], v[200:203], v[108:111], v[26:29]
	v_add_f32_e32 v196, v196, v197
	v_add_f32_e32 v196, v196, v198
	v_add_f32_e32 v196, v196, v199
	v_add_f32_e32 v224, v224, v196
	v_mfma_f32_16x16x32_bf16 v[30:33], v[200:203], v[112:115], v[30:33]
	v_cvt_pk_bf16_f32 v162, v180, v181
	v_cvt_pk_bf16_f32 v163, v182, v183
	v_cvt_pk_bf16_f32 v164, v184, v185
	v_cvt_pk_bf16_f32 v165, v186, v187
	v_mfma_f32_16x16x32_bf16 v[34:37], v[200:203], v[116:119], v[34:37]
	s_waitcnt vmcnt(10)
	s_waitcnt lgkmcnt(0)
	s_barrier
	s_mov_b32 s33, s94
	s_mov_b32 s94, s95
	s_mov_b32 s95, s91
	s_mov_b32 s91, s25
	s_mov_b32 s25, s33
	s_add_i32 s39, s39, 0x80
	s_and_b32 s39, s39, 0x1fff
	s_add_u32 s40, s86, s39
	s_addc_u32 s41, s87, 0
	s_lshl_b32 s33, s39, 1
	s_add_u32 s44, s66, s33
	s_addc_u32 s45, s67, 0
	global_load_dwordx4 v[10:13], v216, s[44:45]
	global_load_dwordx4 v[14:17], v216, s[44:45] offset:16
	s_add_i32 m0, s94, s98
	s_nop 0
	global_load_lds_dwordx4 v208, s[40:41]
	s_add_i32 m0, s94, s99
	s_nop 0
	global_load_lds_dwordx4 v209, s[40:41]
	s_add_i32 m0, s94, s100
	s_nop 0
	global_load_lds_dwordx4 v210, s[40:41]
	v_add_u32_e32 v214, s95, v212
	v_add_u32_e32 v215, s95, v213
	ds_read_b128 v[38:41], v215
	ds_read_b128 v[58:61], v214 offset:0
	ds_read_b128 v[62:65], v214 offset:2048
	ds_read_b128 v[66:69], v214 offset:4096
	ds_read_b128 v[70:73], v214 offset:6144
	ds_read_b128 v[74:77], v214 offset:8192
	ds_read_b128 v[100:103], v214 offset:10240
	ds_read_b128 v[104:107], v214 offset:12288
	ds_read_b128 v[108:111], v214 offset:14336
	ds_read_b128 v[112:115], v214 offset:16384
	ds_read_b128 v[116:119], v214 offset:18432
	v_mfma_f32_16x16x32_bf16 v[18:21], v[158:161], v[230:233], v[18:21]
	v_mfma_f32_16x16x32_bf16 v[22:25], v[158:161], v[234:237], v[22:25]
	s_waitcnt lgkmcnt(10)
; __device__ __forceinline__ unsigned f2bf(float f) { unsigned u = __builtin_bit_cast(unsigned, f); return (u + 0x7fffu + ((u >> 16) & 1u)) >> 16; }
; __device__ __forceinline__ void rt_step(const RtLoad& L, const bf16_t* bh, const bf16_t* bl, f32x4 (&acc)[2][5], float (&ss)[2], int ko) {
;     RtW W;
; #pragma unroll
;     for (int n = 0; n < 5; ++n) { W.wh[n] = *(const bf16x8*)(bh + (size_t)n * 16 * D + ko); W.wl[n] = *(const bf16x8*)(bl + (size_t)n * 16 * D + ko); }
;     bf16x8 ahi[2], alo[2];
; #pragma unroll
;     for (int mi = 0; mi < 2; ++mi) { const u32x4 xw = L.x[mi]; const f32x4 xa = (f32x4){bflo(xw.x), bfhi(xw.x), bflo(xw.y), bfhi(xw.y)}, xb = (f32x4){bflo(xw.z), bfhi(xw.z), bflo(xw.w), bfhi(xw.w)};
;         ss[mi] += (xa.x * xa.x + xa.y * xa.y) + (xa.z * xa.z + xa.w * xa.w) + (xb.x * xb.x + xb.y * xb.y) + (xb.z * xb.z + xb.w * xb.w);
;         const float u[8] = {xa.x * L.g[0].x, xa.y * L.g[0].y, xa.z * L.g[0].z, xa.w * L.g[0].w, xb.x * L.g[1].x, xb.y * L.g[1].y, xb.z * L.g[1].z, xb.w * L.g[1].w};
;         unsigned hb[8]; float lo[8];
; #pragma unroll
;         for (int j = 0; j < 8; ++j) { hb[j] = f2bf(u[j]); lo[j] = u[j] - __builtin_bit_cast(float, hb[j] << 16); }
;         const u32x4 hw = (u32x4){hb[0] | (hb[1] << 16), hb[2] | (hb[3] << 16), hb[4] | (hb[5] << 16), hb[6] | (hb[7] << 16)};
;         const u32x4 lw = (u32x4){pk2(lo[0], lo[1]), pk2(lo[2], lo[3]), pk2(lo[4], lo[5]), pk2(lo[6], lo[7])};
;         ahi[mi] = __builtin_bit_cast(bf16x8, hw); alo[mi] = __builtin_bit_cast(bf16x8, lw); }
; #pragma unroll
;     for (int n = 0; n < 5; ++n)
; #pragma unroll
;         for (int mi = 0; mi < 2; ++mi) { acc[mi][n] = __builtin_amdgcn_mfma_f32_16x16x32_bf16(ahi[mi], W.wh[n], acc[mi][n], 0, 0, 0);
;             acc[mi][n] = __builtin_amdgcn_mfma_f32_16x16x32_bf16(alo[mi], W.wh[n], acc[mi][n], 0, 0, 0);
;             acc[mi][n] = __builtin_amdgcn_mfma_f32_16x16x32_bf16(ahi[mi], W.wl[n], acc[mi][n], 0, 0, 0); }
; __device__ __forceinline__ void p5_router(Frame& F) {
;     ...
;           RtLoad La, Lb; rt_load(La, h0, h1, gp, 0);
; #pragma unroll 1
;           for (int ks = 0; ks < 32; ks += 2) {
;               rt_load(Lb, h0, h1, gp, (ks + 1) * 32); rt_step(La, bh, bl, acc, ss, ks * 32);
;               if (ks + 2 < 32) rt_load(La, h0, h1, gp, (ks + 2) * 32);
;               rt_step(Lb, bh, bl, acc, ss, (ks + 1) * 32); }
	v_lshlrev_b32_e32 v172, 16, v38
	v_and_b32_e32 v173, 0xffff0000, v38
	v_lshlrev_b32_e32 v174, 16, v39
	v_and_b32_e32 v175, 0xffff0000, v39
	v_mfma_f32_16x16x32_bf16 v[26:29], v[158:161], v[238:241], v[26:29]
	v_lshlrev_b32_e32 v176, 16, v40
	v_and_b32_e32 v177, 0xffff0000, v40
	v_lshlrev_b32_e32 v178, 16, v41
	v_and_b32_e32 v179, 0xffff0000, v41
	v_mfma_f32_16x16x32_bf16 v[30:33], v[158:161], v[242:245], v[30:33]
	v_mul_f32_e32 v180, v42, v172
	v_mul_f32_e32 v181, v43, v173
	v_mul_f32_e32 v182, v44, v174
	v_mul_f32_e32 v183, v45, v175
	v_mfma_f32_16x16x32_bf16 v[34:37], v[158:161], v[246:249], v[34:37]
	v_mul_f32_e32 v184, v46, v176
	v_mul_f32_e32 v185, v47, v177
	v_mul_f32_e32 v186, v48, v178
	v_mul_f32_e32 v187, v49, v179
	v_mfma_f32_16x16x32_bf16 v[18:21], v[162:165], v[230:233], v[18:21]
	v_cvt_pk_bf16_f32 v200, v180, v181
	v_cvt_pk_bf16_f32 v201, v182, v183
	v_cvt_pk_bf16_f32 v202, v184, v185
	v_cvt_pk_bf16_f32 v203, v186, v187
	v_mfma_f32_16x16x32_bf16 v[22:25], v[162:165], v[234:237], v[22:25]
	v_mul_f32_e32 v196, v172, v172
	v_mul_f32_e32 v197, v174, v174
	v_mul_f32_e32 v198, v176, v176
	v_mul_f32_e32 v199, v178, v178
	v_mfma_f32_16x16x32_bf16 v[26:29], v[162:165], v[238:241], v[26:29]
	v_fma_f32 v196, v173, v173, v196
	v_fma_f32 v197, v175, v175, v197
	v_fma_f32 v198, v177, v177, v198
	v_fma_f32 v199, v179, v179, v199
	v_mfma_f32_16x16x32_bf16 v[30:33], v[162:165], v[242:245], v[30:33]
	v_lshlrev_b32_e32 v188, 16, v200
	v_and_b32_e32 v189, 0xffff0000, v200
	v_lshlrev_b32_e32 v190, 16, v201
	v_and_b32_e32 v191, 0xffff0000, v201
	v_mfma_f32_16x16x32_bf16 v[34:37], v[162:165], v[246:249], v[34:37]
	v_lshlrev_b32_e32 v192, 16, v202
	v_and_b32_e32 v193, 0xffff0000, v202
	v_lshlrev_b32_e32 v194, 16, v203
	v_and_b32_e32 v195, 0xffff0000, v203
	v_mfma_f32_16x16x32_bf16 v[18:21], v[158:161], v[120:123], v[18:21]
	v_fma_f32 v180, v42, v172, -v188
	v_fma_f32 v181, v43, v173, -v189
	v_fma_f32 v182, v44, v174, -v190
	v_fma_f32 v183, v45, v175, -v191
	v_mfma_f32_16x16x32_bf16 v[22:25], v[158:161], v[124:127], v[22:25]
	v_fma_f32 v184, v46, v176, -v192
	v_fma_f32 v185, v47, v177, -v193
	v_fma_f32 v186, v48, v178, -v194
	v_fma_f32 v187, v49, v179, -v195
	v_mfma_f32_16x16x32_bf16 v[26:29], v[158:161], v[132:135], v[26:29]
	v_add_f32_e32 v196, v196, v197
	v_add_f32_e32 v196, v196, v198
	v_add_f32_e32 v196, v196, v199
	v_add_f32_e32 v224, v224, v196
	v_mfma_f32_16x16x32_bf16 v[30:33], v[158:161], v[136:139], v[30:33]
	v_cvt_pk_bf16_f32 v204, v180, v181
	v_cvt_pk_bf16_f32 v205, v182, v183
	v_cvt_pk_bf16_f32 v206, v184, v185
	v_cvt_pk_bf16_f32 v207, v186, v187
	v_mfma_f32_16x16x32_bf16 v[34:37], v[158:161], v[140:143], v[34:37]
	s_waitcnt vmcnt(10)
	s_waitcnt lgkmcnt(0)
	s_barrier
	s_mov_b32 s33, s94
	s_mov_b32 s94, s95
	s_mov_b32 s95, s91
	s_mov_b32 s91, s25
	s_mov_b32 s25, s33
	v_add_u32_e32 v214, s95, v212
	v_add_u32_e32 v215, s95, v213
	ds_read_b128 v[226:229], v215
	ds_read_b128 v[230:233], v214 offset:0
	ds_read_b128 v[234:237], v214 offset:2048
	ds_read_b128 v[238:241], v214 offset:4096
	ds_read_b128 v[242:245], v214 offset:6144
	ds_read_b128 v[246:249], v214 offset:8192
	ds_read_b128 v[120:123], v214 offset:10240
	ds_read_b128 v[124:127], v214 offset:12288
	ds_read_b128 v[132:135], v214 offset:14336
	ds_read_b128 v[136:139], v214 offset:16384
	ds_read_b128 v[140:143], v214 offset:18432
	v_mfma_f32_16x16x32_bf16 v[18:21], v[200:203], v[58:61], v[18:21]
	v_mfma_f32_16x16x32_bf16 v[22:25], v[200:203], v[62:65], v[22:25]
	s_waitcnt lgkmcnt(10)
	v_lshlrev_b32_e32 v172, 16, v226
	v_and_b32_e32 v173, 0xffff0000, v226
	v_lshlrev_b32_e32 v174, 16, v227
	v_and_b32_e32 v175, 0xffff0000, v227
	v_mfma_f32_16x16x32_bf16 v[26:29], v[200:203], v[66:69], v[26:29]
	v_lshlrev_b32_e32 v176, 16, v228
	v_and_b32_e32 v177, 0xffff0000, v228
	v_lshlrev_b32_e32 v178, 16, v229
	v_and_b32_e32 v179, 0xffff0000, v229
	v_mfma_f32_16x16x32_bf16 v[30:33], v[200:203], v[70:73], v[30:33]
	v_mul_f32_e32 v180, v50, v172
	v_mul_f32_e32 v181, v51, v173
	v_mul_f32_e32 v182, v52, v174
	v_mul_f32_e32 v183, v53, v175
	v_mfma_f32_16x16x32_bf16 v[34:37], v[200:203], v[74:77], v[34:37]
	v_mul_f32_e32 v184, v54, v176
	v_mul_f32_e32 v185, v55, v177
	v_mul_f32_e32 v186, v56, v178
	v_mul_f32_e32 v187, v57, v179
	v_mfma_f32_16x16x32_bf16 v[18:21], v[204:207], v[58:61], v[18:21]
	v_cvt_pk_bf16_f32 v158, v180, v181
	v_cvt_pk_bf16_f32 v159, v182, v183
	v_cvt_pk_bf16_f32 v160, v184, v185
	v_cvt_pk_bf16_f32 v161, v186, v187
	v_mfma_f32_16x16x32_bf16 v[22:25], v[204:207], v[62:65], v[22:25]
	v_mul_f32_e32 v196, v172, v172
	v_mul_f32_e32 v197, v174, v174
	v_mul_f32_e32 v198, v176, v176
	v_mul_f32_e32 v199, v178, v178
	v_mfma_f32_16x16x32_bf16 v[26:29], v[204:207], v[66:69], v[26:29]
	v_fma_f32 v196, v173, v173, v196
	v_fma_f32 v197, v175, v175, v197
	v_fma_f32 v198, v177, v177, v198
	v_fma_f32 v199, v179, v179, v199
	v_mfma_f32_16x16x32_bf16 v[30:33], v[204:207], v[70:73], v[30:33]
	v_lshlrev_b32_e32 v188, 16, v158
	v_and_b32_e32 v189, 0xffff0000, v158
	v_lshlrev_b32_e32 v190, 16, v159
	v_and_b32_e32 v191, 0xffff0000, v159
	v_mfma_f32_16x16x32_bf16 v[34:37], v[204:207], v[74:77], v[34:37]
	v_lshlrev_b32_e32 v192, 16, v160
	v_and_b32_e32 v193, 0xffff0000, v160
	v_lshlrev_b32_e32 v194, 16, v161
	v_and_b32_e32 v195, 0xffff0000, v161
	v_mfma_f32_16x16x32_bf16 v[18:21], v[200:203], v[100:103], v[18:21]
	v_fma_f32 v180, v50, v172, -v188
	v_fma_f32 v181, v51, v173, -v189
	v_fma_f32 v182, v52, v174, -v190
	v_fma_f32 v183, v53, v175, -v191
	v_mfma_f32_16x16x32_bf16 v[22:25], v[200:203], v[104:107], v[22:25]
	v_fma_f32 v184, v54, v176, -v192
	v_fma_f32 v185, v55, v177, -v193
	v_fma_f32 v186, v56, v178, -v194
	v_fma_f32 v187, v57, v179, -v195
	v_mfma_f32_16x16x32_bf16 v[26:29], v[200:203], v[108:111], v[26:29]
	v_add_f32_e32 v196, v196, v197
	v_add_f32_e32 v196, v196, v198
	v_add_f32_e32 v196, v196, v199
	v_add_f32_e32 v224, v224, v196
	v_mfma_f32_16x16x32_bf16 v[30:33], v[200:203], v[112:115], v[30:33]
	v_cvt_pk_bf16_f32 v162, v180, v181
	v_cvt_pk_bf16_f32 v163, v182, v183
	v_cvt_pk_bf16_f32 v164, v184, v185
	v_cvt_pk_bf16_f32 v165, v186, v187
	v_mfma_f32_16x16x32_bf16 v[34:37], v[200:203], v[116:119], v[34:37]
	s_waitcnt vmcnt(5)
	s_waitcnt lgkmcnt(0)
	s_barrier
; __device__ __forceinline__ unsigned f2bf(float f) { unsigned u = __builtin_bit_cast(unsigned, f); return (u + 0x7fffu + ((u >> 16) & 1u)) >> 16; }
; __device__ __forceinline__ void rt_step(const RtLoad& L, const bf16_t* bh, const bf16_t* bl, f32x4 (&acc)[2][5], float (&ss)[2], int ko) {
;     RtW W;
; #pragma unroll
;     for (int n = 0; n < 5; ++n) { W.wh[n] = *(const bf16x8*)(bh + (size_t)n * 16 * D + ko); W.wl[n] = *(const bf16x8*)(bl + (size_t)n * 16 * D + ko); }
;     bf16x8 ahi[2], alo[2];
; #pragma unroll
;     for (int mi = 0; mi < 2; ++mi) { const u32x4 xw = L.x[mi]; const f32x4 xa = (f32x4){bflo(xw.x), bfhi(xw.x), bflo(xw.y), bfhi(xw.y)}, xb = (f32x4){bflo(xw.z), bfhi(xw.z), bflo(xw.w), bfhi(xw.w)};
;         ss[mi] += (xa.x * xa.x + xa.y * xa.y) + (xa.z * xa.z + xa.w * xa.w) + (xb.x * xb.x + xb.y * xb.y) + (xb.z * xb.z + xb.w * xb.w);
;         const float u[8] = {xa.x * L.g[0].x, xa.y * L.g[0].y, xa.z * L.g[0].z, xa.w * L.g[0].w, xb.x * L.g[1].x, xb.y * L.g[1].y, xb.z * L.g[1].z, xb.w * L.g[1].w};
;         unsigned hb[8]; float lo[8];
; #pragma unroll
;         for (int j = 0; j < 8; ++j) { hb[j] = f2bf(u[j]); lo[j] = u[j] - __builtin_bit_cast(float, hb[j] << 16); }
;         const u32x4 hw = (u32x4){hb[0] | (hb[1] << 16), hb[2] | (hb[3] << 16), hb[4] | (hb[5] << 16), hb[6] | (hb[7] << 16)};
;         const u32x4 lw = (u32x4){pk2(lo[0], lo[1]), pk2(lo[2], lo[3]), pk2(lo[4], lo[5]), pk2(lo[6], lo[7])};
;         ahi[mi] = __builtin_bit_cast(bf16x8, hw); alo[mi] = __builtin_bit_cast(bf16x8, lw); }
; #pragma unroll
;     for (int n = 0; n < 5; ++n)
; #pragma unroll
;         for (int mi = 0; mi < 2; ++mi) { acc[mi][n] = __builtin_amdgcn_mfma_f32_16x16x32_bf16(ahi[mi], W.wh[n], acc[mi][n], 0, 0, 0);
;             acc[mi][n] = __builtin_amdgcn_mfma_f32_16x16x32_bf16(alo[mi], W.wh[n], acc[mi][n], 0, 0, 0);
;             acc[mi][n] = __builtin_amdgcn_mfma_f32_16x16x32_bf16(ahi[mi], W.wl[n], acc[mi][n], 0, 0, 0); }
; __device__ __forceinline__ void p5_router(Frame& F) {
;     ...
;           RtLoad La, Lb; rt_load(La, h0, h1, gp, 0);
; #pragma unroll 1
;           for (int ks = 0; ks < 32; ks += 2) {
;               rt_load(Lb, h0, h1, gp, (ks + 1) * 32); rt_step(La, bh, bl, acc, ss, ks * 32);
;               if (ks + 2 < 32) rt_load(La, h0, h1, gp, (ks + 2) * 32);
;               rt_step(Lb, bh, bl, acc, ss, (ks + 1) * 32); }
	s_mov_b32 s33, s94
	s_mov_b32 s94, s95
	s_mov_b32 s95, s91
	s_mov_b32 s91, s25
	s_mov_b32 s25, s33
	v_add_u32_e32 v214, s95, v212
	v_add_u32_e32 v215, s95, v213
	ds_read_b128 v[38:41], v215
	ds_read_b128 v[58:61], v214 offset:0
	ds_read_b128 v[62:65], v214 offset:2048
	ds_read_b128 v[66:69], v214 offset:4096
	ds_read_b128 v[70:73], v214 offset:6144
	ds_read_b128 v[74:77], v214 offset:8192
	ds_read_b128 v[100:103], v214 offset:10240
	ds_read_b128 v[104:107], v214 offset:12288
	ds_read_b128 v[108:111], v214 offset:14336
	ds_read_b128 v[112:115], v214 offset:16384
	ds_read_b128 v[116:119], v214 offset:18432
	v_mfma_f32_16x16x32_bf16 v[18:21], v[158:161], v[230:233], v[18:21]
	v_mfma_f32_16x16x32_bf16 v[22:25], v[158:161], v[234:237], v[22:25]
	s_waitcnt lgkmcnt(10)
	v_lshlrev_b32_e32 v172, 16, v38
	v_and_b32_e32 v173, 0xffff0000, v38
	v_lshlrev_b32_e32 v174, 16, v39
	v_and_b32_e32 v175, 0xffff0000, v39
	v_mfma_f32_16x16x32_bf16 v[26:29], v[158:161], v[238:241], v[26:29]
	v_lshlrev_b32_e32 v176, 16, v40
	v_and_b32_e32 v177, 0xffff0000, v40
	v_lshlrev_b32_e32 v178, 16, v41
	v_and_b32_e32 v179, 0xffff0000, v41
	v_mfma_f32_16x16x32_bf16 v[30:33], v[158:161], v[242:245], v[30:33]
	v_mul_f32_e32 v180, v2, v172
	v_mul_f32_e32 v181, v3, v173
	v_mul_f32_e32 v182, v4, v174
	v_mul_f32_e32 v183, v5, v175
	v_mfma_f32_16x16x32_bf16 v[34:37], v[158:161], v[246:249], v[34:37]
	v_mul_f32_e32 v184, v6, v176
	v_mul_f32_e32 v185, v7, v177
	v_mul_f32_e32 v186, v8, v178
	v_mul_f32_e32 v187, v9, v179
	v_mfma_f32_16x16x32_bf16 v[18:21], v[162:165], v[230:233], v[18:21]
	v_cvt_pk_bf16_f32 v200, v180, v181
	v_cvt_pk_bf16_f32 v201, v182, v183
	v_cvt_pk_bf16_f32 v202, v184, v185
	v_cvt_pk_bf16_f32 v203, v186, v187
	v_mfma_f32_16x16x32_bf16 v[22:25], v[162:165], v[234:237], v[22:25]
	v_mul_f32_e32 v196, v172, v172
	v_mul_f32_e32 v197, v174, v174
	v_mul_f32_e32 v198, v176, v176
	v_mul_f32_e32 v199, v178, v178
	v_mfma_f32_16x16x32_bf16 v[26:29], v[162:165], v[238:241], v[26:29]
	v_fma_f32 v196, v173, v173, v196
	v_fma_f32 v197, v175, v175, v197
	v_fma_f32 v198, v177, v177, v198
	v_fma_f32 v199, v179, v179, v199
	v_mfma_f32_16x16x32_bf16 v[30:33], v[162:165], v[242:245], v[30:33]
	v_lshlrev_b32_e32 v188, 16, v200
	v_and_b32_e32 v189, 0xffff0000, v200
	v_lshlrev_b32_e32 v190, 16, v201
	v_and_b32_e32 v191, 0xffff0000, v201
	v_mfma_f32_16x16x32_bf16 v[34:37], v[162:165], v[246:249], v[34:37]
	v_lshlrev_b32_e32 v192, 16, v202
	v_and_b32_e32 v193, 0xffff0000, v202
	v_lshlrev_b32_e32 v194, 16, v203
	v_and_b32_e32 v195, 0xffff0000, v203
	v_mfma_f32_16x16x32_bf16 v[18:21], v[158:161], v[120:123], v[18:21]
	v_fma_f32 v180, v2, v172, -v188
	v_fma_f32 v181, v3, v173, -v189
	v_fma_f32 v182, v4, v174, -v190
	v_fma_f32 v183, v5, v175, -v191
	v_mfma_f32_16x16x32_bf16 v[22:25], v[158:161], v[124:127], v[22:25]
	v_fma_f32 v184, v6, v176, -v192
	v_fma_f32 v185, v7, v177, -v193
	v_fma_f32 v186, v8, v178, -v194
	v_fma_f32 v187, v9, v179, -v195
	v_mfma_f32_16x16x32_bf16 v[26:29], v[158:161], v[132:135], v[26:29]
	v_add_f32_e32 v196, v196, v197
	v_add_f32_e32 v196, v196, v198
	v_add_f32_e32 v196, v196, v199
	v_add_f32_e32 v224, v224, v196
	v_mfma_f32_16x16x32_bf16 v[30:33], v[158:161], v[136:139], v[30:33]
	v_cvt_pk_bf16_f32 v204, v180, v181
	v_cvt_pk_bf16_f32 v205, v182, v183
	v_cvt_pk_bf16_f32 v206, v184, v185
	v_cvt_pk_bf16_f32 v207, v186, v187
	v_mfma_f32_16x16x32_bf16 v[34:37], v[158:161], v[140:143], v[34:37]
	s_waitcnt vmcnt(0)
	s_waitcnt lgkmcnt(0)
	s_barrier
	s_mov_b32 s33, s94
	s_mov_b32 s94, s95
	s_mov_b32 s95, s91
	s_mov_b32 s91, s25
	s_mov_b32 s25, s33
	v_add_u32_e32 v214, s95, v212
	v_add_u32_e32 v215, s95, v213
	ds_read_b128 v[226:229], v215
	ds_read_b128 v[230:233], v214 offset:0
	ds_read_b128 v[234:237], v214 offset:2048
	ds_read_b128 v[238:241], v214 offset:4096
	ds_read_b128 v[242:245], v214 offset:6144
	ds_read_b128 v[246:249], v214 offset:8192
	ds_read_b128 v[120:123], v214 offset:10240
	ds_read_b128 v[124:127], v214 offset:12288
	ds_read_b128 v[132:135], v214 offset:14336
	ds_read_b128 v[136:139], v214 offset:16384
	ds_read_b128 v[140:143], v214 offset:18432
	v_mfma_f32_16x16x32_bf16 v[18:21], v[200:203], v[58:61], v[18:21]
	v_mfma_f32_16x16x32_bf16 v[22:25], v[200:203], v[62:65], v[22:25]
	s_waitcnt lgkmcnt(10)
	v_lshlrev_b32_e32 v172, 16, v226
	v_and_b32_e32 v173, 0xffff0000, v226
	v_lshlrev_b32_e32 v174, 16, v227
	v_and_b32_e32 v175, 0xffff0000, v227
	v_mfma_f32_16x16x32_bf16 v[26:29], v[200:203], v[66:69], v[26:29]
	v_lshlrev_b32_e32 v176, 16, v228
	v_and_b32_e32 v177, 0xffff0000, v228
	v_lshlrev_b32_e32 v178, 16, v229
	v_and_b32_e32 v179, 0xffff0000, v229
	v_mfma_f32_16x16x32_bf16 v[30:33], v[200:203], v[70:73], v[30:33]
	v_mul_f32_e32 v180, v10, v172
	v_mul_f32_e32 v181, v11, v173
	v_mul_f32_e32 v182, v12, v174
	v_mul_f32_e32 v183, v13, v175
	v_mfma_f32_16x16x32_bf16 v[34:37], v[200:203], v[74:77], v[34:37]
	v_mul_f32_e32 v184, v14, v176
	v_mul_f32_e32 v185, v15, v177
	v_mul_f32_e32 v186, v16, v178
	v_mul_f32_e32 v187, v17, v179
	v_mfma_f32_16x16x32_bf16 v[18:21], v[204:207], v[58:61], v[18:21]
	v_cvt_pk_bf16_f32 v158, v180, v181
	v_cvt_pk_bf16_f32 v159, v182, v183
	v_cvt_pk_bf16_f32 v160, v184, v185
	v_cvt_pk_bf16_f32 v161, v186, v187
	v_mfma_f32_16x16x32_bf16 v[22:25], v[204:207], v[62:65], v[22:25]
	v_mul_f32_e32 v196, v172, v172
	v_mul_f32_e32 v197, v174, v174
	v_mul_f32_e32 v198, v176, v176
	v_mul_f32_e32 v199, v178, v178
	v_mfma_f32_16x16x32_bf16 v[26:29], v[204:207], v[66:69], v[26:29]
	v_fma_f32 v196, v173, v173, v196
	v_fma_f32 v197, v175, v175, v197
	v_fma_f32 v198, v177, v177, v198
	v_fma_f32 v199, v179, v179, v199
	v_mfma_f32_16x16x32_bf16 v[30:33], v[204:207], v[70:73], v[30:33]
	v_lshlrev_b32_e32 v188, 16, v158
	v_and_b32_e32 v189, 0xffff0000, v158
	v_lshlrev_b32_e32 v190, 16, v159
	v_and_b32_e32 v191, 0xffff0000, v159
	v_mfma_f32_16x16x32_bf16 v[34:37], v[204:207], v[74:77], v[34:37]
	v_lshlrev_b32_e32 v192, 16, v160
	v_and_b32_e32 v193, 0xffff0000, v160
	v_lshlrev_b32_e32 v194, 16, v161
	v_and_b32_e32 v195, 0xffff0000, v161
	v_mfma_f32_16x16x32_bf16 v[18:21], v[200:203], v[100:103], v[18:21]
	v_fma_f32 v180, v10, v172, -v188
	v_fma_f32 v181, v11, v173, -v189
	v_fma_f32 v182, v12, v174, -v190
	v_fma_f32 v183, v13, v175, -v191
	v_mfma_f32_16x16x32_bf16 v[22:25], v[200:203], v[104:107], v[22:25]
	v_fma_f32 v184, v14, v176, -v192
	v_fma_f32 v185, v15, v177, -v193
	v_fma_f32 v186, v16, v178, -v194
	v_fma_f32 v187, v17, v179, -v195
	v_mfma_f32_16x16x32_bf16 v[26:29], v[200:203], v[108:111], v[26:29]
	v_add_f32_e32 v196, v196, v197
	v_add_f32_e32 v196, v196, v198
	v_add_f32_e32 v196, v196, v199
	v_add_f32_e32 v224, v224, v196
	v_mfma_f32_16x16x32_bf16 v[30:33], v[200:203], v[112:115], v[30:33]
	v_cvt_pk_bf16_f32 v162, v180, v181
	v_cvt_pk_bf16_f32 v163, v182, v183
	v_cvt_pk_bf16_f32 v164, v184, v185
	v_cvt_pk_bf16_f32 v165, v186, v187
	v_mfma_f32_16x16x32_bf16 v[34:37], v[200:203], v[116:119], v[34:37]
	s_waitcnt lgkmcnt(0)
	s_barrier
; __device__ __forceinline__ void rt_step(const RtLoad& L, const bf16_t* bh, const bf16_t* bl, f32x4 (&acc)[2][5], float (&ss)[2], int ko) {
;     ...
;         for (int mi = 0; mi < 2; ++mi) { acc[mi][n] = __builtin_amdgcn_mfma_f32_16x16x32_bf16(ahi[mi], W.wh[n], acc[mi][n], 0, 0, 0);
;             acc[mi][n] = __builtin_amdgcn_mfma_f32_16x16x32_bf16(alo[mi], W.wh[n], acc[mi][n], 0, 0, 0);
;             acc[mi][n] = __builtin_amdgcn_mfma_f32_16x16x32_bf16(ahi[mi], W.wl[n], acc[mi][n], 0, 0, 0); }
; __device__ __forceinline__ void p5_router(Frame& F) {
;     ...
;           for (int mi = 0; mi < 2; ++mi) { float s = ss[mi]; s += __shfl_xor(s, 16); s += __shfl_xor(s, 32); if (fq == 0) ssp[kq * 64 + 32 * tg + 16 * mi + fr] = s;
; #pragma unroll
;               for (int n = 0; n < 5; ++n)
; #pragma unroll
;                   for (int i = 0; i < 4; ++i) part[(kq * 64 + 32 * tg + 16 * mi + 4 * fq + i) * 80 + 16 * n + fr] = acc[mi][n][i]; } }
;         __syncthreads();
;         if (F.tid < 64) { const float s = (ssp[F.tid] + ssp[64 + F.tid]) + (ssp[128 + F.tid] + ssp[192 + F.tid]); const float r = 1.0f / sqrtf(s * (1.f / D) + RMS_EPS); rs[F.tid] = r; }
	s_mov_b32 s33, s94
	s_mov_b32 s94, s95
	s_mov_b32 s95, s91
	s_mov_b32 s91, s25
	s_mov_b32 s25, s33
	v_mfma_f32_16x16x32_bf16 v[18:21], v[158:161], v[230:233], v[18:21]
	v_mfma_f32_16x16x32_bf16 v[22:25], v[158:161], v[234:237], v[22:25]
	v_mfma_f32_16x16x32_bf16 v[26:29], v[158:161], v[238:241], v[26:29]
	v_mfma_f32_16x16x32_bf16 v[30:33], v[158:161], v[242:245], v[30:33]
	v_mfma_f32_16x16x32_bf16 v[34:37], v[158:161], v[246:249], v[34:37]
	v_mfma_f32_16x16x32_bf16 v[18:21], v[162:165], v[230:233], v[18:21]
	v_mfma_f32_16x16x32_bf16 v[22:25], v[162:165], v[234:237], v[22:25]
	v_mfma_f32_16x16x32_bf16 v[26:29], v[162:165], v[238:241], v[26:29]
	v_mfma_f32_16x16x32_bf16 v[30:33], v[162:165], v[242:245], v[30:33]
	v_mfma_f32_16x16x32_bf16 v[34:37], v[162:165], v[246:249], v[34:37]
	v_mfma_f32_16x16x32_bf16 v[18:21], v[158:161], v[120:123], v[18:21]
	v_mfma_f32_16x16x32_bf16 v[22:25], v[158:161], v[124:127], v[22:25]
	v_mfma_f32_16x16x32_bf16 v[26:29], v[158:161], v[132:135], v[26:29]
	v_mfma_f32_16x16x32_bf16 v[30:33], v[158:161], v[136:139], v[30:33]
	v_mfma_f32_16x16x32_bf16 v[34:37], v[158:161], v[140:143], v[34:37]
.Lrt_out:
	s_nop 7
	s_nop 7
	s_lshl_b32 s24, s89, 6
	s_lshl_b32 s33, s88, 4
	s_add_i32 s24, s24, s33
	s_mul_i32 s33, s24, 320
	v_mul_u32_u24_e32 v217, 0x500, v171
	v_lshl_add_u32 v217, v170, 2, v217
	v_add_u32_e32 v217, s33, v217
	ds_write_b32 v217, v18 offset:0
	ds_write_b32 v217, v19 offset:320
	ds_write_b32 v217, v20 offset:640
	ds_write_b32 v217, v21 offset:960
	ds_write_b32 v217, v22 offset:64
	ds_write_b32 v217, v23 offset:384
	ds_write_b32 v217, v24 offset:704
	ds_write_b32 v217, v25 offset:1024
	ds_write_b32 v217, v26 offset:128
	ds_write_b32 v217, v27 offset:448
	ds_write_b32 v217, v28 offset:768
	ds_write_b32 v217, v29 offset:1088
	ds_write_b32 v217, v30 offset:192
	ds_write_b32 v217, v31 offset:512
	ds_write_b32 v217, v32 offset:832
	ds_write_b32 v217, v33 offset:1152
	ds_write_b32 v217, v34 offset:256
	ds_write_b32 v217, v35 offset:576
	ds_write_b32 v217, v36 offset:896
	ds_write_b32 v217, v37 offset:1216
	v_mov_b32_e32 v218, 0
	v_mov_b32_e32 v219, 0
	v_mov_b32_e32 v220, 0
	v_mov_b32_e32 v221, 0
	v_lshlrev_b32_e32 v222, 4, v0
	v_add_u32_e32 v222, 0xa000, v222
	ds_write_b128 v222, v[218:221] offset:0
	ds_write_b128 v222, v[218:221] offset:8192
	ds_write_b128 v222, v[218:221] offset:16384
	ds_write_b128 v222, v[218:221] offset:24576
	ds_write_b128 v222, v[218:221] offset:32768
	ds_bpermute_b32 v223, v144, v224
	s_waitcnt lgkmcnt(0)
	v_add_f32_e32 v223, v224, v223
	ds_bpermute_b32 v222, v145, v223
	s_lshl_b32 s24, s24, 2
	s_add_i32 s24, s24, 0x19000
	v_lshl_add_u32 v217, v170, 2, s24
	s_waitcnt lgkmcnt(0)
	v_add_f32_e32 v223, v223, v222
	s_and_saveexec_b64 s[98:99], s[6:7]
	ds_write_b32 v217, v223
	s_or_b64 exec, exec, s[98:99]
	v_cmp_gt_u32_e32 vcc, 0x80, v0
	v_lshlrev_b32_e32 v222, 2, v0
	v_add_u32_e32 v222, 0x19200, v222
	s_and_saveexec_b64 s[98:99], vcc
	ds_write_b32 v222, v218
	s_or_b64 exec, exec, s[98:99]
	s_waitcnt lgkmcnt(0)
	s_barrier
	s_and_saveexec_b64 s[8:9], s[4:5]
	s_cbranch_execz .LBB0_616
	ds_read2st64_b32 v[2:3], v147 offset1:1
	ds_read2st64_b32 v[4:5], v147 offset0:2 offset1:3
	s_waitcnt lgkmcnt(1)
	v_mov_b32_e32 v6, v2
	s_waitcnt lgkmcnt(0)
	v_mov_b32_e32 v7, v4
	v_mov_b32_e32 v4, v3
	v_pk_add_f32 v[2:3], v[6:7], v[4:5]
	s_nop 0
	v_add_f32_e32 v2, v2, v3
	v_fmamk_f32 v2, v2, 0x39800000, v151
	v_mul_f32_e32 v3, 0x4f800000, v2
	v_cmp_gt_f32_e32 vcc, s57, v2
	s_nop 1
	v_cndmask_b32_e32 v2, v2, v3, vcc
	v_sqrt_f32_e32 v3, v2
	s_nop 0
	v_add_u32_e32 v4, -1, v3
	v_add_u32_e32 v5, 1, v3
	v_fma_f32 v6, -v4, v3, v2
	v_fma_f32 v7, -v5, v3, v2
	v_cmp_ge_f32_e64 s[0:1], 0, v6
	s_nop 1
	v_cndmask_b32_e64 v3, v3, v4, s[0:1]
	v_cmp_lt_f32_e64 s[0:1], 0, v7
	s_nop 1
	v_cndmask_b32_e64 v3, v3, v5, s[0:1]
	v_mul_f32_e32 v4, 0x37800000, v3
	v_cndmask_b32_e32 v3, v3, v4, vcc
	v_cmp_class_f32_e32 vcc, v2, v152
	s_nop 1
	v_cndmask_b32_e32 v2, v3, v2, vcc
	v_div_scale_f32 v3, s[0:1], v2, v2, 1.0
	v_rcp_f32_e32 v4, v3
	s_nop 0
	v_fma_f32 v5, -v3, v4, 1.0
	v_fmac_f32_e32 v4, v5, v4
	v_div_scale_f32 v5, vcc, 1.0, v2, 1.0
	v_mul_f32_e32 v6, v5, v4
	v_fma_f32 v7, -v3, v6, v5
	v_fmac_f32_e32 v6, v7, v4
	v_fma_f32 v3, -v3, v6, v5
	v_div_fmas_f32 v3, v3, v4, v6
	v_div_fixup_f32 v2, v3, v2, 1.0
	ds_write_b32 v148, v2
